# P1: row scales of every unit requested at the top of the unit (free VGPRs), epilogues no longer load them and wait
# baseline (speedup 1.0000x reference)
; template <class Epi, class Sched, bool ALIGN_EPI = false, bool SP2 = false>
; __device__ __forceinline__ void gemm_phase(PG8_LAS unsigned char* lds, const Gemm g, const Sched& S, const Epi& E) {
;     ...
;         const bool has_next = S.next(ui + 1, nxt);
;         const char* nA = has_next ? (const char*)g.A + (size_t)nxt.pm * tstep : cA; const char* nB = has_next ? (const char*)g.Bt + (size_t)nxt.pn * tstep : cB;
;     ...
;         for (int a = 0; a < 2; ++a)
; #pragma unroll
;             for (int b = 0; b < 2; ++b)
; #pragma unroll
;                 for (int m = 0; m < 4; ++m)
; #pragma unroll
;                     for (int n = 0; n < 2; ++n) acc[a][b][m][n] = (f32x4){0.f, 0.f, 0.f, 0.f};
;         cur = nxt; cA = nA; cB = nB; ++ui;
.LBB0_152:
	s_ashr_i32 s41, s40, 31
	s_lshl_b64 s[42:43], s[40:41], 21
	s_add_u32 s42, s54, s42
	s_addc_u32 s43, s55, s43
	s_and_b64 s[44:45], s[10:11], exec
	s_cselect_b32 s41, s43, s13
	s_cselect_b32 s50, s42, s12
	s_ashr_i32 s39, s38, 31
	s_lshl_b64 s[44:45], s[38:39], 21
	s_add_u32 s44, s56, s44
	s_addc_u32 s45, s57, s45
	s_and_b64 s[48:49], s[10:11], exec
	s_cselect_b32 s39, s45, s47
	s_cselect_b32 s51, s44, s46
	s_add_u32 s12, s12, 0x100080
	s_addc_u32 s13, s13, 0
	s_add_u32 s52, s46, 0x100
	v_mov_b32_e32 v4, 0
	s_addc_u32 s53, s47, 0
	v_lshl_add_u32 v146, s2, 8, v1
	v_ashrrev_i32_e32 v147, 31, v146
	v_lshl_add_u64 v[146:147], v[146:147], 2, s[22:23]
	global_load_dword v218, v[146:147], off
	global_load_dword v220, v[146:147], off offset:64
	global_load_dword v224, v[146:147], off offset:128
	global_load_dword v226, v[146:147], off offset:192
	global_load_dword v228, v[146:147], off offset:512
	global_load_dword v230, v[146:147], off offset:576
	global_load_dword v240, v[146:147], off offset:640
	global_load_dword v250, v[146:147], off offset:704
	s_mov_b32 s80, -2
	v_mov_b32_e32 v5, v4
	v_mov_b32_e32 v6, v4
	v_mov_b32_e32 v7, v4
	v_mov_b32_e32 v8, v4
	v_mov_b32_e32 v9, v4
	v_mov_b32_e32 v10, v4
	v_mov_b32_e32 v11, v4
	v_mov_b32_e32 v20, v4
	v_mov_b32_e32 v21, v4
	v_mov_b32_e32 v22, v4
	v_mov_b32_e32 v23, v4
	v_mov_b32_e32 v24, v4
	v_mov_b32_e32 v25, v4
	v_mov_b32_e32 v26, v4
	v_mov_b32_e32 v27, v4
	v_mov_b32_e32 v36, v4
	v_mov_b32_e32 v37, v4
	v_mov_b32_e32 v38, v4
	v_mov_b32_e32 v39, v4
	v_mov_b32_e32 v40, v4
	v_mov_b32_e32 v41, v4
	v_mov_b32_e32 v42, v4
	v_mov_b32_e32 v43, v4
	v_mov_b32_e32 v52, v4
	v_mov_b32_e32 v53, v4
	v_mov_b32_e32 v54, v4
	v_mov_b32_e32 v55, v4
	v_mov_b32_e32 v56, v4
	v_mov_b32_e32 v57, v4
	v_mov_b32_e32 v58, v4
	v_mov_b32_e32 v59, v4
	v_mov_b32_e32 v12, v4
	v_mov_b32_e32 v13, v4
	v_mov_b32_e32 v14, v4
	v_mov_b32_e32 v15, v4
	v_mov_b32_e32 v16, v4
	v_mov_b32_e32 v17, v4
	v_mov_b32_e32 v18, v4
	v_mov_b32_e32 v19, v4
	v_mov_b32_e32 v28, v4
	v_mov_b32_e32 v29, v4
	v_mov_b32_e32 v30, v4
	v_mov_b32_e32 v31, v4
	v_mov_b32_e32 v32, v4
	v_mov_b32_e32 v33, v4
	v_mov_b32_e32 v34, v4
	v_mov_b32_e32 v35, v4
	v_mov_b32_e32 v44, v4
	v_mov_b32_e32 v45, v4
	v_mov_b32_e32 v46, v4
	v_mov_b32_e32 v47, v4
	v_mov_b32_e32 v48, v4
	v_mov_b32_e32 v49, v4
	v_mov_b32_e32 v50, v4
	v_mov_b32_e32 v51, v4
	v_mov_b32_e32 v60, v4
	v_mov_b32_e32 v61, v4
	v_mov_b32_e32 v62, v4
	v_mov_b32_e32 v63, v4
	v_mov_b32_e32 v64, v4
	v_mov_b32_e32 v65, v4
	v_mov_b32_e32 v66, v4
	v_mov_b32_e32 v67, v4
	v_mov_b32_e32 v68, v4
	v_mov_b32_e32 v69, v4
	v_mov_b32_e32 v70, v4
	v_mov_b32_e32 v71, v4
	v_mov_b32_e32 v72, v4
	v_mov_b32_e32 v73, v4
	v_mov_b32_e32 v74, v4
	v_mov_b32_e32 v75, v4
	v_mov_b32_e32 v84, v4
	v_mov_b32_e32 v85, v4
	v_mov_b32_e32 v86, v4
	v_mov_b32_e32 v87, v4
	v_mov_b32_e32 v88, v4
	v_mov_b32_e32 v89, v4
	v_mov_b32_e32 v90, v4
	v_mov_b32_e32 v91, v4
	v_mov_b32_e32 v100, v4
	v_mov_b32_e32 v101, v4
	v_mov_b32_e32 v102, v4
	v_mov_b32_e32 v103, v4
	v_mov_b32_e32 v104, v4
	v_mov_b32_e32 v105, v4
	v_mov_b32_e32 v106, v4
	v_mov_b32_e32 v107, v4
	v_mov_b32_e32 v116, v4
	v_mov_b32_e32 v117, v4
	v_mov_b32_e32 v118, v4
	v_mov_b32_e32 v119, v4
	v_mov_b32_e32 v120, v4
	v_mov_b32_e32 v121, v4
	v_mov_b32_e32 v122, v4
	v_mov_b32_e32 v123, v4
	v_mov_b32_e32 v76, v4
	v_mov_b32_e32 v77, v4
	v_mov_b32_e32 v78, v4
	v_mov_b32_e32 v79, v4
	v_mov_b32_e32 v80, v4
	v_mov_b32_e32 v81, v4
	v_mov_b32_e32 v82, v4
	v_mov_b32_e32 v83, v4
	v_mov_b32_e32 v92, v4
	v_mov_b32_e32 v93, v4
	v_mov_b32_e32 v94, v4
	v_mov_b32_e32 v95, v4
	v_mov_b32_e32 v96, v4
	v_mov_b32_e32 v97, v4
	v_mov_b32_e32 v98, v4
	v_mov_b32_e32 v99, v4
	v_mov_b32_e32 v108, v4
	v_mov_b32_e32 v109, v4
	v_mov_b32_e32 v110, v4
	v_mov_b32_e32 v111, v4
	v_mov_b32_e32 v112, v4
	v_mov_b32_e32 v113, v4
	v_mov_b32_e32 v114, v4
	v_mov_b32_e32 v115, v4
	v_mov_b32_e32 v124, v4
	v_mov_b32_e32 v125, v4
	v_mov_b32_e32 v126, v4
	v_mov_b32_e32 v127, v4
	v_mov_b32_e32 v128, v4
	v_mov_b32_e32 v129, v4
	v_mov_b32_e32 v130, v4
	v_mov_b32_e32 v131, v4

;     template <int ACT, int AUX> __device__ __forceinline__ void run(const f32x4 (&acc)[2][2][4][2], const Unit& uu, int wr, int wc, int fr, int fq) const {
;     ...
;         for (int i = 0; i < 8; ++i) rsv[i] = ss[row0 + (i >> 2) * HALF + (i & 3) * 16];
;         asm volatile("" ::: "memory");
; #pragma unroll
;         for (int i = 0; i < 8; ++i) rsv[i] = __builtin_amdgcn_rsqf(rsv[i] * (1.0f / cfg::DM) + cfg::RMS_EPS);
;     ...
;                 for (int bj = 0; bj < 2; ++bj) { f32x4 v0 = acc[ai][bj][m][0] * rs, v1 = acc[ai][bj][m][1] * rs;
; #pragma unroll
;                     for (int j = 0; j < 4; ++j) { v0[j] = act_f<ACT>(v0[j]); v1[j] = act_f<ACT>(v1[j]); }
;                     if (AUX == 4) {
;                         unsigned q[8];
; #pragma unroll
;                         for (int j = 0; j < 4; ++j) { q[j] = (unsigned)fminf(fmaxf(fmaf(v0[j], 255.0f, 0.5f), 1.0f), 255.0f); q[4 + j] = (unsigned)fminf(fmaxf(fmaf(v1[j], 255.0f, 0.5f), 1.0f), 255.0f); }
;                         u32x2 w8; w8.x = q[0] | (q[1] << 8) | (q[2] << 16) | (q[3] << 24); w8.y = q[4] | (q[5] << 8) | (q[6] << 16) | (q[7] << 24);
;                         __builtin_nontemporal_store(w8, (u32x2*)(g8 + ((size_t)((u.pn - 52) >> 4) * cfg::MT + r) * cfg::DM + ((u.pn - 52) & 15) * BM + wc * 32 + 8 * fq + bj * HALF));
.LBB0_157:
	v_lshl_add_u32 v156, s2, 8, v1
	v_ashrrev_i32_e32 v157, 31, v156
	s_waitcnt lgkmcnt(0)
	v_lshl_add_u64 v[146:147], v[156:157], 2, s[22:23]
	v_mov_b32_e32 v151, v218
	v_mov_b32_e32 v153, v220
	v_mov_b32_e32 v155, v224
	v_mov_b32_e32 v157, v226
	v_mov_b32_e32 v159, v228
	v_mov_b32_e32 v154, v230
	v_mov_b32_e32 v156, v240
	v_mov_b32_e32 v158, v250
	s_lshl_b32 s100, s2, 20
	s_sub_i32 s12, s1, 52
	s_lshr_b32 s2, s12, 4
	s_lshl_b32 s39, s12, 8
	s_lshl_b64 s[12:13], s[2:3], 25
	s_and_b32 s2, s39, 0xf00
	s_add_u32 s12, s63, s12
	s_addc_u32 s13, s64, s13
	s_lshl_b32 s101, s2, 8
	s_add_i32 s100, s100, s101
	s_lshl_b32 s101, s58, 3
	s_add_i32 s100, s100, s101
	s_addk_i32 s100, 0x1000
	s_add_u32 s100, s12, s100
	s_addc_u32 s101, s13, 0
	v_mbcnt_lo_u32_b32 v148, -1, 0
	v_mbcnt_hi_u32_b32 v148, -1, v148
	v_lshlrev_b32_e32 v148, 3, v148
	v_mov_b32_e32 v149, 0
	v_lshl_add_u64 v[148:149], s[100:101], 0, v[148:149]
	s_mov_b32 s39, 0x437f0000
	v_mov_b32_e32 v146, 1.0
	v_mov_b32_e32 v150, 0x437f0000
	v_mov_b32_e32 v152, 0.5
	v_fmamk_f32 v164, v151, 0x39800000, v221
	v_rsq_f32_e32 v164, v164
	v_fmamk_f32 v162, v153, 0x39800000, v221
	v_rsq_f32_e32 v162, v162
	v_mul_f32_e32 v164, 0xbfb8aa3b, v164
	v_mul_f32_e32 v162, 0xbfb8aa3b, v162
	v_pk_mul_f32 v[128:129], v[128:129], v[164:165] op_sel_hi:[1,0]
	v_pk_mul_f32 v[130:131], v[130:131], v[164:165] op_sel_hi:[1,0]
	v_pk_mul_f32 v[124:125], v[124:125], v[164:165] op_sel_hi:[1,0]
	v_pk_mul_f32 v[126:127], v[126:127], v[164:165] op_sel_hi:[1,0]
	v_pk_mul_f32 v[120:121], v[120:121], v[164:165] op_sel_hi:[1,0]
	v_pk_mul_f32 v[122:123], v[122:123], v[164:165] op_sel_hi:[1,0]
	v_pk_mul_f32 v[116:117], v[116:117], v[164:165] op_sel_hi:[1,0]
	v_pk_mul_f32 v[118:119], v[118:119], v[164:165] op_sel_hi:[1,0]
	v_fmamk_f32 v160, v155, 0x39800000, v221
	v_rsq_f32_e32 v160, v160
	v_exp_f32_e32 v128, v128
	v_exp_f32_e32 v129, v129
	v_exp_f32_e32 v130, v130
	v_exp_f32_e32 v131, v131
	v_mul_f32_e32 v160, 0xbfb8aa3b, v160
	v_exp_f32_e32 v124, v124
	v_exp_f32_e32 v125, v125
	v_exp_f32_e32 v126, v126
	v_exp_f32_e32 v127, v127
	v_exp_f32_e32 v120, v120
	v_exp_f32_e32 v121, v121
	v_exp_f32_e32 v122, v122
	v_exp_f32_e32 v123, v123
	v_exp_f32_e32 v116, v116
	v_exp_f32_e32 v117, v117
	v_exp_f32_e32 v118, v118
	v_exp_f32_e32 v119, v119
	v_pk_add_f32 v[128:129], v[128:129], v[146:147] op_sel_hi:[1,0]
	v_pk_add_f32 v[130:131], v[130:131], v[146:147] op_sel_hi:[1,0]
	v_pk_add_f32 v[124:125], v[124:125], v[146:147] op_sel_hi:[1,0]
	v_pk_add_f32 v[126:127], v[126:127], v[146:147] op_sel_hi:[1,0]
	v_pk_add_f32 v[120:121], v[120:121], v[146:147] op_sel_hi:[1,0]
	v_pk_add_f32 v[122:123], v[122:123], v[146:147] op_sel_hi:[1,0]
	v_pk_add_f32 v[116:117], v[116:117], v[146:147] op_sel_hi:[1,0]
	v_pk_add_f32 v[118:119], v[118:119], v[146:147] op_sel_hi:[1,0]
	v_rcp_f32_e32 v128, v128
	v_rcp_f32_e32 v129, v129
	v_rcp_f32_e32 v130, v130
	v_rcp_f32_e32 v131, v131
	v_rcp_f32_e32 v124, v124
	v_rcp_f32_e32 v125, v125
	v_rcp_f32_e32 v126, v126
	v_rcp_f32_e32 v127, v127
	v_rcp_f32_e32 v120, v120
	v_rcp_f32_e32 v121, v121
	v_rcp_f32_e32 v122, v122
	v_rcp_f32_e32 v123, v123
	v_rcp_f32_e32 v116, v116
	v_rcp_f32_e32 v117, v117
	v_rcp_f32_e32 v118, v118
	v_rcp_f32_e32 v119, v119
	v_pk_fma_f32 v[128:129], v[128:129], v[150:151], v[152:153] op_sel_hi:[1,0,0]
	v_pk_fma_f32 v[130:131], v[130:131], v[150:151], v[152:153] op_sel_hi:[1,0,0]
	v_pk_fma_f32 v[124:125], v[124:125], v[150:151], v[152:153] op_sel_hi:[1,0,0]
	v_pk_fma_f32 v[126:127], v[126:127], v[150:151], v[152:153] op_sel_hi:[1,0,0]
	v_pk_fma_f32 v[120:121], v[120:121], v[150:151], v[152:153] op_sel_hi:[1,0,0]
	v_pk_fma_f32 v[122:123], v[122:123], v[150:151], v[152:153] op_sel_hi:[1,0,0]
	v_pk_fma_f32 v[116:117], v[116:117], v[150:151], v[152:153] op_sel_hi:[1,0,0]
	v_pk_fma_f32 v[118:119], v[118:119], v[150:151], v[152:153] op_sel_hi:[1,0,0]
	v_med3_f32 v128, v128, 1.0, v231
	v_med3_f32 v129, v129, 1.0, v231
	v_med3_f32 v130, v130, 1.0, v231
	v_med3_f32 v131, v131, 1.0, v231
	v_med3_f32 v124, v124, 1.0, v231
	v_med3_f32 v125, v125, 1.0, v231
	v_med3_f32 v126, v126, 1.0, v231
	v_med3_f32 v127, v127, 1.0, v231
	v_med3_f32 v120, v120, 1.0, v231
	v_med3_f32 v121, v121, 1.0, v231
	v_med3_f32 v122, v122, 1.0, v231
	v_med3_f32 v123, v123, 1.0, v231
	v_med3_f32 v116, v116, 1.0, v231
	v_med3_f32 v117, v117, 1.0, v231
	v_med3_f32 v118, v118, 1.0, v231
	v_med3_f32 v119, v119, 1.0, v231
	v_cvt_u32_f32_e32 v128, v128
	v_cvt_u32_f32_e32 v120, v120
	v_cvt_u32_f32_sdwa v128, v129 dst_sel:BYTE_1 dst_unused:UNUSED_PRESERVE src0_sel:DWORD
	v_cvt_u32_f32_sdwa v120, v121 dst_sel:BYTE_1 dst_unused:UNUSED_PRESERVE src0_sel:DWORD
	v_cvt_u32_f32_e32 v129, v124
	v_cvt_u32_f32_e32 v121, v116
	v_cvt_u32_f32_sdwa v128, v130 dst_sel:BYTE_2 dst_unused:UNUSED_PRESERVE src0_sel:DWORD
	v_cvt_u32_f32_sdwa v120, v122 dst_sel:BYTE_2 dst_unused:UNUSED_PRESERVE src0_sel:DWORD
	v_cvt_u32_f32_sdwa v129, v125 dst_sel:BYTE_1 dst_unused:UNUSED_PRESERVE src0_sel:DWORD
	v_cvt_u32_f32_sdwa v121, v117 dst_sel:BYTE_1 dst_unused:UNUSED_PRESERVE src0_sel:DWORD
	v_cvt_u32_f32_sdwa v128, v131 dst_sel:BYTE_3 dst_unused:UNUSED_PRESERVE src0_sel:DWORD
	v_cvt_u32_f32_sdwa v120, v123 dst_sel:BYTE_3 dst_unused:UNUSED_PRESERVE src0_sel:DWORD
	v_cvt_u32_f32_sdwa v129, v126 dst_sel:BYTE_2 dst_unused:UNUSED_PRESERVE src0_sel:DWORD
	v_cvt_u32_f32_sdwa v121, v118 dst_sel:BYTE_2 dst_unused:UNUSED_PRESERVE src0_sel:DWORD
	v_cvt_u32_f32_sdwa v129, v127 dst_sel:BYTE_3 dst_unused:UNUSED_PRESERVE src0_sel:DWORD
	v_cvt_u32_f32_sdwa v121, v119 dst_sel:BYTE_3 dst_unused:UNUSED_PRESERVE src0_sel:DWORD
	s_nop 0
	global_store_dwordx2 v[148:149], v[128:129], off offset:-4096 nt
;     template <int ACT, int AUX> __device__ __forceinline__ void run(const f32x4 (&acc)[2][2][4][2], const Unit& uu, int wr, int wc, int fr, int fq) const {
;     ...
;                 for (int bj = 0; bj < 2; ++bj) { f32x4 v0 = acc[ai][bj][m][0] * rs, v1 = acc[ai][bj][m][1] * rs;
; #pragma unroll
;                     for (int j = 0; j < 4; ++j) { v0[j] = act_f<ACT>(v0[j]); v1[j] = act_f<ACT>(v1[j]); }
;                     if (AUX == 4) {
;                         unsigned q[8];
; #pragma unroll
;                         for (int j = 0; j < 4; ++j) { q[j] = (unsigned)fminf(fmaxf(fmaf(v0[j], 255.0f, 0.5f), 1.0f), 255.0f); q[4 + j] = (unsigned)fminf(fmaxf(fmaf(v1[j], 255.0f, 0.5f), 1.0f), 255.0f); }
;                         u32x2 w8; w8.x = q[0] | (q[1] << 8) | (q[2] << 16) | (q[3] << 24); w8.y = q[4] | (q[5] << 8) | (q[6] << 16) | (q[7] << 24);
;                         __builtin_nontemporal_store(w8, (u32x2*)(g8 + ((size_t)((u.pn - 52) >> 4) * cfg::MT + r) * cfg::DM + ((u.pn - 52) & 15) * BM + wc * 32 + 8 * fq + bj * HALF));
	global_store_dwordx2 v[148:149], v[120:121], off offset:-3584 nt
	v_pk_mul_f32 v[112:113], v[112:113], v[162:163] op_sel_hi:[1,0]
	v_pk_mul_f32 v[114:115], v[114:115], v[162:163] op_sel_hi:[1,0]
	v_pk_mul_f32 v[108:109], v[108:109], v[162:163] op_sel_hi:[1,0]
	v_pk_mul_f32 v[110:111], v[110:111], v[162:163] op_sel_hi:[1,0]
	v_pk_mul_f32 v[104:105], v[104:105], v[162:163] op_sel_hi:[1,0]
	v_pk_mul_f32 v[106:107], v[106:107], v[162:163] op_sel_hi:[1,0]
	v_pk_mul_f32 v[100:101], v[100:101], v[162:163] op_sel_hi:[1,0]
	v_pk_mul_f32 v[102:103], v[102:103], v[162:163] op_sel_hi:[1,0]
	v_fmamk_f32 v164, v157, 0x39800000, v221
	v_rsq_f32_e32 v164, v164
	v_exp_f32_e32 v112, v112
	v_exp_f32_e32 v113, v113
	v_exp_f32_e32 v114, v114
	v_exp_f32_e32 v115, v115
	v_mul_f32_e32 v164, 0xbfb8aa3b, v164
	v_exp_f32_e32 v108, v108
	v_exp_f32_e32 v109, v109
	v_exp_f32_e32 v110, v110
	v_exp_f32_e32 v111, v111
	v_exp_f32_e32 v104, v104
	v_exp_f32_e32 v105, v105
	v_exp_f32_e32 v106, v106
	v_exp_f32_e32 v107, v107
	v_exp_f32_e32 v100, v100
	v_exp_f32_e32 v101, v101
	v_exp_f32_e32 v102, v102
	v_exp_f32_e32 v103, v103
	v_pk_add_f32 v[112:113], v[112:113], v[146:147] op_sel_hi:[1,0]
	v_pk_add_f32 v[114:115], v[114:115], v[146:147] op_sel_hi:[1,0]
	v_pk_add_f32 v[108:109], v[108:109], v[146:147] op_sel_hi:[1,0]
	v_pk_add_f32 v[110:111], v[110:111], v[146:147] op_sel_hi:[1,0]
	v_pk_add_f32 v[104:105], v[104:105], v[146:147] op_sel_hi:[1,0]
	v_pk_add_f32 v[106:107], v[106:107], v[146:147] op_sel_hi:[1,0]
	v_pk_add_f32 v[100:101], v[100:101], v[146:147] op_sel_hi:[1,0]
	v_pk_add_f32 v[102:103], v[102:103], v[146:147] op_sel_hi:[1,0]
	v_rcp_f32_e32 v112, v112
	v_rcp_f32_e32 v113, v113
	v_rcp_f32_e32 v114, v114
	v_rcp_f32_e32 v115, v115
	v_rcp_f32_e32 v108, v108
	v_rcp_f32_e32 v109, v109
	v_rcp_f32_e32 v110, v110
	v_rcp_f32_e32 v111, v111
	v_rcp_f32_e32 v104, v104
	v_rcp_f32_e32 v105, v105
	v_rcp_f32_e32 v106, v106
	v_rcp_f32_e32 v107, v107
	v_rcp_f32_e32 v100, v100
	v_rcp_f32_e32 v101, v101
	v_rcp_f32_e32 v102, v102
	v_rcp_f32_e32 v103, v103
	v_pk_fma_f32 v[112:113], v[112:113], v[150:151], v[152:153] op_sel_hi:[1,0,0]
	v_pk_fma_f32 v[114:115], v[114:115], v[150:151], v[152:153] op_sel_hi:[1,0,0]
	v_pk_fma_f32 v[108:109], v[108:109], v[150:151], v[152:153] op_sel_hi:[1,0,0]
	v_pk_fma_f32 v[110:111], v[110:111], v[150:151], v[152:153] op_sel_hi:[1,0,0]
	v_pk_fma_f32 v[104:105], v[104:105], v[150:151], v[152:153] op_sel_hi:[1,0,0]
	v_pk_fma_f32 v[106:107], v[106:107], v[150:151], v[152:153] op_sel_hi:[1,0,0]
	v_pk_fma_f32 v[100:101], v[100:101], v[150:151], v[152:153] op_sel_hi:[1,0,0]
	v_pk_fma_f32 v[102:103], v[102:103], v[150:151], v[152:153] op_sel_hi:[1,0,0]
	v_med3_f32 v112, v112, 1.0, v231
	v_med3_f32 v113, v113, 1.0, v231
	v_med3_f32 v114, v114, 1.0, v231
	v_med3_f32 v115, v115, 1.0, v231
	v_med3_f32 v108, v108, 1.0, v231
	v_med3_f32 v109, v109, 1.0, v231
	v_med3_f32 v110, v110, 1.0, v231
	v_med3_f32 v111, v111, 1.0, v231
	v_med3_f32 v104, v104, 1.0, v231
	v_med3_f32 v105, v105, 1.0, v231
	v_med3_f32 v106, v106, 1.0, v231
	v_med3_f32 v107, v107, 1.0, v231
	v_med3_f32 v100, v100, 1.0, v231
	v_med3_f32 v101, v101, 1.0, v231
	v_med3_f32 v102, v102, 1.0, v231
	v_med3_f32 v103, v103, 1.0, v231
	v_cvt_u32_f32_e32 v112, v112
	v_cvt_u32_f32_e32 v104, v104
	v_cvt_u32_f32_sdwa v112, v113 dst_sel:BYTE_1 dst_unused:UNUSED_PRESERVE src0_sel:DWORD
	v_cvt_u32_f32_sdwa v104, v105 dst_sel:BYTE_1 dst_unused:UNUSED_PRESERVE src0_sel:DWORD
	v_cvt_u32_f32_e32 v113, v108
	v_cvt_u32_f32_e32 v105, v100
	v_cvt_u32_f32_sdwa v112, v114 dst_sel:BYTE_2 dst_unused:UNUSED_PRESERVE src0_sel:DWORD
	v_cvt_u32_f32_sdwa v104, v106 dst_sel:BYTE_2 dst_unused:UNUSED_PRESERVE src0_sel:DWORD
	v_cvt_u32_f32_sdwa v113, v109 dst_sel:BYTE_1 dst_unused:UNUSED_PRESERVE src0_sel:DWORD
	v_cvt_u32_f32_sdwa v105, v101 dst_sel:BYTE_1 dst_unused:UNUSED_PRESERVE src0_sel:DWORD
	v_cvt_u32_f32_sdwa v112, v115 dst_sel:BYTE_3 dst_unused:UNUSED_PRESERVE src0_sel:DWORD
	v_cvt_u32_f32_sdwa v104, v107 dst_sel:BYTE_3 dst_unused:UNUSED_PRESERVE src0_sel:DWORD
	v_cvt_u32_f32_sdwa v113, v110 dst_sel:BYTE_2 dst_unused:UNUSED_PRESERVE src0_sel:DWORD
	v_cvt_u32_f32_sdwa v105, v102 dst_sel:BYTE_2 dst_unused:UNUSED_PRESERVE src0_sel:DWORD
	v_cvt_u32_f32_sdwa v113, v111 dst_sel:BYTE_3 dst_unused:UNUSED_PRESERVE src0_sel:DWORD
	v_cvt_u32_f32_sdwa v105, v103 dst_sel:BYTE_3 dst_unused:UNUSED_PRESERVE src0_sel:DWORD
	s_nop 0
	global_store_dwordx2 v[148:149], v[112:113], off offset:-3072 nt
	global_store_dwordx2 v[148:149], v[104:105], off offset:-2560 nt
	v_pk_mul_f32 v[96:97], v[96:97], v[160:161] op_sel_hi:[1,0]
	v_pk_mul_f32 v[98:99], v[98:99], v[160:161] op_sel_hi:[1,0]
	v_pk_mul_f32 v[92:93], v[92:93], v[160:161] op_sel_hi:[1,0]
	v_pk_mul_f32 v[94:95], v[94:95], v[160:161] op_sel_hi:[1,0]
	v_pk_mul_f32 v[88:89], v[88:89], v[160:161] op_sel_hi:[1,0]
	v_pk_mul_f32 v[90:91], v[90:91], v[160:161] op_sel_hi:[1,0]
	v_pk_mul_f32 v[84:85], v[84:85], v[160:161] op_sel_hi:[1,0]
	v_pk_mul_f32 v[86:87], v[86:87], v[160:161] op_sel_hi:[1,0]
	v_fmamk_f32 v162, v159, 0x39800000, v221
	v_rsq_f32_e32 v162, v162
	v_exp_f32_e32 v96, v96
	v_exp_f32_e32 v97, v97
	v_exp_f32_e32 v98, v98
	v_exp_f32_e32 v99, v99
	v_mul_f32_e32 v162, 0xbfb8aa3b, v162
	v_exp_f32_e32 v92, v92
	v_exp_f32_e32 v93, v93
	v_exp_f32_e32 v94, v94
	v_exp_f32_e32 v95, v95
	v_exp_f32_e32 v88, v88
	v_exp_f32_e32 v89, v89
	v_exp_f32_e32 v90, v90
	v_exp_f32_e32 v91, v91
	v_exp_f32_e32 v84, v84
	v_exp_f32_e32 v85, v85
	v_exp_f32_e32 v86, v86
	v_exp_f32_e32 v87, v87
	v_pk_add_f32 v[96:97], v[96:97], v[146:147] op_sel_hi:[1,0]
	v_pk_add_f32 v[98:99], v[98:99], v[146:147] op_sel_hi:[1,0]
;     template <int ACT, int AUX> __device__ __forceinline__ void run(const f32x4 (&acc)[2][2][4][2], const Unit& uu, int wr, int wc, int fr, int fq) const {
;     ...
;                 for (int bj = 0; bj < 2; ++bj) { f32x4 v0 = acc[ai][bj][m][0] * rs, v1 = acc[ai][bj][m][1] * rs;
; #pragma unroll
;                     for (int j = 0; j < 4; ++j) { v0[j] = act_f<ACT>(v0[j]); v1[j] = act_f<ACT>(v1[j]); }
;                     if (AUX == 4) {
;                         unsigned q[8];
; #pragma unroll
;                         for (int j = 0; j < 4; ++j) { q[j] = (unsigned)fminf(fmaxf(fmaf(v0[j], 255.0f, 0.5f), 1.0f), 255.0f); q[4 + j] = (unsigned)fminf(fmaxf(fmaf(v1[j], 255.0f, 0.5f), 1.0f), 255.0f); }
;                         u32x2 w8; w8.x = q[0] | (q[1] << 8) | (q[2] << 16) | (q[3] << 24); w8.y = q[4] | (q[5] << 8) | (q[6] << 16) | (q[7] << 24);
;                         __builtin_nontemporal_store(w8, (u32x2*)(g8 + ((size_t)((u.pn - 52) >> 4) * cfg::MT + r) * cfg::DM + ((u.pn - 52) & 15) * BM + wc * 32 + 8 * fq + bj * HALF));
	v_pk_add_f32 v[92:93], v[92:93], v[146:147] op_sel_hi:[1,0]
	v_pk_add_f32 v[94:95], v[94:95], v[146:147] op_sel_hi:[1,0]
	v_pk_add_f32 v[88:89], v[88:89], v[146:147] op_sel_hi:[1,0]
	v_pk_add_f32 v[90:91], v[90:91], v[146:147] op_sel_hi:[1,0]
	v_pk_add_f32 v[84:85], v[84:85], v[146:147] op_sel_hi:[1,0]
	v_pk_add_f32 v[86:87], v[86:87], v[146:147] op_sel_hi:[1,0]
	v_rcp_f32_e32 v96, v96
	v_rcp_f32_e32 v97, v97
	v_rcp_f32_e32 v98, v98
	v_rcp_f32_e32 v99, v99
	v_rcp_f32_e32 v92, v92
	v_rcp_f32_e32 v93, v93
	v_rcp_f32_e32 v94, v94
	v_rcp_f32_e32 v95, v95
	v_rcp_f32_e32 v88, v88
	v_rcp_f32_e32 v89, v89
	v_rcp_f32_e32 v90, v90
	v_rcp_f32_e32 v91, v91
	v_rcp_f32_e32 v84, v84
	v_rcp_f32_e32 v85, v85
	v_rcp_f32_e32 v86, v86
	v_rcp_f32_e32 v87, v87
	v_pk_fma_f32 v[96:97], v[96:97], v[150:151], v[152:153] op_sel_hi:[1,0,0]
	v_pk_fma_f32 v[98:99], v[98:99], v[150:151], v[152:153] op_sel_hi:[1,0,0]
	v_pk_fma_f32 v[92:93], v[92:93], v[150:151], v[152:153] op_sel_hi:[1,0,0]
	v_pk_fma_f32 v[94:95], v[94:95], v[150:151], v[152:153] op_sel_hi:[1,0,0]
	v_pk_fma_f32 v[88:89], v[88:89], v[150:151], v[152:153] op_sel_hi:[1,0,0]
	v_pk_fma_f32 v[90:91], v[90:91], v[150:151], v[152:153] op_sel_hi:[1,0,0]
	v_pk_fma_f32 v[84:85], v[84:85], v[150:151], v[152:153] op_sel_hi:[1,0,0]
	v_pk_fma_f32 v[86:87], v[86:87], v[150:151], v[152:153] op_sel_hi:[1,0,0]
	v_med3_f32 v96, v96, 1.0, v231
	v_med3_f32 v97, v97, 1.0, v231
	v_med3_f32 v98, v98, 1.0, v231
	v_med3_f32 v99, v99, 1.0, v231
	v_med3_f32 v92, v92, 1.0, v231
	v_med3_f32 v93, v93, 1.0, v231
	v_med3_f32 v94, v94, 1.0, v231
	v_med3_f32 v95, v95, 1.0, v231
	v_med3_f32 v88, v88, 1.0, v231
	v_med3_f32 v89, v89, 1.0, v231
	v_med3_f32 v90, v90, 1.0, v231
	v_med3_f32 v91, v91, 1.0, v231
	v_med3_f32 v84, v84, 1.0, v231
	v_med3_f32 v85, v85, 1.0, v231
	v_med3_f32 v86, v86, 1.0, v231
	v_med3_f32 v87, v87, 1.0, v231
	v_cvt_u32_f32_e32 v96, v96
	v_cvt_u32_f32_e32 v88, v88
	v_cvt_u32_f32_sdwa v96, v97 dst_sel:BYTE_1 dst_unused:UNUSED_PRESERVE src0_sel:DWORD
	v_cvt_u32_f32_sdwa v88, v89 dst_sel:BYTE_1 dst_unused:UNUSED_PRESERVE src0_sel:DWORD
	v_cvt_u32_f32_e32 v97, v92
	v_cvt_u32_f32_e32 v89, v84
	v_cvt_u32_f32_sdwa v96, v98 dst_sel:BYTE_2 dst_unused:UNUSED_PRESERVE src0_sel:DWORD
	v_cvt_u32_f32_sdwa v88, v90 dst_sel:BYTE_2 dst_unused:UNUSED_PRESERVE src0_sel:DWORD
	v_cvt_u32_f32_sdwa v97, v93 dst_sel:BYTE_1 dst_unused:UNUSED_PRESERVE src0_sel:DWORD
	v_cvt_u32_f32_sdwa v89, v85 dst_sel:BYTE_1 dst_unused:UNUSED_PRESERVE src0_sel:DWORD
	v_cvt_u32_f32_sdwa v96, v99 dst_sel:BYTE_3 dst_unused:UNUSED_PRESERVE src0_sel:DWORD
	v_cvt_u32_f32_sdwa v88, v91 dst_sel:BYTE_3 dst_unused:UNUSED_PRESERVE src0_sel:DWORD
	v_cvt_u32_f32_sdwa v97, v94 dst_sel:BYTE_2 dst_unused:UNUSED_PRESERVE src0_sel:DWORD
	v_cvt_u32_f32_sdwa v89, v86 dst_sel:BYTE_2 dst_unused:UNUSED_PRESERVE src0_sel:DWORD
	v_cvt_u32_f32_sdwa v97, v95 dst_sel:BYTE_3 dst_unused:UNUSED_PRESERVE src0_sel:DWORD
	v_cvt_u32_f32_sdwa v89, v87 dst_sel:BYTE_3 dst_unused:UNUSED_PRESERVE src0_sel:DWORD
	s_nop 0
	global_store_dwordx2 v[148:149], v[96:97], off offset:-2048 nt
	global_store_dwordx2 v[148:149], v[88:89], off offset:-1536 nt
	v_pk_mul_f32 v[80:81], v[80:81], v[164:165] op_sel_hi:[1,0]
	v_pk_mul_f32 v[82:83], v[82:83], v[164:165] op_sel_hi:[1,0]
	v_pk_mul_f32 v[76:77], v[76:77], v[164:165] op_sel_hi:[1,0]
	v_pk_mul_f32 v[78:79], v[78:79], v[164:165] op_sel_hi:[1,0]
	v_pk_mul_f32 v[72:73], v[72:73], v[164:165] op_sel_hi:[1,0]
	v_pk_mul_f32 v[74:75], v[74:75], v[164:165] op_sel_hi:[1,0]
	v_pk_mul_f32 v[68:69], v[68:69], v[164:165] op_sel_hi:[1,0]
	v_pk_mul_f32 v[70:71], v[70:71], v[164:165] op_sel_hi:[1,0]
	v_fmamk_f32 v160, v154, 0x39800000, v221
	v_rsq_f32_e32 v160, v160
	v_exp_f32_e32 v80, v80
	v_exp_f32_e32 v81, v81
	v_exp_f32_e32 v82, v82
	v_exp_f32_e32 v83, v83
	v_mul_f32_e32 v160, 0xbfb8aa3b, v160
	v_exp_f32_e32 v76, v76
	v_exp_f32_e32 v77, v77
	v_exp_f32_e32 v78, v78
	v_exp_f32_e32 v79, v79
	v_exp_f32_e32 v72, v72
	v_exp_f32_e32 v73, v73
	v_exp_f32_e32 v74, v74
	v_exp_f32_e32 v75, v75
	v_exp_f32_e32 v68, v68
	v_exp_f32_e32 v69, v69
	v_exp_f32_e32 v70, v70
	v_exp_f32_e32 v71, v71
	v_pk_add_f32 v[80:81], v[80:81], v[146:147] op_sel_hi:[1,0]
	v_pk_add_f32 v[82:83], v[82:83], v[146:147] op_sel_hi:[1,0]
	v_pk_add_f32 v[76:77], v[76:77], v[146:147] op_sel_hi:[1,0]
	v_pk_add_f32 v[78:79], v[78:79], v[146:147] op_sel_hi:[1,0]
	v_pk_add_f32 v[72:73], v[72:73], v[146:147] op_sel_hi:[1,0]
	v_pk_add_f32 v[74:75], v[74:75], v[146:147] op_sel_hi:[1,0]
	v_pk_add_f32 v[68:69], v[68:69], v[146:147] op_sel_hi:[1,0]
	v_pk_add_f32 v[70:71], v[70:71], v[146:147] op_sel_hi:[1,0]
	v_rcp_f32_e32 v80, v80
	v_rcp_f32_e32 v81, v81
	v_rcp_f32_e32 v82, v82
	v_rcp_f32_e32 v83, v83
	v_rcp_f32_e32 v76, v76
	v_rcp_f32_e32 v77, v77
	v_rcp_f32_e32 v78, v78
	v_rcp_f32_e32 v79, v79
	v_rcp_f32_e32 v72, v72
	v_rcp_f32_e32 v73, v73
	v_rcp_f32_e32 v74, v74
	v_rcp_f32_e32 v75, v75
	v_rcp_f32_e32 v68, v68
	v_rcp_f32_e32 v69, v69
	v_rcp_f32_e32 v70, v70
	v_rcp_f32_e32 v71, v71
	v_pk_fma_f32 v[80:81], v[80:81], v[150:151], v[152:153] op_sel_hi:[1,0,0]
	v_pk_fma_f32 v[82:83], v[82:83], v[150:151], v[152:153] op_sel_hi:[1,0,0]
	v_pk_fma_f32 v[76:77], v[76:77], v[150:151], v[152:153] op_sel_hi:[1,0,0]
	v_pk_fma_f32 v[78:79], v[78:79], v[150:151], v[152:153] op_sel_hi:[1,0,0]
	v_pk_fma_f32 v[72:73], v[72:73], v[150:151], v[152:153] op_sel_hi:[1,0,0]
	v_pk_fma_f32 v[74:75], v[74:75], v[150:151], v[152:153] op_sel_hi:[1,0,0]
	v_pk_fma_f32 v[68:69], v[68:69], v[150:151], v[152:153] op_sel_hi:[1,0,0]
	v_pk_fma_f32 v[70:71], v[70:71], v[150:151], v[152:153] op_sel_hi:[1,0,0]
	v_med3_f32 v80, v80, 1.0, v231
;     template <int ACT, int AUX> __device__ __forceinline__ void run(const f32x4 (&acc)[2][2][4][2], const Unit& uu, int wr, int wc, int fr, int fq) const {
;     ...
;                 for (int bj = 0; bj < 2; ++bj) { f32x4 v0 = acc[ai][bj][m][0] * rs, v1 = acc[ai][bj][m][1] * rs;
; #pragma unroll
;                     for (int j = 0; j < 4; ++j) { v0[j] = act_f<ACT>(v0[j]); v1[j] = act_f<ACT>(v1[j]); }
;                     if (AUX == 4) {
;                         unsigned q[8];
; #pragma unroll
;                         for (int j = 0; j < 4; ++j) { q[j] = (unsigned)fminf(fmaxf(fmaf(v0[j], 255.0f, 0.5f), 1.0f), 255.0f); q[4 + j] = (unsigned)fminf(fmaxf(fmaf(v1[j], 255.0f, 0.5f), 1.0f), 255.0f); }
;                         u32x2 w8; w8.x = q[0] | (q[1] << 8) | (q[2] << 16) | (q[3] << 24); w8.y = q[4] | (q[5] << 8) | (q[6] << 16) | (q[7] << 24);
;                         __builtin_nontemporal_store(w8, (u32x2*)(g8 + ((size_t)((u.pn - 52) >> 4) * cfg::MT + r) * cfg::DM + ((u.pn - 52) & 15) * BM + wc * 32 + 8 * fq + bj * HALF));
	v_med3_f32 v81, v81, 1.0, v231
	v_med3_f32 v82, v82, 1.0, v231
	v_med3_f32 v83, v83, 1.0, v231
	v_med3_f32 v76, v76, 1.0, v231
	v_med3_f32 v77, v77, 1.0, v231
	v_med3_f32 v78, v78, 1.0, v231
	v_med3_f32 v79, v79, 1.0, v231
	v_med3_f32 v72, v72, 1.0, v231
	v_med3_f32 v73, v73, 1.0, v231
	v_med3_f32 v74, v74, 1.0, v231
	v_med3_f32 v75, v75, 1.0, v231
	v_med3_f32 v68, v68, 1.0, v231
	v_med3_f32 v69, v69, 1.0, v231
	v_med3_f32 v70, v70, 1.0, v231
	v_med3_f32 v71, v71, 1.0, v231
	v_cvt_u32_f32_e32 v80, v80
	v_cvt_u32_f32_e32 v72, v72
	v_cvt_u32_f32_sdwa v80, v81 dst_sel:BYTE_1 dst_unused:UNUSED_PRESERVE src0_sel:DWORD
	v_cvt_u32_f32_sdwa v72, v73 dst_sel:BYTE_1 dst_unused:UNUSED_PRESERVE src0_sel:DWORD
	v_cvt_u32_f32_e32 v81, v76
	v_cvt_u32_f32_e32 v73, v68
	v_cvt_u32_f32_sdwa v80, v82 dst_sel:BYTE_2 dst_unused:UNUSED_PRESERVE src0_sel:DWORD
	v_cvt_u32_f32_sdwa v72, v74 dst_sel:BYTE_2 dst_unused:UNUSED_PRESERVE src0_sel:DWORD
	v_cvt_u32_f32_sdwa v81, v77 dst_sel:BYTE_1 dst_unused:UNUSED_PRESERVE src0_sel:DWORD
	v_cvt_u32_f32_sdwa v73, v69 dst_sel:BYTE_1 dst_unused:UNUSED_PRESERVE src0_sel:DWORD
	v_cvt_u32_f32_sdwa v80, v83 dst_sel:BYTE_3 dst_unused:UNUSED_PRESERVE src0_sel:DWORD
	v_cvt_u32_f32_sdwa v72, v75 dst_sel:BYTE_3 dst_unused:UNUSED_PRESERVE src0_sel:DWORD
	v_cvt_u32_f32_sdwa v81, v78 dst_sel:BYTE_2 dst_unused:UNUSED_PRESERVE src0_sel:DWORD
	v_cvt_u32_f32_sdwa v73, v70 dst_sel:BYTE_2 dst_unused:UNUSED_PRESERVE src0_sel:DWORD
	v_cvt_u32_f32_sdwa v81, v79 dst_sel:BYTE_3 dst_unused:UNUSED_PRESERVE src0_sel:DWORD
	v_cvt_u32_f32_sdwa v73, v71 dst_sel:BYTE_3 dst_unused:UNUSED_PRESERVE src0_sel:DWORD
	s_nop 0
	global_store_dwordx2 v[148:149], v[80:81], off offset:-1024 nt
	global_store_dwordx2 v[148:149], v[72:73], off offset:-512 nt
	v_pk_mul_f32 v[64:65], v[64:65], v[162:163] op_sel_hi:[1,0]
	v_pk_mul_f32 v[66:67], v[66:67], v[162:163] op_sel_hi:[1,0]
	v_pk_mul_f32 v[60:61], v[60:61], v[162:163] op_sel_hi:[1,0]
	v_pk_mul_f32 v[62:63], v[62:63], v[162:163] op_sel_hi:[1,0]
	v_pk_mul_f32 v[56:57], v[56:57], v[162:163] op_sel_hi:[1,0]
	v_pk_mul_f32 v[58:59], v[58:59], v[162:163] op_sel_hi:[1,0]
	v_pk_mul_f32 v[52:53], v[52:53], v[162:163] op_sel_hi:[1,0]
	v_pk_mul_f32 v[54:55], v[54:55], v[162:163] op_sel_hi:[1,0]
	v_fmamk_f32 v164, v156, 0x39800000, v221
	v_rsq_f32_e32 v164, v164
	v_exp_f32_e32 v64, v64
	v_exp_f32_e32 v65, v65
	v_exp_f32_e32 v66, v66
	v_exp_f32_e32 v67, v67
	v_mul_f32_e32 v164, 0xbfb8aa3b, v164
	v_exp_f32_e32 v60, v60
	v_exp_f32_e32 v61, v61
	v_exp_f32_e32 v62, v62
	v_exp_f32_e32 v63, v63
	v_exp_f32_e32 v56, v56
	v_exp_f32_e32 v57, v57
	v_exp_f32_e32 v58, v58
	v_exp_f32_e32 v59, v59
	v_exp_f32_e32 v52, v52
	v_exp_f32_e32 v53, v53
	v_exp_f32_e32 v54, v54
	v_exp_f32_e32 v55, v55
	v_pk_add_f32 v[64:65], v[64:65], v[146:147] op_sel_hi:[1,0]
	v_pk_add_f32 v[66:67], v[66:67], v[146:147] op_sel_hi:[1,0]
	v_pk_add_f32 v[60:61], v[60:61], v[146:147] op_sel_hi:[1,0]
	v_pk_add_f32 v[62:63], v[62:63], v[146:147] op_sel_hi:[1,0]
	v_pk_add_f32 v[56:57], v[56:57], v[146:147] op_sel_hi:[1,0]
	v_pk_add_f32 v[58:59], v[58:59], v[146:147] op_sel_hi:[1,0]
	v_pk_add_f32 v[52:53], v[52:53], v[146:147] op_sel_hi:[1,0]
	v_pk_add_f32 v[54:55], v[54:55], v[146:147] op_sel_hi:[1,0]
	v_rcp_f32_e32 v64, v64
	v_rcp_f32_e32 v65, v65
	v_rcp_f32_e32 v66, v66
	v_rcp_f32_e32 v67, v67
	v_rcp_f32_e32 v60, v60
	v_rcp_f32_e32 v61, v61
	v_rcp_f32_e32 v62, v62
	v_rcp_f32_e32 v63, v63
	v_rcp_f32_e32 v56, v56
	v_rcp_f32_e32 v57, v57
	v_rcp_f32_e32 v58, v58
	v_rcp_f32_e32 v59, v59
	v_rcp_f32_e32 v52, v52
	v_rcp_f32_e32 v53, v53
	v_rcp_f32_e32 v54, v54
	v_rcp_f32_e32 v55, v55
	v_pk_fma_f32 v[64:65], v[64:65], v[150:151], v[152:153] op_sel_hi:[1,0,0]
	v_pk_fma_f32 v[66:67], v[66:67], v[150:151], v[152:153] op_sel_hi:[1,0,0]
	v_pk_fma_f32 v[60:61], v[60:61], v[150:151], v[152:153] op_sel_hi:[1,0,0]
	v_pk_fma_f32 v[62:63], v[62:63], v[150:151], v[152:153] op_sel_hi:[1,0,0]
	v_pk_fma_f32 v[56:57], v[56:57], v[150:151], v[152:153] op_sel_hi:[1,0,0]
	v_pk_fma_f32 v[58:59], v[58:59], v[150:151], v[152:153] op_sel_hi:[1,0,0]
	v_pk_fma_f32 v[52:53], v[52:53], v[150:151], v[152:153] op_sel_hi:[1,0,0]
	v_pk_fma_f32 v[54:55], v[54:55], v[150:151], v[152:153] op_sel_hi:[1,0,0]
	v_med3_f32 v64, v64, 1.0, v231
	v_med3_f32 v65, v65, 1.0, v231
	v_med3_f32 v66, v66, 1.0, v231
	v_med3_f32 v67, v67, 1.0, v231
	v_med3_f32 v60, v60, 1.0, v231
	v_med3_f32 v61, v61, 1.0, v231
	v_med3_f32 v62, v62, 1.0, v231
	v_med3_f32 v63, v63, 1.0, v231
	v_med3_f32 v56, v56, 1.0, v231
	v_med3_f32 v57, v57, 1.0, v231
	v_med3_f32 v58, v58, 1.0, v231
	v_med3_f32 v59, v59, 1.0, v231
	v_med3_f32 v52, v52, 1.0, v231
	v_med3_f32 v53, v53, 1.0, v231
	v_med3_f32 v54, v54, 1.0, v231
	v_med3_f32 v55, v55, 1.0, v231
	v_cvt_u32_f32_e32 v64, v64
	v_cvt_u32_f32_e32 v56, v56
	v_cvt_u32_f32_sdwa v64, v65 dst_sel:BYTE_1 dst_unused:UNUSED_PRESERVE src0_sel:DWORD
	v_cvt_u32_f32_sdwa v56, v57 dst_sel:BYTE_1 dst_unused:UNUSED_PRESERVE src0_sel:DWORD
	v_cvt_u32_f32_e32 v65, v60
	v_cvt_u32_f32_e32 v57, v52
	v_cvt_u32_f32_sdwa v64, v66 dst_sel:BYTE_2 dst_unused:UNUSED_PRESERVE src0_sel:DWORD
	v_cvt_u32_f32_sdwa v56, v58 dst_sel:BYTE_2 dst_unused:UNUSED_PRESERVE src0_sel:DWORD
	v_cvt_u32_f32_sdwa v65, v61 dst_sel:BYTE_1 dst_unused:UNUSED_PRESERVE src0_sel:DWORD
	v_cvt_u32_f32_sdwa v57, v53 dst_sel:BYTE_1 dst_unused:UNUSED_PRESERVE src0_sel:DWORD
	v_cvt_u32_f32_sdwa v64, v67 dst_sel:BYTE_3 dst_unused:UNUSED_PRESERVE src0_sel:DWORD
	v_cvt_u32_f32_sdwa v56, v59 dst_sel:BYTE_3 dst_unused:UNUSED_PRESERVE src0_sel:DWORD
	v_cvt_u32_f32_sdwa v65, v62 dst_sel:BYTE_2 dst_unused:UNUSED_PRESERVE src0_sel:DWORD
;     template <int ACT, int AUX> __device__ __forceinline__ void run(const f32x4 (&acc)[2][2][4][2], const Unit& uu, int wr, int wc, int fr, int fq) const {
;     ...
;                 for (int bj = 0; bj < 2; ++bj) { f32x4 v0 = acc[ai][bj][m][0] * rs, v1 = acc[ai][bj][m][1] * rs;
; #pragma unroll
;                     for (int j = 0; j < 4; ++j) { v0[j] = act_f<ACT>(v0[j]); v1[j] = act_f<ACT>(v1[j]); }
;                     if (AUX == 4) {
;                         unsigned q[8];
; #pragma unroll
;                         for (int j = 0; j < 4; ++j) { q[j] = (unsigned)fminf(fmaxf(fmaf(v0[j], 255.0f, 0.5f), 1.0f), 255.0f); q[4 + j] = (unsigned)fminf(fmaxf(fmaf(v1[j], 255.0f, 0.5f), 1.0f), 255.0f); }
;                         u32x2 w8; w8.x = q[0] | (q[1] << 8) | (q[2] << 16) | (q[3] << 24); w8.y = q[4] | (q[5] << 8) | (q[6] << 16) | (q[7] << 24);
;                         __builtin_nontemporal_store(w8, (u32x2*)(g8 + ((size_t)((u.pn - 52) >> 4) * cfg::MT + r) * cfg::DM + ((u.pn - 52) & 15) * BM + wc * 32 + 8 * fq + bj * HALF));
	v_cvt_u32_f32_sdwa v57, v54 dst_sel:BYTE_2 dst_unused:UNUSED_PRESERVE src0_sel:DWORD
	v_cvt_u32_f32_sdwa v65, v63 dst_sel:BYTE_3 dst_unused:UNUSED_PRESERVE src0_sel:DWORD
	v_cvt_u32_f32_sdwa v57, v55 dst_sel:BYTE_3 dst_unused:UNUSED_PRESERVE src0_sel:DWORD
	s_nop 0
	global_store_dwordx2 v[148:149], v[64:65], off offset:0 nt
	global_store_dwordx2 v[148:149], v[56:57], off offset:512 nt
	v_pk_mul_f32 v[48:49], v[48:49], v[160:161] op_sel_hi:[1,0]
	v_pk_mul_f32 v[50:51], v[50:51], v[160:161] op_sel_hi:[1,0]
	v_pk_mul_f32 v[44:45], v[44:45], v[160:161] op_sel_hi:[1,0]
	v_pk_mul_f32 v[46:47], v[46:47], v[160:161] op_sel_hi:[1,0]
	v_pk_mul_f32 v[40:41], v[40:41], v[160:161] op_sel_hi:[1,0]
	v_pk_mul_f32 v[42:43], v[42:43], v[160:161] op_sel_hi:[1,0]
	v_pk_mul_f32 v[36:37], v[36:37], v[160:161] op_sel_hi:[1,0]
	v_pk_mul_f32 v[38:39], v[38:39], v[160:161] op_sel_hi:[1,0]
	v_fmamk_f32 v162, v158, 0x39800000, v221
	v_rsq_f32_e32 v162, v162
	v_exp_f32_e32 v48, v48
	v_exp_f32_e32 v49, v49
	v_exp_f32_e32 v50, v50
	v_exp_f32_e32 v51, v51
	v_mul_f32_e32 v162, 0xbfb8aa3b, v162
	v_exp_f32_e32 v44, v44
	v_exp_f32_e32 v45, v45
	v_exp_f32_e32 v46, v46
	v_exp_f32_e32 v47, v47
	v_exp_f32_e32 v40, v40
	v_exp_f32_e32 v41, v41
	v_exp_f32_e32 v42, v42
	v_exp_f32_e32 v43, v43
	v_exp_f32_e32 v36, v36
	v_exp_f32_e32 v37, v37
	v_exp_f32_e32 v38, v38
	v_exp_f32_e32 v39, v39
	v_pk_add_f32 v[48:49], v[48:49], v[146:147] op_sel_hi:[1,0]
	v_pk_add_f32 v[50:51], v[50:51], v[146:147] op_sel_hi:[1,0]
	v_pk_add_f32 v[44:45], v[44:45], v[146:147] op_sel_hi:[1,0]
	v_pk_add_f32 v[46:47], v[46:47], v[146:147] op_sel_hi:[1,0]
	v_pk_add_f32 v[40:41], v[40:41], v[146:147] op_sel_hi:[1,0]
	v_pk_add_f32 v[42:43], v[42:43], v[146:147] op_sel_hi:[1,0]
	v_pk_add_f32 v[36:37], v[36:37], v[146:147] op_sel_hi:[1,0]
	v_pk_add_f32 v[38:39], v[38:39], v[146:147] op_sel_hi:[1,0]
	v_rcp_f32_e32 v48, v48
	v_rcp_f32_e32 v49, v49
	v_rcp_f32_e32 v50, v50
	v_rcp_f32_e32 v51, v51
	v_rcp_f32_e32 v44, v44
	v_rcp_f32_e32 v45, v45
	v_rcp_f32_e32 v46, v46
	v_rcp_f32_e32 v47, v47
	v_rcp_f32_e32 v40, v40
	v_rcp_f32_e32 v41, v41
	v_rcp_f32_e32 v42, v42
	v_rcp_f32_e32 v43, v43
	v_rcp_f32_e32 v36, v36
	v_rcp_f32_e32 v37, v37
	v_rcp_f32_e32 v38, v38
	v_rcp_f32_e32 v39, v39
	v_pk_fma_f32 v[48:49], v[48:49], v[150:151], v[152:153] op_sel_hi:[1,0,0]
	v_pk_fma_f32 v[50:51], v[50:51], v[150:151], v[152:153] op_sel_hi:[1,0,0]
	v_pk_fma_f32 v[44:45], v[44:45], v[150:151], v[152:153] op_sel_hi:[1,0,0]
	v_pk_fma_f32 v[46:47], v[46:47], v[150:151], v[152:153] op_sel_hi:[1,0,0]
	v_pk_fma_f32 v[40:41], v[40:41], v[150:151], v[152:153] op_sel_hi:[1,0,0]
	v_pk_fma_f32 v[42:43], v[42:43], v[150:151], v[152:153] op_sel_hi:[1,0,0]
	v_pk_fma_f32 v[36:37], v[36:37], v[150:151], v[152:153] op_sel_hi:[1,0,0]
	v_pk_fma_f32 v[38:39], v[38:39], v[150:151], v[152:153] op_sel_hi:[1,0,0]
	v_med3_f32 v48, v48, 1.0, v231
	v_med3_f32 v49, v49, 1.0, v231
	v_med3_f32 v50, v50, 1.0, v231
	v_med3_f32 v51, v51, 1.0, v231
	v_med3_f32 v44, v44, 1.0, v231
	v_med3_f32 v45, v45, 1.0, v231
	v_med3_f32 v46, v46, 1.0, v231
	v_med3_f32 v47, v47, 1.0, v231
	v_med3_f32 v40, v40, 1.0, v231
	v_med3_f32 v41, v41, 1.0, v231
	v_med3_f32 v42, v42, 1.0, v231
	v_med3_f32 v43, v43, 1.0, v231
	v_med3_f32 v36, v36, 1.0, v231
	v_med3_f32 v37, v37, 1.0, v231
	v_med3_f32 v38, v38, 1.0, v231
	v_med3_f32 v39, v39, 1.0, v231
	v_cvt_u32_f32_e32 v48, v48
	v_cvt_u32_f32_e32 v40, v40
	v_cvt_u32_f32_sdwa v48, v49 dst_sel:BYTE_1 dst_unused:UNUSED_PRESERVE src0_sel:DWORD
	v_cvt_u32_f32_sdwa v40, v41 dst_sel:BYTE_1 dst_unused:UNUSED_PRESERVE src0_sel:DWORD
	v_cvt_u32_f32_e32 v49, v44
	v_cvt_u32_f32_e32 v41, v36
	v_cvt_u32_f32_sdwa v48, v50 dst_sel:BYTE_2 dst_unused:UNUSED_PRESERVE src0_sel:DWORD
	v_cvt_u32_f32_sdwa v40, v42 dst_sel:BYTE_2 dst_unused:UNUSED_PRESERVE src0_sel:DWORD
	v_cvt_u32_f32_sdwa v49, v45 dst_sel:BYTE_1 dst_unused:UNUSED_PRESERVE src0_sel:DWORD
	v_cvt_u32_f32_sdwa v41, v37 dst_sel:BYTE_1 dst_unused:UNUSED_PRESERVE src0_sel:DWORD
	v_cvt_u32_f32_sdwa v48, v51 dst_sel:BYTE_3 dst_unused:UNUSED_PRESERVE src0_sel:DWORD
	v_cvt_u32_f32_sdwa v40, v43 dst_sel:BYTE_3 dst_unused:UNUSED_PRESERVE src0_sel:DWORD
	v_cvt_u32_f32_sdwa v49, v46 dst_sel:BYTE_2 dst_unused:UNUSED_PRESERVE src0_sel:DWORD
	v_cvt_u32_f32_sdwa v41, v38 dst_sel:BYTE_2 dst_unused:UNUSED_PRESERVE src0_sel:DWORD
	v_cvt_u32_f32_sdwa v49, v47 dst_sel:BYTE_3 dst_unused:UNUSED_PRESERVE src0_sel:DWORD
	v_cvt_u32_f32_sdwa v41, v39 dst_sel:BYTE_3 dst_unused:UNUSED_PRESERVE src0_sel:DWORD
	s_nop 0
	global_store_dwordx2 v[148:149], v[48:49], off offset:1024 nt
	global_store_dwordx2 v[148:149], v[40:41], off offset:1536 nt
	v_pk_mul_f32 v[32:33], v[32:33], v[164:165] op_sel_hi:[1,0]
	v_pk_mul_f32 v[34:35], v[34:35], v[164:165] op_sel_hi:[1,0]
	v_pk_mul_f32 v[28:29], v[28:29], v[164:165] op_sel_hi:[1,0]
	v_pk_mul_f32 v[30:31], v[30:31], v[164:165] op_sel_hi:[1,0]
	v_pk_mul_f32 v[24:25], v[24:25], v[164:165] op_sel_hi:[1,0]
	v_pk_mul_f32 v[26:27], v[26:27], v[164:165] op_sel_hi:[1,0]
	v_pk_mul_f32 v[20:21], v[20:21], v[164:165] op_sel_hi:[1,0]
	v_pk_mul_f32 v[22:23], v[22:23], v[164:165] op_sel_hi:[1,0]
	v_exp_f32_e32 v32, v32
	v_exp_f32_e32 v33, v33
	v_exp_f32_e32 v34, v34
	v_exp_f32_e32 v35, v35
	v_exp_f32_e32 v28, v28
	v_exp_f32_e32 v29, v29
	v_exp_f32_e32 v30, v30
	v_exp_f32_e32 v31, v31
	v_exp_f32_e32 v24, v24
	v_exp_f32_e32 v25, v25
	v_exp_f32_e32 v26, v26
	v_exp_f32_e32 v27, v27
	v_exp_f32_e32 v20, v20
	v_exp_f32_e32 v21, v21
	v_exp_f32_e32 v22, v22
	v_exp_f32_e32 v23, v23
	v_pk_add_f32 v[32:33], v[32:33], v[146:147] op_sel_hi:[1,0]
	v_pk_add_f32 v[34:35], v[34:35], v[146:147] op_sel_hi:[1,0]
;     template <int ACT, int AUX> __device__ __forceinline__ void run(const f32x4 (&acc)[2][2][4][2], const Unit& uu, int wr, int wc, int fr, int fq) const {
;     ...
;                 for (int bj = 0; bj < 2; ++bj) { f32x4 v0 = acc[ai][bj][m][0] * rs, v1 = acc[ai][bj][m][1] * rs;
; #pragma unroll
;                     for (int j = 0; j < 4; ++j) { v0[j] = act_f<ACT>(v0[j]); v1[j] = act_f<ACT>(v1[j]); }
;                     if (AUX == 4) {
;                         unsigned q[8];
; #pragma unroll
;                         for (int j = 0; j < 4; ++j) { q[j] = (unsigned)fminf(fmaxf(fmaf(v0[j], 255.0f, 0.5f), 1.0f), 255.0f); q[4 + j] = (unsigned)fminf(fmaxf(fmaf(v1[j], 255.0f, 0.5f), 1.0f), 255.0f); }
;                         u32x2 w8; w8.x = q[0] | (q[1] << 8) | (q[2] << 16) | (q[3] << 24); w8.y = q[4] | (q[5] << 8) | (q[6] << 16) | (q[7] << 24);
;                         __builtin_nontemporal_store(w8, (u32x2*)(g8 + ((size_t)((u.pn - 52) >> 4) * cfg::MT + r) * cfg::DM + ((u.pn - 52) & 15) * BM + wc * 32 + 8 * fq + bj * HALF));
	v_pk_add_f32 v[28:29], v[28:29], v[146:147] op_sel_hi:[1,0]
	v_pk_add_f32 v[30:31], v[30:31], v[146:147] op_sel_hi:[1,0]
	v_pk_add_f32 v[24:25], v[24:25], v[146:147] op_sel_hi:[1,0]
	v_pk_add_f32 v[26:27], v[26:27], v[146:147] op_sel_hi:[1,0]
	v_pk_add_f32 v[20:21], v[20:21], v[146:147] op_sel_hi:[1,0]
	v_pk_add_f32 v[22:23], v[22:23], v[146:147] op_sel_hi:[1,0]
	v_rcp_f32_e32 v32, v32
	v_rcp_f32_e32 v33, v33
	v_rcp_f32_e32 v34, v34
	v_rcp_f32_e32 v35, v35
	v_rcp_f32_e32 v28, v28
	v_rcp_f32_e32 v29, v29
	v_rcp_f32_e32 v30, v30
	v_rcp_f32_e32 v31, v31
	v_rcp_f32_e32 v24, v24
	v_rcp_f32_e32 v25, v25
	v_rcp_f32_e32 v26, v26
	v_rcp_f32_e32 v27, v27
	v_rcp_f32_e32 v20, v20
	v_rcp_f32_e32 v21, v21
	v_rcp_f32_e32 v22, v22
	v_rcp_f32_e32 v23, v23
	v_pk_fma_f32 v[32:33], v[32:33], v[150:151], v[152:153] op_sel_hi:[1,0,0]
	v_pk_fma_f32 v[34:35], v[34:35], v[150:151], v[152:153] op_sel_hi:[1,0,0]
	v_pk_fma_f32 v[28:29], v[28:29], v[150:151], v[152:153] op_sel_hi:[1,0,0]
	v_pk_fma_f32 v[30:31], v[30:31], v[150:151], v[152:153] op_sel_hi:[1,0,0]
	v_pk_fma_f32 v[24:25], v[24:25], v[150:151], v[152:153] op_sel_hi:[1,0,0]
	v_pk_fma_f32 v[26:27], v[26:27], v[150:151], v[152:153] op_sel_hi:[1,0,0]
	v_pk_fma_f32 v[20:21], v[20:21], v[150:151], v[152:153] op_sel_hi:[1,0,0]
	v_pk_fma_f32 v[22:23], v[22:23], v[150:151], v[152:153] op_sel_hi:[1,0,0]
	v_med3_f32 v32, v32, 1.0, v231
	v_med3_f32 v33, v33, 1.0, v231
	v_med3_f32 v34, v34, 1.0, v231
	v_med3_f32 v35, v35, 1.0, v231
	v_med3_f32 v28, v28, 1.0, v231
	v_med3_f32 v29, v29, 1.0, v231
	v_med3_f32 v30, v30, 1.0, v231
	v_med3_f32 v31, v31, 1.0, v231
	v_med3_f32 v24, v24, 1.0, v231
	v_med3_f32 v25, v25, 1.0, v231
	v_med3_f32 v26, v26, 1.0, v231
	v_med3_f32 v27, v27, 1.0, v231
	v_med3_f32 v20, v20, 1.0, v231
	v_med3_f32 v21, v21, 1.0, v231
	v_med3_f32 v22, v22, 1.0, v231
	v_med3_f32 v23, v23, 1.0, v231
	v_cvt_u32_f32_e32 v32, v32
	v_cvt_u32_f32_e32 v24, v24
	v_cvt_u32_f32_sdwa v32, v33 dst_sel:BYTE_1 dst_unused:UNUSED_PRESERVE src0_sel:DWORD
	v_cvt_u32_f32_sdwa v24, v25 dst_sel:BYTE_1 dst_unused:UNUSED_PRESERVE src0_sel:DWORD
	v_cvt_u32_f32_e32 v33, v28
	v_cvt_u32_f32_e32 v25, v20
	v_cvt_u32_f32_sdwa v32, v34 dst_sel:BYTE_2 dst_unused:UNUSED_PRESERVE src0_sel:DWORD
	v_cvt_u32_f32_sdwa v24, v26 dst_sel:BYTE_2 dst_unused:UNUSED_PRESERVE src0_sel:DWORD
	v_cvt_u32_f32_sdwa v33, v29 dst_sel:BYTE_1 dst_unused:UNUSED_PRESERVE src0_sel:DWORD
	v_cvt_u32_f32_sdwa v25, v21 dst_sel:BYTE_1 dst_unused:UNUSED_PRESERVE src0_sel:DWORD
	v_cvt_u32_f32_sdwa v32, v35 dst_sel:BYTE_3 dst_unused:UNUSED_PRESERVE src0_sel:DWORD
	v_cvt_u32_f32_sdwa v24, v27 dst_sel:BYTE_3 dst_unused:UNUSED_PRESERVE src0_sel:DWORD
	v_cvt_u32_f32_sdwa v33, v30 dst_sel:BYTE_2 dst_unused:UNUSED_PRESERVE src0_sel:DWORD
	v_cvt_u32_f32_sdwa v25, v22 dst_sel:BYTE_2 dst_unused:UNUSED_PRESERVE src0_sel:DWORD
	v_cvt_u32_f32_sdwa v33, v31 dst_sel:BYTE_3 dst_unused:UNUSED_PRESERVE src0_sel:DWORD
	v_cvt_u32_f32_sdwa v25, v23 dst_sel:BYTE_3 dst_unused:UNUSED_PRESERVE src0_sel:DWORD
	s_nop 0
	global_store_dwordx2 v[148:149], v[32:33], off offset:2048 nt
	global_store_dwordx2 v[148:149], v[24:25], off offset:2560 nt
	v_pk_mul_f32 v[16:17], v[16:17], v[162:163] op_sel_hi:[1,0]
	v_pk_mul_f32 v[18:19], v[18:19], v[162:163] op_sel_hi:[1,0]
	v_pk_mul_f32 v[12:13], v[12:13], v[162:163] op_sel_hi:[1,0]
	v_pk_mul_f32 v[14:15], v[14:15], v[162:163] op_sel_hi:[1,0]
	v_pk_mul_f32 v[8:9], v[8:9], v[162:163] op_sel_hi:[1,0]
	v_pk_mul_f32 v[10:11], v[10:11], v[162:163] op_sel_hi:[1,0]
	v_pk_mul_f32 v[4:5], v[4:5], v[162:163] op_sel_hi:[1,0]
	v_pk_mul_f32 v[6:7], v[6:7], v[162:163] op_sel_hi:[1,0]
;     template <int ACT, int AUX> __device__ __forceinline__ void run(const f32x4 (&acc)[2][2][4][2], const Unit& uu, int wr, int wc, int fr, int fq) const {
;     ...
;                 for (int bj = 0; bj < 2; ++bj) { f32x4 v0 = acc[ai][bj][m][0] * rs, v1 = acc[ai][bj][m][1] * rs;
; #pragma unroll
;                     for (int j = 0; j < 4; ++j) { v0[j] = act_f<ACT>(v0[j]); v1[j] = act_f<ACT>(v1[j]); }
;                     if (AUX == 4) {
;                         unsigned q[8];
; #pragma unroll
;                         for (int j = 0; j < 4; ++j) { q[j] = (unsigned)fminf(fmaxf(fmaf(v0[j], 255.0f, 0.5f), 1.0f), 255.0f); q[4 + j] = (unsigned)fminf(fmaxf(fmaf(v1[j], 255.0f, 0.5f), 1.0f), 255.0f); }
;                         u32x2 w8; w8.x = q[0] | (q[1] << 8) | (q[2] << 16) | (q[3] << 24); w8.y = q[4] | (q[5] << 8) | (q[6] << 16) | (q[7] << 24);
;                         __builtin_nontemporal_store(w8, (u32x2*)(g8 + ((size_t)((u.pn - 52) >> 4) * cfg::MT + r) * cfg::DM + ((u.pn - 52) & 15) * BM + wc * 32 + 8 * fq + bj * HALF));
	v_exp_f32_e32 v16, v16
	v_exp_f32_e32 v17, v17
	v_exp_f32_e32 v18, v18
	v_exp_f32_e32 v19, v19
	v_exp_f32_e32 v12, v12
	v_exp_f32_e32 v13, v13
	v_exp_f32_e32 v14, v14
	v_exp_f32_e32 v15, v15
	v_exp_f32_e32 v8, v8
	v_exp_f32_e32 v9, v9
	v_exp_f32_e32 v10, v10
	v_exp_f32_e32 v11, v11
	v_exp_f32_e32 v4, v4
	v_exp_f32_e32 v5, v5
	v_exp_f32_e32 v6, v6
	v_exp_f32_e32 v7, v7
	v_pk_add_f32 v[16:17], v[16:17], v[146:147] op_sel_hi:[1,0]
	v_pk_add_f32 v[18:19], v[18:19], v[146:147] op_sel_hi:[1,0]
	v_pk_add_f32 v[12:13], v[12:13], v[146:147] op_sel_hi:[1,0]
	v_pk_add_f32 v[14:15], v[14:15], v[146:147] op_sel_hi:[1,0]
	v_pk_add_f32 v[8:9], v[8:9], v[146:147] op_sel_hi:[1,0]
	v_pk_add_f32 v[10:11], v[10:11], v[146:147] op_sel_hi:[1,0]
	v_pk_add_f32 v[4:5], v[4:5], v[146:147] op_sel_hi:[1,0]
	v_pk_add_f32 v[6:7], v[6:7], v[146:147] op_sel_hi:[1,0]
	v_rcp_f32_e32 v16, v16
	v_rcp_f32_e32 v17, v17
	v_rcp_f32_e32 v18, v18
	v_rcp_f32_e32 v19, v19
	v_rcp_f32_e32 v12, v12
	v_rcp_f32_e32 v13, v13
	v_rcp_f32_e32 v14, v14
	v_rcp_f32_e32 v15, v15
	v_rcp_f32_e32 v8, v8
	v_rcp_f32_e32 v9, v9
	v_rcp_f32_e32 v10, v10
	v_rcp_f32_e32 v11, v11
	v_rcp_f32_e32 v4, v4
	v_rcp_f32_e32 v5, v5
	v_rcp_f32_e32 v6, v6
	v_rcp_f32_e32 v7, v7
	v_pk_fma_f32 v[16:17], v[16:17], v[150:151], v[152:153] op_sel_hi:[1,0,0]
	v_pk_fma_f32 v[18:19], v[18:19], v[150:151], v[152:153] op_sel_hi:[1,0,0]
	v_pk_fma_f32 v[12:13], v[12:13], v[150:151], v[152:153] op_sel_hi:[1,0,0]
	v_pk_fma_f32 v[14:15], v[14:15], v[150:151], v[152:153] op_sel_hi:[1,0,0]
	v_pk_fma_f32 v[8:9], v[8:9], v[150:151], v[152:153] op_sel_hi:[1,0,0]
	v_pk_fma_f32 v[10:11], v[10:11], v[150:151], v[152:153] op_sel_hi:[1,0,0]
	v_pk_fma_f32 v[4:5], v[4:5], v[150:151], v[152:153] op_sel_hi:[1,0,0]
	v_pk_fma_f32 v[6:7], v[6:7], v[150:151], v[152:153] op_sel_hi:[1,0,0]
	v_med3_f32 v16, v16, 1.0, v231
	v_med3_f32 v17, v17, 1.0, v231
	v_med3_f32 v18, v18, 1.0, v231
	v_med3_f32 v19, v19, 1.0, v231
	v_med3_f32 v12, v12, 1.0, v231
	v_med3_f32 v13, v13, 1.0, v231
	v_med3_f32 v14, v14, 1.0, v231
	v_med3_f32 v15, v15, 1.0, v231
	v_med3_f32 v8, v8, 1.0, v231
	v_med3_f32 v9, v9, 1.0, v231
	v_med3_f32 v10, v10, 1.0, v231
	v_med3_f32 v11, v11, 1.0, v231
	v_med3_f32 v4, v4, 1.0, v231
	v_med3_f32 v5, v5, 1.0, v231
	v_med3_f32 v6, v6, 1.0, v231
	v_med3_f32 v7, v7, 1.0, v231
	v_cvt_u32_f32_e32 v16, v16
	v_cvt_u32_f32_e32 v8, v8
	v_cvt_u32_f32_sdwa v16, v17 dst_sel:BYTE_1 dst_unused:UNUSED_PRESERVE src0_sel:DWORD
	v_cvt_u32_f32_sdwa v8, v9 dst_sel:BYTE_1 dst_unused:UNUSED_PRESERVE src0_sel:DWORD
	v_cvt_u32_f32_e32 v17, v12
	v_cvt_u32_f32_e32 v9, v4
	v_cvt_u32_f32_sdwa v16, v18 dst_sel:BYTE_2 dst_unused:UNUSED_PRESERVE src0_sel:DWORD
	v_cvt_u32_f32_sdwa v8, v10 dst_sel:BYTE_2 dst_unused:UNUSED_PRESERVE src0_sel:DWORD
	v_cvt_u32_f32_sdwa v17, v13 dst_sel:BYTE_1 dst_unused:UNUSED_PRESERVE src0_sel:DWORD
	v_cvt_u32_f32_sdwa v9, v5 dst_sel:BYTE_1 dst_unused:UNUSED_PRESERVE src0_sel:DWORD
	v_cvt_u32_f32_sdwa v16, v19 dst_sel:BYTE_3 dst_unused:UNUSED_PRESERVE src0_sel:DWORD
	v_cvt_u32_f32_sdwa v8, v11 dst_sel:BYTE_3 dst_unused:UNUSED_PRESERVE src0_sel:DWORD
	v_cvt_u32_f32_sdwa v17, v14 dst_sel:BYTE_2 dst_unused:UNUSED_PRESERVE src0_sel:DWORD
	v_cvt_u32_f32_sdwa v9, v6 dst_sel:BYTE_2 dst_unused:UNUSED_PRESERVE src0_sel:DWORD
	v_cvt_u32_f32_sdwa v17, v15 dst_sel:BYTE_3 dst_unused:UNUSED_PRESERVE src0_sel:DWORD
	v_cvt_u32_f32_sdwa v9, v7 dst_sel:BYTE_3 dst_unused:UNUSED_PRESERVE src0_sel:DWORD
	s_nop 0
	global_store_dwordx2 v[148:149], v[16:17], off offset:3072 nt
	global_store_dwordx2 v[148:149], v[8:9], off offset:3584 nt
	s_mov_b32 s2, 0xb0000
	s_mov_b64 s[12:13], 0xb0000

;     template <int ACT, int AUX> __device__ __forceinline__ void run(const f32x4 (&acc)[2][2][4][2], const Unit& uu, int wr, int wc, int fr, int fq) const {
;     ...
;         for (int i = 0; i < 8; ++i) rsv[i] = ss[row0 + (i >> 2) * HALF + (i & 3) * 16];
;         asm volatile("" ::: "memory");
; #pragma unroll
;         for (int i = 0; i < 8; ++i) rsv[i] = __builtin_amdgcn_rsqf(rsv[i] * (1.0f / cfg::DM) + cfg::RMS_EPS);
;     ...
;             for (int m = 0; m < 4; ++m) { const int r = row0 + ai * HALF + m * 16; const float rs = rsv[ai * 4 + m];
;                 bf16_t* rowp = O + (size_t)r * cfg::NC + col0; float s1 = 0.f, s2 = 0.f;
; #pragma unroll
;                 for (int bj = 0; bj < 2; ++bj) { f32x4 v0 = acc[ai][bj][m][0] * rs, v1 = acc[ai][bj][m][1] * rs;
; #pragma unroll
;                     for (int j = 0; j < 4; ++j) { v0[j] = act_f<ACT>(v0[j]); v1[j] = act_f<ACT>(v1[j]); }
;                     if (AUX == 4) {
;                         unsigned q[8];
; #pragma unroll
;                         for (int j = 0; j < 4; ++j) { q[j] = (unsigned)fminf(fmaxf(fmaf(v0[j], 255.0f, 0.5f), 1.0f), 255.0f); q[4 + j] = (unsigned)fminf(fmaxf(fmaf(v1[j], 255.0f, 0.5f), 1.0f), 255.0f); }
;                         u32x2 w8; w8.x = q[0] | (q[1] << 8) | (q[2] << 16) | (q[3] << 24); w8.y = q[4] | (q[5] << 8) | (q[6] << 16) | (q[7] << 24);
;                         __builtin_nontemporal_store(w8, (u32x2*)(g8 + ((size_t)((u.pn - 52) >> 4) * cfg::MT + r) * cfg::DM + ((u.pn - 52) & 15) * BM + wc * 32 + 8 * fq + bj * HALF));
;                     } else {
;                     u32x4 w; w.x = cvt_pk_bf16(v0[0], v0[1]); w.y = cvt_pk_bf16(v0[2], v0[3]); w.z = cvt_pk_bf16(v1[0], v1[1]); w.w = cvt_pk_bf16(v1[2], v1[3]);
;                     __builtin_nontemporal_store(w, (u32x4*)(rowp + bj * HALF)); }
;                     if (AUX == 1) {
; #pragma unroll
;                         for (int j = 0; j < 4; ++j) { cs[bj][j] += v0[j]; cs[bj][4 + j] += v1[j]; } }
;                     if (AUX == 2) { float p = (v0[0] * v0[0] + v0[1] * v0[1]) + (v0[2] * v0[2] + v0[3] * v0[3]) + (v1[0] * v1[0] + v1[1] * v1[1]) + (v1[2] * v1[2] + v1[3] * v1[3]);
;                         p += __shfl_xor(p, 16); p += __shfl_xor(p, 32); mx[ai][bj] = fmaxf(mx[ai][bj], p); }
;                     if (AUX == 3) { s1 += (v0[0] + v0[1]) + (v0[2] + v0[3]) + (v1[0] + v1[1]) + (v1[2] + v1[3]);
.LBB0_170:
	s_and_b64 vcc, exec, s[12:13]
	s_cbranch_vccz .LBB0_188
	v_lshl_add_u32 v146, s2, 8, v1
	v_ashrrev_i32_e32 v147, 31, v146
	v_lshl_add_u64 v[148:149], v[146:147], 2, s[22:23]
	v_mov_b32_e32 v150, v218
	v_mov_b32_e32 v182, v220
	v_mov_b32_e32 v198, v224
	v_mov_b32_e32 v197, v226
	v_mov_b32_e32 v189, v228
	v_mov_b32_e32 v188, v230
	v_mov_b32_e32 v187, v240
	v_mov_b32_e32 v186, v250
	v_and_b32_e32 v151, 64, v229
	v_add_u32_e32 v151, 64, v151
	s_lshl_b32 s12, s1, 2
	s_addk_i32 s12, 0xff70
	s_ashr_i32 s13, s12, 31
	s_or_b64 s[52:53], s[12:13], s[28:29]
	s_mov_b32 s12, 0xe800
	v_fmamk_f32 v148, v150, 0x39800000, v221
	v_rsq_f32_e32 v160, v148
	v_xor_b32_e32 v150, 16, v229
	v_cmp_lt_i32_e32 vcc, v150, v151
	v_lshl_or_b32 v148, s1, 8, v191
	v_pk_mul_f32 v[162:163], v[124:125], v[160:161] op_sel_hi:[1,0]
	v_pk_mul_f32 v[164:165], v[128:129], v[160:161] op_sel_hi:[1,0]
	v_mul_f32_e32 v153, 0x3d372713, v162
	v_mul_f32_e32 v153, v162, v153
	v_fma_f32 v153, v162, v153, v162
	v_mul_f32_e32 v153, 0x3fcc422a, v153
	v_mul_f32_e32 v153, 0xbfb8aa3b, v153
	v_exp_f32_e32 v153, v153
	v_pk_mul_f32 v[158:159], v[130:131], v[160:161] op_sel_hi:[1,0]
	v_pk_mul_f32 v[156:157], v[126:127], v[160:161] op_sel_hi:[1,0]
	v_pk_mul_f32 v[200:201], v[120:121], v[160:161] op_sel_hi:[1,0]
	v_add_f32_e32 v153, 1.0, v153
	v_rcp_f32_e32 v154, v153
	v_mul_f32_e32 v153, 0x3d372713, v165
	v_mul_f32_e32 v153, v165, v153
	v_fma_f32 v153, v165, v153, v165
	v_mul_f32_e32 v153, 0x3fcc422a, v153
	v_mul_f32_e32 v153, 0xbfb8aa3b, v153
	v_exp_f32_e32 v153, v153
	v_pk_mul_f32 v[202:203], v[116:117], v[160:161] op_sel_hi:[1,0]
	v_pk_mul_f32 v[178:179], v[122:123], v[160:161] op_sel_hi:[1,0]
	v_pk_mul_f32 v[176:177], v[118:119], v[160:161] op_sel_hi:[1,0]
	v_add_f32_e32 v153, 1.0, v153
	v_rcp_f32_e32 v170, v153
	v_mul_f32_e32 v153, 0x3d372713, v163
	v_mul_f32_e32 v153, v163, v153
	v_fma_f32 v153, v163, v153, v163
	v_mul_f32_e32 v153, 0x3fcc422a, v153
	v_mul_f32_e32 v153, 0xbfb8aa3b, v153
	v_exp_f32_e32 v153, v153
	v_mul_f32_e32 v155, 0x3d372713, v176
	v_mul_f32_e32 v155, v176, v155
	v_fma_f32 v155, v176, v155, v176
	v_add_f32_e32 v153, 1.0, v153
	v_rcp_f32_e32 v172, v153
	v_mul_f32_e32 v153, 0x3d372713, v158
	v_mul_f32_e32 v153, v158, v153
	v_fma_f32 v153, v158, v153, v158
	v_mul_f32_e32 v153, 0x3fcc422a, v153
	v_mul_f32_e32 v153, 0xbfb8aa3b, v153
	v_exp_f32_e32 v153, v153
	v_mul_f32_e32 v155, 0x3fcc422a, v155
	v_mul_f32_e32 v155, 0xbfb8aa3b, v155
	v_exp_f32_e32 v155, v155
	v_add_f32_e32 v153, 1.0, v153
	v_rcp_f32_e32 v166, v153
	v_mul_f32_e32 v153, 0x3d372713, v156
	v_mul_f32_e32 v153, v156, v153
	v_fma_f32 v153, v156, v153, v156
	v_mul_f32_e32 v153, 0x3fcc422a, v153
	v_mul_f32_e32 v153, 0xbfb8aa3b, v153
	v_exp_f32_e32 v153, v153
	v_add_f32_e32 v155, 1.0, v155
	v_rcp_f32_e32 v208, v155
	v_mul_f32_e32 v155, 0x3d372713, v179
	v_add_f32_e32 v153, 1.0, v153
	v_rcp_f32_e32 v168, v153
	v_mul_f32_e32 v153, 0x3d372713, v159
	v_mul_f32_e32 v153, v159, v153
	v_fma_f32 v153, v159, v153, v159
	v_mul_f32_e32 v153, 0x3fcc422a, v153
	v_mul_f32_e32 v153, 0xbfb8aa3b, v153
	v_exp_f32_e32 v153, v153
	v_mul_f32_e32 v155, v179, v155
	v_fma_f32 v155, v179, v155, v179
	v_mul_f32_e32 v152, 0x3d372713, v164
	v_add_f32_e32 v153, 1.0, v153
	v_rcp_f32_e32 v174, v153
	v_mul_f32_e32 v153, 0x3d372713, v157
	v_mul_f32_e32 v153, v157, v153
	v_fma_f32 v153, v157, v153, v157
	v_mul_f32_e32 v153, 0x3fcc422a, v153
	v_mul_f32_e32 v153, 0xbfb8aa3b, v153
	v_exp_f32_e32 v153, v153
	v_mul_f32_e32 v155, 0x3fcc422a, v155
	v_mul_f32_e32 v152, v164, v152
	v_mul_f32_e32 v155, 0xbfb8aa3b, v155
	v_add_f32_e32 v153, 1.0, v153
	v_rcp_f32_e32 v194, v153
	v_mul_f32_e32 v153, 0x3d372713, v200
	v_mul_f32_e32 v153, v200, v153
	v_fma_f32 v153, v200, v153, v200
	v_mul_f32_e32 v153, 0x3fcc422a, v153
	v_mul_f32_e32 v153, 0xbfb8aa3b, v153
	v_exp_f32_e32 v153, v153
	v_fma_f32 v152, v164, v152, v164
	v_exp_f32_e32 v155, v155
	v_mul_f32_e32 v152, 0x3fcc422a, v152
	v_add_f32_e32 v153, 1.0, v153
	v_rcp_f32_e32 v160, v153
	v_mul_f32_e32 v153, 0x3d372713, v202
	v_mul_f32_e32 v153, v202, v153
	v_fma_f32 v153, v202, v153, v202
	v_mul_f32_e32 v153, 0x3fcc422a, v153
	v_mul_f32_e32 v153, 0xbfb8aa3b, v153
	v_exp_f32_e32 v153, v153
	v_mul_f32_e32 v152, 0xbfb8aa3b, v152
	v_exp_f32_e32 v152, v152
	v_add_f32_e32 v155, 1.0, v155
	v_add_f32_e32 v153, 1.0, v153
	v_rcp_f32_e32 v180, v153
	v_mul_f32_e32 v153, 0x3d372713, v201
	v_mul_f32_e32 v153, v201, v153
	v_fma_f32 v153, v201, v153, v201
	v_mul_f32_e32 v153, 0x3fcc422a, v153
	v_mul_f32_e32 v153, 0xbfb8aa3b, v153
	v_exp_f32_e32 v153, v153
	v_rcp_f32_e32 v167, v155
	v_mul_f32_e32 v155, 0x3d372713, v177
	v_mul_f32_e32 v155, v177, v155
	v_add_f32_e32 v153, 1.0, v153
	v_rcp_f32_e32 v204, v153
	v_mul_f32_e32 v153, 0x3d372713, v203
	v_mul_f32_e32 v153, v203, v153
	v_fma_f32 v153, v203, v153, v203
	v_mul_f32_e32 v153, 0x3fcc422a, v153
	v_mul_f32_e32 v153, 0xbfb8aa3b, v153
	v_exp_f32_e32 v153, v153
	v_add_f32_e32 v152, 1.0, v152
	v_fma_f32 v155, v177, v155, v177
	v_rcp_f32_e32 v152, v152
	v_add_f32_e32 v153, 1.0, v153
	v_rcp_f32_e32 v206, v153
	v_mul_f32_e32 v153, 0x3d372713, v178
;     template <int ACT, int AUX> __device__ __forceinline__ void run(const f32x4 (&acc)[2][2][4][2], const Unit& uu, int wr, int wc, int fr, int fq) const {
;     ...
;                     if (AUX == 2) { float p = (v0[0] * v0[0] + v0[1] * v0[1]) + (v0[2] * v0[2] + v0[3] * v0[3]) + (v1[0] * v1[0] + v1[1] * v1[1]) + (v1[2] * v1[2] + v1[3] * v1[3]);
;                         p += __shfl_xor(p, 16); p += __shfl_xor(p, 32); mx[ai][bj] = fmaxf(mx[ai][bj], p); }
;                     if (AUX == 3) { s1 += (v0[0] + v0[1]) + (v0[2] + v0[3]) + (v1[0] + v1[1]) + (v1[2] + v1[3]);
;                         s2 += (v0[0] * v0[0] + v0[1] * v0[1]) + (v0[2] * v0[2] + v0[3] * v0[3]) + (v1[0] * v1[0] + v1[1] * v1[1]) + (v1[2] * v1[2] + v1[3] * v1[3]); } }
;                 if (AUX == 3) { s1 += __shfl_xor(s1, 16); s1 += __shfl_xor(s1, 32); s2 += __shfl_xor(s2, 16); s2 += __shfl_xor(s2, 32);
;                     if (fq == 0) *(float2*)(st2 + ((size_t)r * 16 + (u.pn - 36) * 4 + wc) * 2) = make_float2(s1, s2); } }
	v_mul_f32_e32 v153, v178, v153
	v_fma_f32 v153, v178, v153, v178
	v_mul_f32_e32 v153, 0x3fcc422a, v153
	v_mul_f32_e32 v153, 0xbfb8aa3b, v153
	v_exp_f32_e32 v153, v153
	v_mul_f32_e32 v155, 0x3fcc422a, v155
	v_mul_f32_e32 v155, 0xbfb8aa3b, v155
	v_exp_f32_e32 v155, v155
	v_add_f32_e32 v153, 1.0, v153
	v_rcp_f32_e32 v153, v153
	v_mov_b32_e32 v212, v164
	v_mov_b32_e32 v213, v178
	v_pk_mov_b32 v[164:165], v[164:165], v[178:179] op_sel:[1,0]
	v_mov_b32_e32 v171, v153
	v_pk_mul_f32 v[214:215], v[212:213], v[152:153]
	v_pk_mul_f32 v[164:165], v[164:165], v[170:171]
	v_mov_b32_e32 v216, v200
	v_mov_b32_e32 v217, v214
	v_mov_b32_e32 v161, v214
	v_mov_b32_e32 v170, v201
	v_mov_b32_e32 v171, v164
	v_mov_b32_e32 v205, v164
	v_add_f32_e32 v155, 1.0, v155
	v_pk_mul_f32 v[222:223], v[216:217], v[160:161]
	v_pk_mul_f32 v[170:171], v[170:171], v[204:205]
	v_cndmask_b32_e32 v150, v229, v150, vcc
	v_rcp_f32_e32 v210, v155
	v_mov_b32_e32 v232, v162
	v_mov_b32_e32 v233, v222
	v_mov_b32_e32 v155, v222
	v_mov_b32_e32 v162, v163
	v_mov_b32_e32 v163, v170
	v_mov_b32_e32 v173, v170
	v_lshlrev_b32_e32 v185, 2, v150
	v_xor_b32_e32 v150, 32, v229
	v_pk_mul_f32 v[234:235], v[232:233], v[154:155]
	v_pk_mul_f32 v[162:163], v[162:163], v[172:173]
	v_mov_b32_e32 v172, v158
	v_mov_b32_e32 v158, v159
	v_mov_b32_e32 v159, v179
	v_mov_b32_e32 v175, v167
	v_cmp_lt_i32_e32 vcc, v150, v151
	v_mov_b32_e32 v204, v202
	v_mov_b32_e32 v205, v234
	v_mov_b32_e32 v181, v234
	v_pk_mul_f32 v[174:175], v[158:159], v[174:175]
	v_mov_b32_e32 v158, v203
	v_mov_b32_e32 v159, v162
	v_mov_b32_e32 v207, v162
	v_cndmask_b32_e32 v150, v229, v150, vcc
	v_pk_mul_f32 v[236:237], v[204:205], v[180:181]
	v_pk_mul_f32 v[202:203], v[158:159], v[206:207]
	v_lshlrev_b32_e32 v184, 2, v150
	v_mov_b64_e32 v[150:151], s[20:21]
	v_mov_b32_e32 v173, v179
	v_mov_b32_e32 v238, v156
	v_mov_b32_e32 v239, v236
	v_mov_b32_e32 v169, v236
	v_mov_b32_e32 v156, v157
	v_mov_b32_e32 v157, v202
	v_mov_b32_e32 v195, v202
	v_ashrrev_i32_e32 v149, 31, v148
	v_mad_i64_i32 v[150:151], s[12:13], v146, s12, v[150:151]
	v_pk_mul_f32 v[200:201], v[172:173], v[166:167]
	v_pk_mul_f32 v[244:245], v[238:239], v[168:169]
	v_pk_mul_f32 v[194:195], v[156:157], v[194:195]
	v_lshl_add_u64 v[150:151], v[148:149], 1, v[150:151]
	v_cvt_pk_bf16_f32 v156, v214, v164
	v_cvt_pk_bf16_f32 v157, v200, v174
	v_cvt_pk_bf16_f32 v158, v234, v162
	v_cvt_pk_bf16_f32 v159, v244, v194
	global_store_dwordx4 v[150:151], v[156:159], off nt
	v_pk_mov_b32 v[234:235], v[152:153], v[200:201] op_sel:[1,0]
	v_mov_b32_e32 v209, v244
	v_mov_b32_e32 v156, v176
	v_mov_b32_e32 v157, v244
	v_mov_b32_e32 v206, v178
	v_pk_mul_f32 v[158:159], v[178:179], v[234:235]
	v_pk_mul_f32 v[208:209], v[156:157], v[208:209]
	v_mov_b32_e32 v156, v179
	v_mov_b32_e32 v157, v174
	v_pk_mov_b32 v[178:179], v[166:167], v[174:175] op_sel:[1,0]
	v_mov_b32_e32 v211, v194
	v_pk_mul_f32 v[178:179], v[156:157], v[178:179]
	v_mov_b32_e32 v244, v177
	v_pk_mul_f32 v[176:177], v[176:177], v[210:211] op_sel:[1,0] op_sel_hi:[0,1]
	v_mov_b32_e32 v207, v200
	v_cvt_pk_bf16_f32 v156, v222, v170
	v_cvt_pk_bf16_f32 v157, v158, v178
	v_cvt_pk_bf16_f32 v158, v236, v202
	v_cvt_pk_bf16_f32 v159, v208, v176
	global_store_dwordx4 v[150:151], v[156:159], off offset:256 nt
	v_pk_fma_f32 v[150:151], v[216:217], v[160:161], v[170:171]
	v_mov_b32_e32 v245, v194
	v_pk_fma_f32 v[156:157], v[206:207], v[234:235], v[178:179]
	v_pk_fma_f32 v[152:153], v[212:213], v[152:153], v[164:165]
	v_pk_add_f32 v[150:151], v[150:151], v[156:157]
	v_pk_fma_f32 v[156:157], v[204:205], v[180:181], v[202:203]
	v_pk_mul_f32 v[158:159], v[200:201], v[174:175]
	v_pk_add_f32 v[150:151], v[156:157], v[150:151]
	v_pk_fma_f32 v[156:157], v[244:245], v[210:211], v[208:209]
	v_pk_fma_f32 v[154:155], v[232:233], v[154:155], v[162:163]
	v_pk_add_f32 v[150:151], v[156:157], v[150:151]
	v_pk_mul_f32 v[156:157], v[214:215], v[164:165]
	v_mov_b32_e32 v246, v208
	v_mov_b32_e32 v153, v157
	v_pk_fma_f32 v[156:157], v[172:173], v[166:167], v[174:175]
	v_mov_b32_e32 v247, v176
	v_mov_b32_e32 v157, v159
	v_pk_add_f32 v[152:153], v[152:153], v[156:157]
	s_nop 0
	v_pk_add_f32 v[152:153], v[154:155], v[152:153]
	v_pk_fma_f32 v[154:155], v[238:239], v[168:169], v[194:195]
	s_nop 0
	v_pk_add_f32 v[152:153], v[154:155], v[152:153]
	v_mul_f32_e32 v154, v208, v208
	v_pk_fma_f32 v[154:155], v[246:247], v[246:247], v[154:155] op_sel_hi:[1,1,0]
	s_nop 0
	v_mov_b32_e32 v154, v3
	v_pk_add_f32 v[152:153], v[152:153], v[154:155]
	s_nop 0
	v_pk_add_f32 v[150:151], v[150:151], v[152:153]
	ds_bpermute_b32 v152, v185, v150
	ds_bpermute_b32 v153, v185, v151
	s_waitcnt lgkmcnt(0)
	v_pk_add_f32 v[150:151], v[150:151], v[152:153]
	ds_bpermute_b32 v152, v184, v150
	ds_bpermute_b32 v153, v184, v151
	s_and_saveexec_b64 s[12:13], s[8:9]
	s_cbranch_execz .LBB0_173
	v_lshlrev_b64 v[154:155], 7, v[146:147]
	v_lshl_add_u64 v[154:155], s[24:25], 0, v[154:155]
	v_lshl_add_u64 v[154:155], s[52:53], 3, v[154:155]
	s_waitcnt lgkmcnt(0)
	v_pk_add_f32 v[150:151], v[150:151], v[152:153]
	global_store_dwordx2 v[154:155], v[150:151], off

; __device__ __forceinline__ unsigned cvt_pk_bf16(float lo, float hi) { f32x2_t v = {lo, hi}; bf16x2_t b = __builtin_convertvector(v, bf16x2_t); return __builtin_bit_cast(unsigned, b); }
;     template <int ACT, int AUX> __device__ __forceinline__ void run(const f32x4 (&acc)[2][2][4][2], const Unit& uu, int wr, int wc, int fr, int fq) const {
;     ...
;             for (int m = 0; m < 4; ++m) { const int r = row0 + ai * HALF + m * 16; const float rs = rsv[ai * 4 + m];
;                 bf16_t* rowp = O + (size_t)r * cfg::NC + col0; float s1 = 0.f, s2 = 0.f;
; #pragma unroll
;                 for (int bj = 0; bj < 2; ++bj) { f32x4 v0 = acc[ai][bj][m][0] * rs, v1 = acc[ai][bj][m][1] * rs;
; #pragma unroll
;                     for (int j = 0; j < 4; ++j) { v0[j] = act_f<ACT>(v0[j]); v1[j] = act_f<ACT>(v1[j]); }
;                     if (AUX == 4) {
;                         unsigned q[8];
; #pragma unroll
;                         for (int j = 0; j < 4; ++j) { q[j] = (unsigned)fminf(fmaxf(fmaf(v0[j], 255.0f, 0.5f), 1.0f), 255.0f); q[4 + j] = (unsigned)fminf(fmaxf(fmaf(v1[j], 255.0f, 0.5f), 1.0f), 255.0f); }
;                         u32x2 w8; w8.x = q[0] | (q[1] << 8) | (q[2] << 16) | (q[3] << 24); w8.y = q[4] | (q[5] << 8) | (q[6] << 16) | (q[7] << 24);
;                         __builtin_nontemporal_store(w8, (u32x2*)(g8 + ((size_t)((u.pn - 52) >> 4) * cfg::MT + r) * cfg::DM + ((u.pn - 52) & 15) * BM + wc * 32 + 8 * fq + bj * HALF));
;                     } else {
;                     u32x4 w; w.x = cvt_pk_bf16(v0[0], v0[1]); w.y = cvt_pk_bf16(v0[2], v0[3]); w.z = cvt_pk_bf16(v1[0], v1[1]); w.w = cvt_pk_bf16(v1[2], v1[3]);
;                     __builtin_nontemporal_store(w, (u32x4*)(rowp + bj * HALF)); }
;     __device__ __forceinline__ void operator()(const f32x4 (&acc)[2][2][4][2], const Unit& u, int wr, int wc, int fr, int fq) const {
;         const int seg = (u.pn + pn0) >> 2;
;         if (seg >= 13) run<3, 4>(acc, u, wr, wc, fr, fq);
;         else if (seg == 3 || seg == 7 || seg == 10 || seg == 12) run<1, 0>(acc, u, wr, wc, fr, fq);
;         else if (seg == 8) run<2, 0>(acc, u, wr, wc, fr, fq);
;         else if (seg == 9) run<2, 3>(acc, u, wr, wc, fr, fq);
;         else if (seg == 1) run<0, 1>(acc, u, wr, wc, fr, fq);
;         else if (seg == 5) run<0, 2>(acc, u, wr, wc, fr, fq);
;         else run<0, 0>(acc, u, wr, wc, fr, fq);
.LBB0_189:
	s_and_b64 vcc, exec, s[12:13]
	s_cbranch_vccz .LBB0_207
	s_cmp_gt_i32 s39, 4
	s_mov_b64 s[12:13], -1
	s_cbranch_scc0 .LBB0_205
	s_cmp_gt_i32 s39, 7
	s_cbranch_scc0 .LBB0_193
	v_lshl_add_u32 v148, s2, 8, v1
	v_ashrrev_i32_e32 v149, 31, v148
	s_waitcnt lgkmcnt(0)
	v_lshl_add_u64 v[150:151], v[148:149], 2, s[22:23]
	v_mov_b32_e32 v146, v218
	v_mov_b32_e32 v149, v220
	v_mov_b32_e32 v152, v224
	v_mov_b32_e32 v153, v226
	v_mov_b32_e32 v154, v228
	v_mov_b32_e32 v155, v230
	v_mov_b32_e32 v157, v240
	s_nop 0
	v_mov_b32_e32 v150, v250
	s_mov_b32 s41, 0xe800
	v_add_u32_e32 v147, 0x80, v148
	v_fmamk_f32 v146, v146, 0x39800000, v221
	v_rsq_f32_e32 v168, v146
	v_fmamk_f32 v146, v149, 0x39800000, v221
	v_rsq_f32_e32 v164, v146
	v_fmamk_f32 v146, v152, 0x39800000, v221
	v_pk_mul_f32 v[172:173], v[128:129], v[168:169] op_sel_hi:[1,0]
	v_pk_mul_f32 v[174:175], v[124:125], v[168:169] op_sel_hi:[1,0]
	v_mul_f32_e32 v149, 0x3d372713, v172
	v_mul_f32_e32 v149, v172, v149
	v_fma_f32 v149, v172, v149, v172
	v_mul_f32_e32 v149, 0x3fcc422a, v149
	v_mul_f32_e32 v149, 0xbfb8aa3b, v149
	v_exp_f32_e32 v149, v149
	v_pk_mul_f32 v[178:179], v[130:131], v[168:169] op_sel_hi:[1,0]
	v_pk_mul_f32 v[170:171], v[126:127], v[168:169] op_sel_hi:[1,0]
	v_rsq_f32_e32 v162, v146
	v_add_f32_e32 v149, 1.0, v149
	v_rcp_f32_e32 v176, v149
	v_mul_f32_e32 v149, 0x3d372713, v174
	v_mul_f32_e32 v149, v174, v149
	v_fma_f32 v149, v174, v149, v174
	v_mul_f32_e32 v149, 0x3fcc422a, v149
	v_mul_f32_e32 v149, 0xbfb8aa3b, v149
	v_exp_f32_e32 v149, v149
	v_fmamk_f32 v146, v153, 0x39800000, v221
	v_rsq_f32_e32 v160, v146
	v_fmamk_f32 v146, v154, 0x39800000, v221
	v_add_f32_e32 v149, 1.0, v149
	v_rcp_f32_e32 v180, v149
	v_mul_f32_e32 v149, 0x3d372713, v173
	v_mul_f32_e32 v149, v173, v149
	v_fma_f32 v149, v173, v149, v173
	v_mul_f32_e32 v149, 0x3fcc422a, v149
	v_mul_f32_e32 v149, 0xbfb8aa3b, v149
	v_exp_f32_e32 v149, v149
	v_rsq_f32_e32 v158, v146
	v_fmamk_f32 v146, v155, 0x39800000, v221
	v_rsq_f32_e32 v156, v146
	v_add_f32_e32 v149, 1.0, v149
	v_rcp_f32_e32 v177, v149
	v_mul_f32_e32 v149, 0x3d372713, v175
	v_mul_f32_e32 v149, v175, v149
	v_fma_f32 v149, v175, v149, v175
	v_mul_f32_e32 v149, 0x3fcc422a, v149
	v_mul_f32_e32 v149, 0xbfb8aa3b, v149
	v_exp_f32_e32 v149, v149
	v_pk_mul_f32 v[172:173], v[172:173], v[176:177]
	v_fmamk_f32 v146, v157, 0x39800000, v221
	v_lshl_or_b32 v152, s1, 8, v191
	v_add_f32_e32 v149, 1.0, v149
	v_rcp_f32_e32 v181, v149
	v_mul_f32_e32 v149, 0x3d372713, v178
	v_mul_f32_e32 v149, v178, v149
	v_fma_f32 v149, v178, v149, v178
	v_mul_f32_e32 v149, 0x3fcc422a, v149
	v_mul_f32_e32 v149, 0xbfb8aa3b, v149
	v_exp_f32_e32 v149, v149
	v_pk_mul_f32 v[174:175], v[174:175], v[180:181]
	v_rsq_f32_e32 v154, v146
	v_fmamk_f32 v146, v150, 0x39800000, v221
	v_add_f32_e32 v149, 1.0, v149
	v_rcp_f32_e32 v180, v149
	v_mul_f32_e32 v149, 0x3d372713, v170
	v_mul_f32_e32 v149, v170, v149
	v_fma_f32 v149, v170, v149, v170
	v_mul_f32_e32 v149, 0x3fcc422a, v149
	v_mul_f32_e32 v149, 0xbfb8aa3b, v149
	v_exp_f32_e32 v149, v149
	v_ashrrev_i32_e32 v153, 31, v152
	v_mov_b64_e32 v[150:151], s[20:21]
	v_mad_i64_i32 v[166:167], s[12:13], v148, s41, v[150:151]
	v_add_f32_e32 v149, 1.0, v149
	v_rcp_f32_e32 v176, v149
	v_mul_f32_e32 v149, 0x3d372713, v179
	v_mul_f32_e32 v149, v179, v149
	v_fma_f32 v149, v179, v149, v179
	v_mul_f32_e32 v149, 0x3fcc422a, v149
	v_mul_f32_e32 v149, 0xbfb8aa3b, v149
	v_exp_f32_e32 v149, v149
	v_lshlrev_b64 v[152:153], 1, v[152:153]
	v_lshl_add_u64 v[166:167], v[166:167], 0, v[152:153]
	v_rsq_f32_e32 v146, v146
	v_add_f32_e32 v149, 1.0, v149
	v_rcp_f32_e32 v181, v149
	v_mul_f32_e32 v149, 0x3d372713, v171
	v_mul_f32_e32 v149, v171, v149
	v_fma_f32 v149, v171, v149, v171
	v_mul_f32_e32 v149, 0x3fcc422a, v149
	v_mul_f32_e32 v149, 0xbfb8aa3b, v149
	v_exp_f32_e32 v149, v149
	v_pk_mul_f32 v[178:179], v[178:179], v[180:181]
	v_add_f32_e32 v149, 1.0, v149
	v_rcp_f32_e32 v177, v149
	s_nop 0
	v_pk_mul_f32 v[176:177], v[170:171], v[176:177]
	v_cvt_pk_bf16_f32 v170, v172, v173
	v_cvt_pk_bf16_f32 v171, v178, v179
	v_cvt_pk_bf16_f32 v172, v174, v175
	v_cvt_pk_bf16_f32 v173, v176, v177
	global_store_dwordx4 v[166:167], v[170:173], off nt
	v_pk_mul_f32 v[174:175], v[118:119], v[168:169] op_sel_hi:[1,0]
	s_nop 0
	v_pk_mul_f32 v[172:173], v[120:121], v[168:169] op_sel_hi:[1,0]
	v_pk_mul_f32 v[170:171], v[122:123], v[168:169] op_sel_hi:[1,0]
	v_mul_f32_e32 v149, 0x3d372713, v172
	v_mul_f32_e32 v149, v172, v149
	v_fma_f32 v149, v172, v149, v172
	v_mul_f32_e32 v149, 0x3fcc422a, v149
	v_mul_f32_e32 v149, 0xbfb8aa3b, v149
	v_exp_f32_e32 v149, v149
	v_pk_mul_f32 v[168:169], v[116:117], v[168:169] op_sel_hi:[1,0]
	v_add_f32_e32 v149, 1.0, v149
	v_rcp_f32_e32 v176, v149
	v_mul_f32_e32 v149, 0x3d372713, v168
	v_mul_f32_e32 v149, v168, v149
	v_fma_f32 v149, v168, v149, v168
	v_mul_f32_e32 v149, 0x3fcc422a, v149
	v_mul_f32_e32 v149, 0xbfb8aa3b, v149
	v_exp_f32_e32 v149, v149
	s_nop 0
	v_add_f32_e32 v149, 1.0, v149
	v_rcp_f32_e32 v178, v149
	v_mul_f32_e32 v149, 0x3d372713, v173
	v_mul_f32_e32 v149, v173, v149
	v_fma_f32 v149, v173, v149, v173
	v_mul_f32_e32 v149, 0x3fcc422a, v149
	v_mul_f32_e32 v149, 0xbfb8aa3b, v149
	v_exp_f32_e32 v149, v149
	s_nop 0
	v_add_f32_e32 v149, 1.0, v149
	v_rcp_f32_e32 v177, v149
	v_mul_f32_e32 v149, 0x3d372713, v169
	v_mul_f32_e32 v149, v169, v149
	v_fma_f32 v149, v169, v149, v169
	v_mul_f32_e32 v149, 0x3fcc422a, v149
	v_mul_f32_e32 v149, 0xbfb8aa3b, v149
	v_exp_f32_e32 v149, v149
	v_pk_mul_f32 v[172:173], v[172:173], v[176:177]
	v_add_f32_e32 v149, 1.0, v149
	v_rcp_f32_e32 v179, v149
	v_mul_f32_e32 v149, 0x3d372713, v170
	v_mul_f32_e32 v149, v170, v149
; __device__ __forceinline__ unsigned cvt_pk_bf16(float lo, float hi) { f32x2_t v = {lo, hi}; bf16x2_t b = __builtin_convertvector(v, bf16x2_t); return __builtin_bit_cast(unsigned, b); }
;     template <int ACT, int AUX> __device__ __forceinline__ void run(const f32x4 (&acc)[2][2][4][2], const Unit& uu, int wr, int wc, int fr, int fq) const {
;     ...
;             for (int m = 0; m < 4; ++m) { const int r = row0 + ai * HALF + m * 16; const float rs = rsv[ai * 4 + m];
;                 bf16_t* rowp = O + (size_t)r * cfg::NC + col0; float s1 = 0.f, s2 = 0.f;
; #pragma unroll
;                 for (int bj = 0; bj < 2; ++bj) { f32x4 v0 = acc[ai][bj][m][0] * rs, v1 = acc[ai][bj][m][1] * rs;
; #pragma unroll
;                     for (int j = 0; j < 4; ++j) { v0[j] = act_f<ACT>(v0[j]); v1[j] = act_f<ACT>(v1[j]); }
;                     if (AUX == 4) {
;                         unsigned q[8];
; #pragma unroll
;                         for (int j = 0; j < 4; ++j) { q[j] = (unsigned)fminf(fmaxf(fmaf(v0[j], 255.0f, 0.5f), 1.0f), 255.0f); q[4 + j] = (unsigned)fminf(fmaxf(fmaf(v1[j], 255.0f, 0.5f), 1.0f), 255.0f); }
;                         u32x2 w8; w8.x = q[0] | (q[1] << 8) | (q[2] << 16) | (q[3] << 24); w8.y = q[4] | (q[5] << 8) | (q[6] << 16) | (q[7] << 24);
;                         __builtin_nontemporal_store(w8, (u32x2*)(g8 + ((size_t)((u.pn - 52) >> 4) * cfg::MT + r) * cfg::DM + ((u.pn - 52) & 15) * BM + wc * 32 + 8 * fq + bj * HALF));
;                     } else {
;                     u32x4 w; w.x = cvt_pk_bf16(v0[0], v0[1]); w.y = cvt_pk_bf16(v0[2], v0[3]); w.z = cvt_pk_bf16(v1[0], v1[1]); w.w = cvt_pk_bf16(v1[2], v1[3]);
;                     __builtin_nontemporal_store(w, (u32x4*)(rowp + bj * HALF)); }
	v_fma_f32 v149, v170, v149, v170
	v_mul_f32_e32 v149, 0x3fcc422a, v149
	v_mul_f32_e32 v149, 0xbfb8aa3b, v149
	v_exp_f32_e32 v149, v149
	v_pk_mul_f32 v[176:177], v[168:169], v[178:179]
	v_add_f32_e32 v149, 1.0, v149
	v_rcp_f32_e32 v168, v149
	v_mul_f32_e32 v149, 0x3d372713, v174
	v_mul_f32_e32 v149, v174, v149
	v_fma_f32 v149, v174, v149, v174
	v_mul_f32_e32 v149, 0x3fcc422a, v149
	v_mul_f32_e32 v149, 0xbfb8aa3b, v149
	v_exp_f32_e32 v149, v149
	s_nop 0
	v_add_f32_e32 v149, 1.0, v149
	v_rcp_f32_e32 v178, v149
	v_mul_f32_e32 v149, 0x3d372713, v171
	v_mul_f32_e32 v149, v171, v149
	v_fma_f32 v149, v171, v149, v171
	v_mul_f32_e32 v149, 0x3fcc422a, v149
	v_mul_f32_e32 v149, 0xbfb8aa3b, v149
	v_exp_f32_e32 v149, v149
	s_nop 0
	v_add_f32_e32 v149, 1.0, v149
	v_rcp_f32_e32 v169, v149
	v_mul_f32_e32 v149, 0x3d372713, v175
	v_mul_f32_e32 v149, v175, v149
	v_fma_f32 v149, v175, v149, v175
	v_mul_f32_e32 v149, 0x3fcc422a, v149
	v_mul_f32_e32 v149, 0xbfb8aa3b, v149
	v_exp_f32_e32 v149, v149
	v_pk_mul_f32 v[170:171], v[170:171], v[168:169]
	v_cvt_pk_bf16_f32 v168, v172, v173
	v_cvt_pk_bf16_f32 v169, v170, v171
	v_add_f32_e32 v149, 1.0, v149
	v_rcp_f32_e32 v179, v149
	v_cvt_pk_bf16_f32 v170, v176, v177
	v_or_b32_e32 v149, 16, v148
	v_pk_mul_f32 v[172:173], v[110:111], v[164:165] op_sel_hi:[1,0]
	v_pk_mul_f32 v[174:175], v[174:175], v[178:179]
	s_nop 0
	v_cvt_pk_bf16_f32 v171, v174, v175
	global_store_dwordx4 v[166:167], v[168:171], off offset:256 nt
	v_mad_i64_i32 v[166:167], s[12:13], v149, s41, v[150:151]
	s_nop 0
	v_pk_mul_f32 v[170:171], v[112:113], v[164:165] op_sel_hi:[1,0]
	v_pk_mul_f32 v[174:175], v[108:109], v[164:165] op_sel_hi:[1,0]
	v_mul_f32_e32 v149, 0x3d372713, v170
	v_mul_f32_e32 v149, v170, v149
	v_fma_f32 v149, v170, v149, v170
	v_mul_f32_e32 v149, 0x3fcc422a, v149
	v_mul_f32_e32 v149, 0xbfb8aa3b, v149
	v_exp_f32_e32 v149, v149
	v_pk_mul_f32 v[168:169], v[114:115], v[164:165] op_sel_hi:[1,0]
	v_lshl_add_u64 v[166:167], v[166:167], 0, v[152:153]
	v_add_f32_e32 v149, 1.0, v149
	v_rcp_f32_e32 v176, v149
	v_mul_f32_e32 v149, 0x3d372713, v174
	v_mul_f32_e32 v149, v174, v149
	v_fma_f32 v149, v174, v149, v174
	v_mul_f32_e32 v149, 0x3fcc422a, v149
	v_mul_f32_e32 v149, 0xbfb8aa3b, v149
	v_exp_f32_e32 v149, v149
	s_nop 0
	v_add_f32_e32 v149, 1.0, v149
	v_rcp_f32_e32 v178, v149
	v_mul_f32_e32 v149, 0x3d372713, v171
	v_mul_f32_e32 v149, v171, v149
	v_fma_f32 v149, v171, v149, v171
	v_mul_f32_e32 v149, 0x3fcc422a, v149
	v_mul_f32_e32 v149, 0xbfb8aa3b, v149
	v_exp_f32_e32 v149, v149
	s_nop 0
	v_add_f32_e32 v149, 1.0, v149
	v_rcp_f32_e32 v177, v149
	v_mul_f32_e32 v149, 0x3d372713, v175
	v_mul_f32_e32 v149, v175, v149
	v_fma_f32 v149, v175, v149, v175
	v_mul_f32_e32 v149, 0x3fcc422a, v149
	v_mul_f32_e32 v149, 0xbfb8aa3b, v149
	v_exp_f32_e32 v149, v149
	v_pk_mul_f32 v[170:171], v[170:171], v[176:177]
	v_add_f32_e32 v149, 1.0, v149
	v_rcp_f32_e32 v179, v149
	v_mul_f32_e32 v149, 0x3d372713, v168
	v_mul_f32_e32 v149, v168, v149
	v_fma_f32 v149, v168, v149, v168
	v_mul_f32_e32 v149, 0x3fcc422a, v149
	v_mul_f32_e32 v149, 0xbfb8aa3b, v149
	v_exp_f32_e32 v149, v149
	v_pk_mul_f32 v[174:175], v[174:175], v[178:179]
	v_add_f32_e32 v149, 1.0, v149
	v_rcp_f32_e32 v176, v149
	v_mul_f32_e32 v149, 0x3d372713, v172
	v_mul_f32_e32 v149, v172, v149
	v_fma_f32 v149, v172, v149, v172
	v_mul_f32_e32 v149, 0x3fcc422a, v149
	v_mul_f32_e32 v149, 0xbfb8aa3b, v149
	v_exp_f32_e32 v149, v149
	s_nop 0
	v_add_f32_e32 v149, 1.0, v149
	v_rcp_f32_e32 v178, v149
	v_mul_f32_e32 v149, 0x3d372713, v169
	v_mul_f32_e32 v149, v169, v149
	v_fma_f32 v149, v169, v149, v169
	v_mul_f32_e32 v149, 0x3fcc422a, v149
	v_mul_f32_e32 v149, 0xbfb8aa3b, v149
	v_exp_f32_e32 v149, v149
	s_nop 0
	v_add_f32_e32 v149, 1.0, v149
	v_rcp_f32_e32 v177, v149
	v_mul_f32_e32 v149, 0x3d372713, v173
	v_mul_f32_e32 v149, v173, v149
	v_fma_f32 v149, v173, v149, v173
	v_mul_f32_e32 v149, 0x3fcc422a, v149
	v_mul_f32_e32 v149, 0xbfb8aa3b, v149
	v_exp_f32_e32 v149, v149
	v_pk_mul_f32 v[176:177], v[168:169], v[176:177]
	v_cvt_pk_bf16_f32 v168, v170, v171
	v_cvt_pk_bf16_f32 v169, v176, v177
	v_add_f32_e32 v149, 1.0, v149
	v_rcp_f32_e32 v179, v149
	v_cvt_pk_bf16_f32 v170, v174, v175
	v_pk_mul_f32 v[172:173], v[172:173], v[178:179]
	s_nop 0
	v_cvt_pk_bf16_f32 v171, v172, v173
	global_store_dwordx4 v[166:167], v[168:171], off nt
	v_pk_mul_f32 v[172:173], v[102:103], v[164:165] op_sel_hi:[1,0]
	s_nop 0
	v_pk_mul_f32 v[170:171], v[104:105], v[164:165] op_sel_hi:[1,0]
	v_pk_mul_f32 v[168:169], v[106:107], v[164:165] op_sel_hi:[1,0]
	v_mul_f32_e32 v149, 0x3d372713, v170
	v_mul_f32_e32 v149, v170, v149
	v_fma_f32 v149, v170, v149, v170
	v_mul_f32_e32 v149, 0x3fcc422a, v149
	v_mul_f32_e32 v149, 0xbfb8aa3b, v149
	v_exp_f32_e32 v149, v149
	v_pk_mul_f32 v[164:165], v[100:101], v[164:165] op_sel_hi:[1,0]
	v_add_f32_e32 v149, 1.0, v149
	v_rcp_f32_e32 v174, v149
	v_mul_f32_e32 v149, 0x3d372713, v164
	v_mul_f32_e32 v149, v164, v149
	v_fma_f32 v149, v164, v149, v164
	v_mul_f32_e32 v149, 0x3fcc422a, v149
	v_mul_f32_e32 v149, 0xbfb8aa3b, v149
	v_exp_f32_e32 v149, v149
	s_nop 0
	v_add_f32_e32 v149, 1.0, v149
	v_rcp_f32_e32 v176, v149
	v_mul_f32_e32 v149, 0x3d372713, v171
	v_mul_f32_e32 v149, v171, v149
	v_fma_f32 v149, v171, v149, v171
	v_mul_f32_e32 v149, 0x3fcc422a, v149
	v_mul_f32_e32 v149, 0xbfb8aa3b, v149
	v_exp_f32_e32 v149, v149
	s_nop 0
	v_add_f32_e32 v149, 1.0, v149
	v_rcp_f32_e32 v175, v149
	v_mul_f32_e32 v149, 0x3d372713, v165
	v_mul_f32_e32 v149, v165, v149
	v_fma_f32 v149, v165, v149, v165
	v_mul_f32_e32 v149, 0x3fcc422a, v149
	v_mul_f32_e32 v149, 0xbfb8aa3b, v149
	v_exp_f32_e32 v149, v149
	v_pk_mul_f32 v[170:171], v[170:171], v[174:175]
; __device__ __forceinline__ unsigned cvt_pk_bf16(float lo, float hi) { f32x2_t v = {lo, hi}; bf16x2_t b = __builtin_convertvector(v, bf16x2_t); return __builtin_bit_cast(unsigned, b); }
;     template <int ACT, int AUX> __device__ __forceinline__ void run(const f32x4 (&acc)[2][2][4][2], const Unit& uu, int wr, int wc, int fr, int fq) const {
;     ...
;             for (int m = 0; m < 4; ++m) { const int r = row0 + ai * HALF + m * 16; const float rs = rsv[ai * 4 + m];
;                 bf16_t* rowp = O + (size_t)r * cfg::NC + col0; float s1 = 0.f, s2 = 0.f;
; #pragma unroll
;                 for (int bj = 0; bj < 2; ++bj) { f32x4 v0 = acc[ai][bj][m][0] * rs, v1 = acc[ai][bj][m][1] * rs;
; #pragma unroll
;                     for (int j = 0; j < 4; ++j) { v0[j] = act_f<ACT>(v0[j]); v1[j] = act_f<ACT>(v1[j]); }
;                     if (AUX == 4) {
;                         unsigned q[8];
; #pragma unroll
;                         for (int j = 0; j < 4; ++j) { q[j] = (unsigned)fminf(fmaxf(fmaf(v0[j], 255.0f, 0.5f), 1.0f), 255.0f); q[4 + j] = (unsigned)fminf(fmaxf(fmaf(v1[j], 255.0f, 0.5f), 1.0f), 255.0f); }
;                         u32x2 w8; w8.x = q[0] | (q[1] << 8) | (q[2] << 16) | (q[3] << 24); w8.y = q[4] | (q[5] << 8) | (q[6] << 16) | (q[7] << 24);
;                         __builtin_nontemporal_store(w8, (u32x2*)(g8 + ((size_t)((u.pn - 52) >> 4) * cfg::MT + r) * cfg::DM + ((u.pn - 52) & 15) * BM + wc * 32 + 8 * fq + bj * HALF));
;                     } else {
;                     u32x4 w; w.x = cvt_pk_bf16(v0[0], v0[1]); w.y = cvt_pk_bf16(v0[2], v0[3]); w.z = cvt_pk_bf16(v1[0], v1[1]); w.w = cvt_pk_bf16(v1[2], v1[3]);
;                     __builtin_nontemporal_store(w, (u32x4*)(rowp + bj * HALF)); }
	v_add_f32_e32 v149, 1.0, v149
	v_rcp_f32_e32 v177, v149
	v_mul_f32_e32 v149, 0x3d372713, v168
	v_mul_f32_e32 v149, v168, v149
	v_fma_f32 v149, v168, v149, v168
	v_mul_f32_e32 v149, 0x3fcc422a, v149
	v_mul_f32_e32 v149, 0xbfb8aa3b, v149
	v_exp_f32_e32 v149, v149
	v_pk_mul_f32 v[164:165], v[164:165], v[176:177]
	v_add_f32_e32 v149, 1.0, v149
	v_rcp_f32_e32 v174, v149
	v_mul_f32_e32 v149, 0x3d372713, v172
	v_mul_f32_e32 v149, v172, v149
	v_fma_f32 v149, v172, v149, v172
	v_mul_f32_e32 v149, 0x3fcc422a, v149
	v_mul_f32_e32 v149, 0xbfb8aa3b, v149
	v_exp_f32_e32 v149, v149
	s_nop 0
	v_add_f32_e32 v149, 1.0, v149
	v_rcp_f32_e32 v176, v149
	v_mul_f32_e32 v149, 0x3d372713, v169
	v_mul_f32_e32 v149, v169, v149
	v_fma_f32 v149, v169, v149, v169
	v_mul_f32_e32 v149, 0x3fcc422a, v149
	v_mul_f32_e32 v149, 0xbfb8aa3b, v149
	v_exp_f32_e32 v149, v149
	s_nop 0
	v_add_f32_e32 v149, 1.0, v149
	v_rcp_f32_e32 v175, v149
	v_mul_f32_e32 v149, 0x3d372713, v173
	v_mul_f32_e32 v149, v173, v149
	v_fma_f32 v149, v173, v149, v173
	v_mul_f32_e32 v149, 0x3fcc422a, v149
	v_mul_f32_e32 v149, 0xbfb8aa3b, v149
	v_exp_f32_e32 v149, v149
	v_pk_mul_f32 v[174:175], v[168:169], v[174:175]
	v_cvt_pk_bf16_f32 v168, v170, v171
	v_cvt_pk_bf16_f32 v169, v174, v175
	v_add_f32_e32 v149, 1.0, v149
	v_rcp_f32_e32 v177, v149
	v_cvt_pk_bf16_f32 v170, v164, v165
	v_or_b32_e32 v149, 32, v148
	v_mad_i64_i32 v[164:165], s[12:13], v149, s41, v[150:151]
	v_pk_mul_f32 v[172:173], v[172:173], v[176:177]
	v_lshl_add_u64 v[164:165], v[164:165], 0, v[152:153]
	v_cvt_pk_bf16_f32 v171, v172, v173
	global_store_dwordx4 v[166:167], v[168:171], off offset:256 nt
	v_pk_mul_f32 v[172:173], v[92:93], v[162:163] op_sel_hi:[1,0]
	v_pk_mul_f32 v[166:167], v[98:99], v[162:163] op_sel_hi:[1,0]
	v_pk_mul_f32 v[168:169], v[96:97], v[162:163] op_sel_hi:[1,0]
	v_pk_mul_f32 v[170:171], v[94:95], v[162:163] op_sel_hi:[1,0]
	v_mul_f32_e32 v149, 0x3d372713, v168
	v_mul_f32_e32 v149, v168, v149
	v_fma_f32 v149, v168, v149, v168
	v_mul_f32_e32 v149, 0x3fcc422a, v149
	v_mul_f32_e32 v149, 0xbfb8aa3b, v149
	v_exp_f32_e32 v149, v149
	s_nop 0
	v_add_f32_e32 v149, 1.0, v149
	v_rcp_f32_e32 v174, v149
	v_mul_f32_e32 v149, 0x3d372713, v172
	v_mul_f32_e32 v149, v172, v149
	v_fma_f32 v149, v172, v149, v172
	v_mul_f32_e32 v149, 0x3fcc422a, v149
	v_mul_f32_e32 v149, 0xbfb8aa3b, v149
	v_exp_f32_e32 v149, v149
	s_nop 0
	v_add_f32_e32 v149, 1.0, v149
	v_rcp_f32_e32 v176, v149
	v_mul_f32_e32 v149, 0x3d372713, v169
	v_mul_f32_e32 v149, v169, v149
	v_fma_f32 v149, v169, v149, v169
	v_mul_f32_e32 v149, 0x3fcc422a, v149
	v_mul_f32_e32 v149, 0xbfb8aa3b, v149
	v_exp_f32_e32 v149, v149
	s_nop 0
	v_add_f32_e32 v149, 1.0, v149
	v_rcp_f32_e32 v175, v149
	v_mul_f32_e32 v149, 0x3d372713, v173
	v_mul_f32_e32 v149, v173, v149
	v_fma_f32 v149, v173, v149, v173
	v_mul_f32_e32 v149, 0x3fcc422a, v149
	v_mul_f32_e32 v149, 0xbfb8aa3b, v149
	v_exp_f32_e32 v149, v149
	v_pk_mul_f32 v[168:169], v[168:169], v[174:175]
	v_add_f32_e32 v149, 1.0, v149
	v_rcp_f32_e32 v177, v149
	v_mul_f32_e32 v149, 0x3d372713, v166
	v_mul_f32_e32 v149, v166, v149
	v_fma_f32 v149, v166, v149, v166
	v_mul_f32_e32 v149, 0x3fcc422a, v149
	v_mul_f32_e32 v149, 0xbfb8aa3b, v149
	v_exp_f32_e32 v149, v149
	v_pk_mul_f32 v[172:173], v[172:173], v[176:177]
	v_add_f32_e32 v149, 1.0, v149
	v_rcp_f32_e32 v174, v149
	v_mul_f32_e32 v149, 0x3d372713, v170
	v_mul_f32_e32 v149, v170, v149
	v_fma_f32 v149, v170, v149, v170
	v_mul_f32_e32 v149, 0x3fcc422a, v149
	v_mul_f32_e32 v149, 0xbfb8aa3b, v149
	v_exp_f32_e32 v149, v149
	s_nop 0
	v_add_f32_e32 v149, 1.0, v149
	v_rcp_f32_e32 v176, v149
	v_mul_f32_e32 v149, 0x3d372713, v167
	v_mul_f32_e32 v149, v167, v149
	v_fma_f32 v149, v167, v149, v167
	v_mul_f32_e32 v149, 0x3fcc422a, v149
	v_mul_f32_e32 v149, 0xbfb8aa3b, v149
	v_exp_f32_e32 v149, v149
	s_nop 0
	v_add_f32_e32 v149, 1.0, v149
	v_rcp_f32_e32 v175, v149
	v_mul_f32_e32 v149, 0x3d372713, v171
	v_mul_f32_e32 v149, v171, v149
	v_fma_f32 v149, v171, v149, v171
	v_mul_f32_e32 v149, 0x3fcc422a, v149
	v_mul_f32_e32 v149, 0xbfb8aa3b, v149
	v_exp_f32_e32 v149, v149
	v_pk_mul_f32 v[174:175], v[166:167], v[174:175]
	v_cvt_pk_bf16_f32 v166, v168, v169
	v_cvt_pk_bf16_f32 v167, v174, v175
	v_add_f32_e32 v149, 1.0, v149
	v_rcp_f32_e32 v177, v149
	v_cvt_pk_bf16_f32 v168, v172, v173
	v_pk_mul_f32 v[170:171], v[170:171], v[176:177]
	s_nop 0
	v_cvt_pk_bf16_f32 v169, v170, v171
	global_store_dwordx4 v[164:165], v[166:169], off nt
	v_pk_mul_f32 v[170:171], v[86:87], v[162:163] op_sel_hi:[1,0]
	s_nop 0
	v_pk_mul_f32 v[168:169], v[88:89], v[162:163] op_sel_hi:[1,0]
	v_pk_mul_f32 v[166:167], v[90:91], v[162:163] op_sel_hi:[1,0]
	v_mul_f32_e32 v149, 0x3d372713, v168
	v_mul_f32_e32 v149, v168, v149
	v_fma_f32 v149, v168, v149, v168
	v_mul_f32_e32 v149, 0x3fcc422a, v149
	v_mul_f32_e32 v149, 0xbfb8aa3b, v149
	v_exp_f32_e32 v149, v149
	v_pk_mul_f32 v[162:163], v[84:85], v[162:163] op_sel_hi:[1,0]
	v_add_f32_e32 v149, 1.0, v149
	v_rcp_f32_e32 v172, v149
	v_mul_f32_e32 v149, 0x3d372713, v162
	v_mul_f32_e32 v149, v162, v149
	v_fma_f32 v149, v162, v149, v162
	v_mul_f32_e32 v149, 0x3fcc422a, v149
	v_mul_f32_e32 v149, 0xbfb8aa3b, v149
	v_exp_f32_e32 v149, v149
	s_nop 0
	v_add_f32_e32 v149, 1.0, v149
	v_rcp_f32_e32 v174, v149
	v_mul_f32_e32 v149, 0x3d372713, v169
	v_mul_f32_e32 v149, v169, v149
	v_fma_f32 v149, v169, v149, v169
	v_mul_f32_e32 v149, 0x3fcc422a, v149
	v_mul_f32_e32 v149, 0xbfb8aa3b, v149
	v_exp_f32_e32 v149, v149
	s_nop 0
	v_add_f32_e32 v149, 1.0, v149
	v_rcp_f32_e32 v173, v149
	v_mul_f32_e32 v149, 0x3d372713, v163
	v_mul_f32_e32 v149, v163, v149
	v_fma_f32 v149, v163, v149, v163
	v_mul_f32_e32 v149, 0x3fcc422a, v149
; __device__ __forceinline__ unsigned cvt_pk_bf16(float lo, float hi) { f32x2_t v = {lo, hi}; bf16x2_t b = __builtin_convertvector(v, bf16x2_t); return __builtin_bit_cast(unsigned, b); }
;     template <int ACT, int AUX> __device__ __forceinline__ void run(const f32x4 (&acc)[2][2][4][2], const Unit& uu, int wr, int wc, int fr, int fq) const {
;     ...
;             for (int m = 0; m < 4; ++m) { const int r = row0 + ai * HALF + m * 16; const float rs = rsv[ai * 4 + m];
;                 bf16_t* rowp = O + (size_t)r * cfg::NC + col0; float s1 = 0.f, s2 = 0.f;
; #pragma unroll
;                 for (int bj = 0; bj < 2; ++bj) { f32x4 v0 = acc[ai][bj][m][0] * rs, v1 = acc[ai][bj][m][1] * rs;
; #pragma unroll
;                     for (int j = 0; j < 4; ++j) { v0[j] = act_f<ACT>(v0[j]); v1[j] = act_f<ACT>(v1[j]); }
;                     if (AUX == 4) {
;                         unsigned q[8];
; #pragma unroll
;                         for (int j = 0; j < 4; ++j) { q[j] = (unsigned)fminf(fmaxf(fmaf(v0[j], 255.0f, 0.5f), 1.0f), 255.0f); q[4 + j] = (unsigned)fminf(fmaxf(fmaf(v1[j], 255.0f, 0.5f), 1.0f), 255.0f); }
;                         u32x2 w8; w8.x = q[0] | (q[1] << 8) | (q[2] << 16) | (q[3] << 24); w8.y = q[4] | (q[5] << 8) | (q[6] << 16) | (q[7] << 24);
;                         __builtin_nontemporal_store(w8, (u32x2*)(g8 + ((size_t)((u.pn - 52) >> 4) * cfg::MT + r) * cfg::DM + ((u.pn - 52) & 15) * BM + wc * 32 + 8 * fq + bj * HALF));
;                     } else {
;                     u32x4 w; w.x = cvt_pk_bf16(v0[0], v0[1]); w.y = cvt_pk_bf16(v0[2], v0[3]); w.z = cvt_pk_bf16(v1[0], v1[1]); w.w = cvt_pk_bf16(v1[2], v1[3]);
;                     __builtin_nontemporal_store(w, (u32x4*)(rowp + bj * HALF)); }
	v_mul_f32_e32 v149, 0xbfb8aa3b, v149
	v_exp_f32_e32 v149, v149
	v_pk_mul_f32 v[168:169], v[168:169], v[172:173]
	v_add_f32_e32 v149, 1.0, v149
	v_rcp_f32_e32 v175, v149
	v_mul_f32_e32 v149, 0x3d372713, v166
	v_mul_f32_e32 v149, v166, v149
	v_fma_f32 v149, v166, v149, v166
	v_mul_f32_e32 v149, 0x3fcc422a, v149
	v_mul_f32_e32 v149, 0xbfb8aa3b, v149
	v_exp_f32_e32 v149, v149
	v_pk_mul_f32 v[162:163], v[162:163], v[174:175]
	v_add_f32_e32 v149, 1.0, v149
	v_rcp_f32_e32 v172, v149
	v_mul_f32_e32 v149, 0x3d372713, v170
	v_mul_f32_e32 v149, v170, v149
	v_fma_f32 v149, v170, v149, v170
	v_mul_f32_e32 v149, 0x3fcc422a, v149
	v_mul_f32_e32 v149, 0xbfb8aa3b, v149
	v_exp_f32_e32 v149, v149
	s_nop 0
	v_add_f32_e32 v149, 1.0, v149
	v_rcp_f32_e32 v174, v149
	v_mul_f32_e32 v149, 0x3d372713, v167
	v_mul_f32_e32 v149, v167, v149
	v_fma_f32 v149, v167, v149, v167
	v_mul_f32_e32 v149, 0x3fcc422a, v149
	v_mul_f32_e32 v149, 0xbfb8aa3b, v149
	v_exp_f32_e32 v149, v149
	s_nop 0
	v_add_f32_e32 v149, 1.0, v149
	v_rcp_f32_e32 v173, v149
	v_mul_f32_e32 v149, 0x3d372713, v171
	v_mul_f32_e32 v149, v171, v149
	v_fma_f32 v149, v171, v149, v171
	v_mul_f32_e32 v149, 0x3fcc422a, v149
	v_mul_f32_e32 v149, 0xbfb8aa3b, v149
	v_exp_f32_e32 v149, v149
	v_pk_mul_f32 v[172:173], v[166:167], v[172:173]
	v_cvt_pk_bf16_f32 v166, v168, v169
	v_cvt_pk_bf16_f32 v167, v172, v173
	v_add_f32_e32 v149, 1.0, v149
	v_rcp_f32_e32 v175, v149
	v_cvt_pk_bf16_f32 v168, v162, v163
	v_or_b32_e32 v149, 48, v148
	v_mad_i64_i32 v[162:163], s[12:13], v149, s41, v[150:151]
	v_pk_mul_f32 v[170:171], v[170:171], v[174:175]
	v_lshl_add_u64 v[162:163], v[162:163], 0, v[152:153]
	v_cvt_pk_bf16_f32 v169, v170, v171
	global_store_dwordx4 v[164:165], v[166:169], off offset:256 nt
	v_pk_mul_f32 v[170:171], v[76:77], v[160:161] op_sel_hi:[1,0]
	v_pk_mul_f32 v[164:165], v[82:83], v[160:161] op_sel_hi:[1,0]
	v_pk_mul_f32 v[166:167], v[80:81], v[160:161] op_sel_hi:[1,0]
	v_pk_mul_f32 v[168:169], v[78:79], v[160:161] op_sel_hi:[1,0]
	v_mul_f32_e32 v149, 0x3d372713, v166
	v_mul_f32_e32 v149, v166, v149
	v_fma_f32 v149, v166, v149, v166
	v_mul_f32_e32 v149, 0x3fcc422a, v149
	v_mul_f32_e32 v149, 0xbfb8aa3b, v149
	v_exp_f32_e32 v149, v149
	s_nop 0
	v_add_f32_e32 v149, 1.0, v149
	v_rcp_f32_e32 v172, v149
	v_mul_f32_e32 v149, 0x3d372713, v170
	v_mul_f32_e32 v149, v170, v149
	v_fma_f32 v149, v170, v149, v170
	v_mul_f32_e32 v149, 0x3fcc422a, v149
	v_mul_f32_e32 v149, 0xbfb8aa3b, v149
	v_exp_f32_e32 v149, v149
	s_nop 0
	v_add_f32_e32 v149, 1.0, v149
	v_rcp_f32_e32 v174, v149
	v_mul_f32_e32 v149, 0x3d372713, v167
	v_mul_f32_e32 v149, v167, v149
	v_fma_f32 v149, v167, v149, v167
	v_mul_f32_e32 v149, 0x3fcc422a, v149
	v_mul_f32_e32 v149, 0xbfb8aa3b, v149
	v_exp_f32_e32 v149, v149
	s_nop 0
	v_add_f32_e32 v149, 1.0, v149
	v_rcp_f32_e32 v173, v149
	v_mul_f32_e32 v149, 0x3d372713, v171
	v_mul_f32_e32 v149, v171, v149
	v_fma_f32 v149, v171, v149, v171
	v_mul_f32_e32 v149, 0x3fcc422a, v149
	v_mul_f32_e32 v149, 0xbfb8aa3b, v149
	v_exp_f32_e32 v149, v149
	v_pk_mul_f32 v[166:167], v[166:167], v[172:173]
	v_add_f32_e32 v149, 1.0, v149
	v_rcp_f32_e32 v175, v149
	v_mul_f32_e32 v149, 0x3d372713, v164
	v_mul_f32_e32 v149, v164, v149
	v_fma_f32 v149, v164, v149, v164
	v_mul_f32_e32 v149, 0x3fcc422a, v149
	v_mul_f32_e32 v149, 0xbfb8aa3b, v149
	v_exp_f32_e32 v149, v149
	v_pk_mul_f32 v[170:171], v[170:171], v[174:175]
	v_add_f32_e32 v149, 1.0, v149
	v_rcp_f32_e32 v172, v149
	v_mul_f32_e32 v149, 0x3d372713, v168
	v_mul_f32_e32 v149, v168, v149
	v_fma_f32 v149, v168, v149, v168
	v_mul_f32_e32 v149, 0x3fcc422a, v149
	v_mul_f32_e32 v149, 0xbfb8aa3b, v149
	v_exp_f32_e32 v149, v149
	s_nop 0
	v_add_f32_e32 v149, 1.0, v149
	v_rcp_f32_e32 v174, v149
	v_mul_f32_e32 v149, 0x3d372713, v165
	v_mul_f32_e32 v149, v165, v149
	v_fma_f32 v149, v165, v149, v165
	v_mul_f32_e32 v149, 0x3fcc422a, v149
	v_mul_f32_e32 v149, 0xbfb8aa3b, v149
	v_exp_f32_e32 v149, v149
	s_nop 0
	v_add_f32_e32 v149, 1.0, v149
	v_rcp_f32_e32 v173, v149
	v_mul_f32_e32 v149, 0x3d372713, v169
	v_mul_f32_e32 v149, v169, v149
	v_fma_f32 v149, v169, v149, v169
	v_mul_f32_e32 v149, 0x3fcc422a, v149
	v_mul_f32_e32 v149, 0xbfb8aa3b, v149
	v_exp_f32_e32 v149, v149
	v_pk_mul_f32 v[172:173], v[164:165], v[172:173]
	v_cvt_pk_bf16_f32 v164, v166, v167
	v_cvt_pk_bf16_f32 v165, v172, v173
	v_add_f32_e32 v149, 1.0, v149
	v_rcp_f32_e32 v175, v149
	v_cvt_pk_bf16_f32 v166, v170, v171
	v_pk_mul_f32 v[168:169], v[168:169], v[174:175]
	s_nop 0
	v_cvt_pk_bf16_f32 v167, v168, v169
	global_store_dwordx4 v[162:163], v[164:167], off nt
	v_pk_mul_f32 v[168:169], v[70:71], v[160:161] op_sel_hi:[1,0]
	s_nop 0
	v_pk_mul_f32 v[166:167], v[72:73], v[160:161] op_sel_hi:[1,0]
	v_pk_mul_f32 v[164:165], v[74:75], v[160:161] op_sel_hi:[1,0]
	v_mul_f32_e32 v149, 0x3d372713, v166
	v_mul_f32_e32 v149, v166, v149
	v_fma_f32 v149, v166, v149, v166
	v_mul_f32_e32 v149, 0x3fcc422a, v149
	v_mul_f32_e32 v149, 0xbfb8aa3b, v149
	v_exp_f32_e32 v149, v149
	v_pk_mul_f32 v[160:161], v[68:69], v[160:161] op_sel_hi:[1,0]
	v_add_f32_e32 v149, 1.0, v149
	v_rcp_f32_e32 v170, v149
	v_mul_f32_e32 v149, 0x3d372713, v160
	v_mul_f32_e32 v149, v160, v149
	v_fma_f32 v149, v160, v149, v160
	v_mul_f32_e32 v149, 0x3fcc422a, v149
	v_mul_f32_e32 v149, 0xbfb8aa3b, v149
	v_exp_f32_e32 v149, v149
	s_nop 0
	v_add_f32_e32 v149, 1.0, v149
	v_rcp_f32_e32 v172, v149
	v_mul_f32_e32 v149, 0x3d372713, v167
	v_mul_f32_e32 v149, v167, v149
	v_fma_f32 v149, v167, v149, v167
	v_mul_f32_e32 v149, 0x3fcc422a, v149
	v_mul_f32_e32 v149, 0xbfb8aa3b, v149
	v_exp_f32_e32 v149, v149
	s_nop 0
	v_add_f32_e32 v149, 1.0, v149
	v_rcp_f32_e32 v171, v149
	v_mul_f32_e32 v149, 0x3d372713, v161
; __device__ __forceinline__ unsigned cvt_pk_bf16(float lo, float hi) { f32x2_t v = {lo, hi}; bf16x2_t b = __builtin_convertvector(v, bf16x2_t); return __builtin_bit_cast(unsigned, b); }
;     template <int ACT, int AUX> __device__ __forceinline__ void run(const f32x4 (&acc)[2][2][4][2], const Unit& uu, int wr, int wc, int fr, int fq) const {
;     ...
;             for (int m = 0; m < 4; ++m) { const int r = row0 + ai * HALF + m * 16; const float rs = rsv[ai * 4 + m];
;                 bf16_t* rowp = O + (size_t)r * cfg::NC + col0; float s1 = 0.f, s2 = 0.f;
; #pragma unroll
;                 for (int bj = 0; bj < 2; ++bj) { f32x4 v0 = acc[ai][bj][m][0] * rs, v1 = acc[ai][bj][m][1] * rs;
; #pragma unroll
;                     for (int j = 0; j < 4; ++j) { v0[j] = act_f<ACT>(v0[j]); v1[j] = act_f<ACT>(v1[j]); }
;                     if (AUX == 4) {
;                         unsigned q[8];
; #pragma unroll
;                         for (int j = 0; j < 4; ++j) { q[j] = (unsigned)fminf(fmaxf(fmaf(v0[j], 255.0f, 0.5f), 1.0f), 255.0f); q[4 + j] = (unsigned)fminf(fmaxf(fmaf(v1[j], 255.0f, 0.5f), 1.0f), 255.0f); }
;                         u32x2 w8; w8.x = q[0] | (q[1] << 8) | (q[2] << 16) | (q[3] << 24); w8.y = q[4] | (q[5] << 8) | (q[6] << 16) | (q[7] << 24);
;                         __builtin_nontemporal_store(w8, (u32x2*)(g8 + ((size_t)((u.pn - 52) >> 4) * cfg::MT + r) * cfg::DM + ((u.pn - 52) & 15) * BM + wc * 32 + 8 * fq + bj * HALF));
;                     } else {
;                     u32x4 w; w.x = cvt_pk_bf16(v0[0], v0[1]); w.y = cvt_pk_bf16(v0[2], v0[3]); w.z = cvt_pk_bf16(v1[0], v1[1]); w.w = cvt_pk_bf16(v1[2], v1[3]);
;                     __builtin_nontemporal_store(w, (u32x4*)(rowp + bj * HALF)); }
	v_mul_f32_e32 v149, v161, v149
	v_fma_f32 v149, v161, v149, v161
	v_mul_f32_e32 v149, 0x3fcc422a, v149
	v_mul_f32_e32 v149, 0xbfb8aa3b, v149
	v_exp_f32_e32 v149, v149
	v_pk_mul_f32 v[166:167], v[166:167], v[170:171]
	v_add_f32_e32 v149, 1.0, v149
	v_rcp_f32_e32 v173, v149
	v_mul_f32_e32 v149, 0x3d372713, v164
	v_mul_f32_e32 v149, v164, v149
	v_fma_f32 v149, v164, v149, v164
	v_mul_f32_e32 v149, 0x3fcc422a, v149
	v_mul_f32_e32 v149, 0xbfb8aa3b, v149
	v_exp_f32_e32 v149, v149
	v_pk_mul_f32 v[160:161], v[160:161], v[172:173]
	v_add_f32_e32 v149, 1.0, v149
	v_rcp_f32_e32 v170, v149
	v_mul_f32_e32 v149, 0x3d372713, v168
	v_mul_f32_e32 v149, v168, v149
	v_fma_f32 v149, v168, v149, v168
	v_mul_f32_e32 v149, 0x3fcc422a, v149
	v_mul_f32_e32 v149, 0xbfb8aa3b, v149
	v_exp_f32_e32 v149, v149
	s_nop 0
	v_add_f32_e32 v149, 1.0, v149
	v_rcp_f32_e32 v172, v149
	v_mul_f32_e32 v149, 0x3d372713, v165
	v_mul_f32_e32 v149, v165, v149
	v_fma_f32 v149, v165, v149, v165
	v_mul_f32_e32 v149, 0x3fcc422a, v149
	v_mul_f32_e32 v149, 0xbfb8aa3b, v149
	v_exp_f32_e32 v149, v149
	s_nop 0
	v_add_f32_e32 v149, 1.0, v149
	v_rcp_f32_e32 v171, v149
	v_mul_f32_e32 v149, 0x3d372713, v169
	v_mul_f32_e32 v149, v169, v149
	v_fma_f32 v149, v169, v149, v169
	v_mul_f32_e32 v149, 0x3fcc422a, v149
	v_mul_f32_e32 v149, 0xbfb8aa3b, v149
	v_exp_f32_e32 v149, v149
	v_pk_mul_f32 v[170:171], v[164:165], v[170:171]
	v_cvt_pk_bf16_f32 v164, v166, v167
	v_cvt_pk_bf16_f32 v165, v170, v171
	v_add_f32_e32 v149, 1.0, v149
	v_rcp_f32_e32 v173, v149
	v_cvt_pk_bf16_f32 v166, v160, v161
	v_mad_i64_i32 v[160:161], s[12:13], v147, s41, v[150:151]
	v_pk_mul_f32 v[168:169], v[168:169], v[172:173]
	v_lshl_add_u64 v[160:161], v[160:161], 0, v[152:153]
	v_cvt_pk_bf16_f32 v167, v168, v169
	global_store_dwordx4 v[162:163], v[164:167], off offset:256 nt
	v_pk_mul_f32 v[168:169], v[60:61], v[158:159] op_sel_hi:[1,0]
	v_pk_mul_f32 v[162:163], v[66:67], v[158:159] op_sel_hi:[1,0]
	v_pk_mul_f32 v[164:165], v[64:65], v[158:159] op_sel_hi:[1,0]
	v_pk_mul_f32 v[166:167], v[62:63], v[158:159] op_sel_hi:[1,0]
	v_mul_f32_e32 v147, 0x3d372713, v164
	v_mul_f32_e32 v147, v164, v147
	v_fma_f32 v147, v164, v147, v164
	v_mul_f32_e32 v147, 0x3fcc422a, v147
	v_mul_f32_e32 v147, 0xbfb8aa3b, v147
	v_exp_f32_e32 v147, v147
	s_nop 0
	v_add_f32_e32 v147, 1.0, v147
	v_rcp_f32_e32 v170, v147
	v_mul_f32_e32 v147, 0x3d372713, v168
	v_mul_f32_e32 v147, v168, v147
	v_fma_f32 v147, v168, v147, v168
	v_mul_f32_e32 v147, 0x3fcc422a, v147
	v_mul_f32_e32 v147, 0xbfb8aa3b, v147
	v_exp_f32_e32 v147, v147
	s_nop 0
	v_add_f32_e32 v147, 1.0, v147
	v_rcp_f32_e32 v172, v147
	v_mul_f32_e32 v147, 0x3d372713, v165
	v_mul_f32_e32 v147, v165, v147
	v_fma_f32 v147, v165, v147, v165
	v_mul_f32_e32 v147, 0x3fcc422a, v147
	v_mul_f32_e32 v147, 0xbfb8aa3b, v147
	v_exp_f32_e32 v147, v147
	s_nop 0
	v_add_f32_e32 v147, 1.0, v147
	v_rcp_f32_e32 v171, v147
	v_mul_f32_e32 v147, 0x3d372713, v169
	v_mul_f32_e32 v147, v169, v147
	v_fma_f32 v147, v169, v147, v169
	v_mul_f32_e32 v147, 0x3fcc422a, v147
	v_mul_f32_e32 v147, 0xbfb8aa3b, v147
	v_exp_f32_e32 v147, v147
	v_pk_mul_f32 v[164:165], v[164:165], v[170:171]
	v_add_f32_e32 v147, 1.0, v147
	v_rcp_f32_e32 v173, v147
	v_mul_f32_e32 v147, 0x3d372713, v162
	v_mul_f32_e32 v147, v162, v147
	v_fma_f32 v147, v162, v147, v162
	v_mul_f32_e32 v147, 0x3fcc422a, v147
	v_mul_f32_e32 v147, 0xbfb8aa3b, v147
	v_exp_f32_e32 v147, v147
	v_pk_mul_f32 v[168:169], v[168:169], v[172:173]
	v_add_f32_e32 v147, 1.0, v147
	v_rcp_f32_e32 v170, v147
	v_mul_f32_e32 v147, 0x3d372713, v166
	v_mul_f32_e32 v147, v166, v147
	v_fma_f32 v147, v166, v147, v166
	v_mul_f32_e32 v147, 0x3fcc422a, v147
	v_mul_f32_e32 v147, 0xbfb8aa3b, v147
	v_exp_f32_e32 v147, v147
	s_nop 0
	v_add_f32_e32 v147, 1.0, v147
	v_rcp_f32_e32 v172, v147
	v_mul_f32_e32 v147, 0x3d372713, v163
	v_mul_f32_e32 v147, v163, v147
	v_fma_f32 v147, v163, v147, v163
	v_mul_f32_e32 v147, 0x3fcc422a, v147
	v_mul_f32_e32 v147, 0xbfb8aa3b, v147
	v_exp_f32_e32 v147, v147
	s_nop 0
	v_add_f32_e32 v147, 1.0, v147
	v_rcp_f32_e32 v171, v147
	v_mul_f32_e32 v147, 0x3d372713, v167
	v_mul_f32_e32 v147, v167, v147
	v_fma_f32 v147, v167, v147, v167
	v_mul_f32_e32 v147, 0x3fcc422a, v147
	v_mul_f32_e32 v147, 0xbfb8aa3b, v147
	v_exp_f32_e32 v147, v147
	v_pk_mul_f32 v[170:171], v[162:163], v[170:171]
	v_cvt_pk_bf16_f32 v162, v164, v165
	v_cvt_pk_bf16_f32 v163, v170, v171
	v_add_f32_e32 v147, 1.0, v147
	v_rcp_f32_e32 v173, v147
	v_cvt_pk_bf16_f32 v164, v168, v169
	v_pk_mul_f32 v[166:167], v[166:167], v[172:173]
	s_nop 0
	v_cvt_pk_bf16_f32 v165, v166, v167
	global_store_dwordx4 v[160:161], v[162:165], off nt
	v_pk_mul_f32 v[166:167], v[54:55], v[158:159] op_sel_hi:[1,0]
	s_nop 0
	v_pk_mul_f32 v[164:165], v[56:57], v[158:159] op_sel_hi:[1,0]
	v_pk_mul_f32 v[162:163], v[58:59], v[158:159] op_sel_hi:[1,0]
	v_mul_f32_e32 v147, 0x3d372713, v164
	v_mul_f32_e32 v147, v164, v147
	v_fma_f32 v147, v164, v147, v164
	v_mul_f32_e32 v147, 0x3fcc422a, v147
	v_mul_f32_e32 v147, 0xbfb8aa3b, v147
	v_exp_f32_e32 v147, v147
	v_pk_mul_f32 v[158:159], v[52:53], v[158:159] op_sel_hi:[1,0]
	v_add_f32_e32 v147, 1.0, v147
	v_rcp_f32_e32 v168, v147
	v_mul_f32_e32 v147, 0x3d372713, v158
	v_mul_f32_e32 v147, v158, v147
	v_fma_f32 v147, v158, v147, v158
	v_mul_f32_e32 v147, 0x3fcc422a, v147
	v_mul_f32_e32 v147, 0xbfb8aa3b, v147
	v_exp_f32_e32 v147, v147
	s_nop 0
	v_add_f32_e32 v147, 1.0, v147
	v_rcp_f32_e32 v170, v147
	v_mul_f32_e32 v147, 0x3d372713, v165
	v_mul_f32_e32 v147, v165, v147
	v_fma_f32 v147, v165, v147, v165
	v_mul_f32_e32 v147, 0x3fcc422a, v147
	v_mul_f32_e32 v147, 0xbfb8aa3b, v147
	v_exp_f32_e32 v147, v147
	s_nop 0
; __device__ __forceinline__ unsigned cvt_pk_bf16(float lo, float hi) { f32x2_t v = {lo, hi}; bf16x2_t b = __builtin_convertvector(v, bf16x2_t); return __builtin_bit_cast(unsigned, b); }
;     template <int ACT, int AUX> __device__ __forceinline__ void run(const f32x4 (&acc)[2][2][4][2], const Unit& uu, int wr, int wc, int fr, int fq) const {
;     ...
;             for (int m = 0; m < 4; ++m) { const int r = row0 + ai * HALF + m * 16; const float rs = rsv[ai * 4 + m];
;                 bf16_t* rowp = O + (size_t)r * cfg::NC + col0; float s1 = 0.f, s2 = 0.f;
; #pragma unroll
;                 for (int bj = 0; bj < 2; ++bj) { f32x4 v0 = acc[ai][bj][m][0] * rs, v1 = acc[ai][bj][m][1] * rs;
; #pragma unroll
;                     for (int j = 0; j < 4; ++j) { v0[j] = act_f<ACT>(v0[j]); v1[j] = act_f<ACT>(v1[j]); }
;                     if (AUX == 4) {
;                         unsigned q[8];
; #pragma unroll
;                         for (int j = 0; j < 4; ++j) { q[j] = (unsigned)fminf(fmaxf(fmaf(v0[j], 255.0f, 0.5f), 1.0f), 255.0f); q[4 + j] = (unsigned)fminf(fmaxf(fmaf(v1[j], 255.0f, 0.5f), 1.0f), 255.0f); }
;                         u32x2 w8; w8.x = q[0] | (q[1] << 8) | (q[2] << 16) | (q[3] << 24); w8.y = q[4] | (q[5] << 8) | (q[6] << 16) | (q[7] << 24);
;                         __builtin_nontemporal_store(w8, (u32x2*)(g8 + ((size_t)((u.pn - 52) >> 4) * cfg::MT + r) * cfg::DM + ((u.pn - 52) & 15) * BM + wc * 32 + 8 * fq + bj * HALF));
;                     } else {
;                     u32x4 w; w.x = cvt_pk_bf16(v0[0], v0[1]); w.y = cvt_pk_bf16(v0[2], v0[3]); w.z = cvt_pk_bf16(v1[0], v1[1]); w.w = cvt_pk_bf16(v1[2], v1[3]);
;                     __builtin_nontemporal_store(w, (u32x4*)(rowp + bj * HALF)); }
	v_add_f32_e32 v147, 1.0, v147
	v_rcp_f32_e32 v169, v147
	v_mul_f32_e32 v147, 0x3d372713, v159
	v_mul_f32_e32 v147, v159, v147
	v_fma_f32 v147, v159, v147, v159
	v_mul_f32_e32 v147, 0x3fcc422a, v147
	v_mul_f32_e32 v147, 0xbfb8aa3b, v147
	v_exp_f32_e32 v147, v147
	v_pk_mul_f32 v[164:165], v[164:165], v[168:169]
	v_add_f32_e32 v147, 1.0, v147
	v_rcp_f32_e32 v171, v147
	v_mul_f32_e32 v147, 0x3d372713, v162
	v_mul_f32_e32 v147, v162, v147
	v_fma_f32 v147, v162, v147, v162
	v_mul_f32_e32 v147, 0x3fcc422a, v147
	v_mul_f32_e32 v147, 0xbfb8aa3b, v147
	v_exp_f32_e32 v147, v147
	v_pk_mul_f32 v[158:159], v[158:159], v[170:171]
	v_add_f32_e32 v147, 1.0, v147
	v_rcp_f32_e32 v168, v147
	v_mul_f32_e32 v147, 0x3d372713, v166
	v_mul_f32_e32 v147, v166, v147
	v_fma_f32 v147, v166, v147, v166
	v_mul_f32_e32 v147, 0x3fcc422a, v147
	v_mul_f32_e32 v147, 0xbfb8aa3b, v147
	v_exp_f32_e32 v147, v147
	s_nop 0
	v_add_f32_e32 v147, 1.0, v147
	v_rcp_f32_e32 v170, v147
	v_mul_f32_e32 v147, 0x3d372713, v163
	v_mul_f32_e32 v147, v163, v147
	v_fma_f32 v147, v163, v147, v163
	v_mul_f32_e32 v147, 0x3fcc422a, v147
	v_mul_f32_e32 v147, 0xbfb8aa3b, v147
	v_exp_f32_e32 v147, v147
	s_nop 0
	v_add_f32_e32 v147, 1.0, v147
	v_rcp_f32_e32 v169, v147
	v_mul_f32_e32 v147, 0x3d372713, v167
	v_mul_f32_e32 v147, v167, v147
	v_fma_f32 v147, v167, v147, v167
	v_mul_f32_e32 v147, 0x3fcc422a, v147
	v_mul_f32_e32 v147, 0xbfb8aa3b, v147
	v_exp_f32_e32 v147, v147
	v_pk_mul_f32 v[168:169], v[162:163], v[168:169]
	v_cvt_pk_bf16_f32 v162, v164, v165
	v_cvt_pk_bf16_f32 v163, v168, v169
	v_add_f32_e32 v147, 1.0, v147
	v_rcp_f32_e32 v171, v147
	v_cvt_pk_bf16_f32 v164, v158, v159
	v_add_u32_e32 v147, 0x90, v148
	v_mad_i64_i32 v[158:159], s[12:13], v147, s41, v[150:151]
	v_pk_mul_f32 v[166:167], v[166:167], v[170:171]
	v_lshl_add_u64 v[158:159], v[158:159], 0, v[152:153]
	v_cvt_pk_bf16_f32 v165, v166, v167
	global_store_dwordx4 v[160:161], v[162:165], off offset:256 nt
	v_pk_mul_f32 v[166:167], v[44:45], v[156:157] op_sel_hi:[1,0]
	v_pk_mul_f32 v[160:161], v[50:51], v[156:157] op_sel_hi:[1,0]
	v_pk_mul_f32 v[162:163], v[48:49], v[156:157] op_sel_hi:[1,0]
	v_pk_mul_f32 v[164:165], v[46:47], v[156:157] op_sel_hi:[1,0]
	v_mul_f32_e32 v147, 0x3d372713, v162
	v_mul_f32_e32 v147, v162, v147
	v_fma_f32 v147, v162, v147, v162
	v_mul_f32_e32 v147, 0x3fcc422a, v147
	v_mul_f32_e32 v147, 0xbfb8aa3b, v147
	v_exp_f32_e32 v147, v147
	s_nop 0
	v_add_f32_e32 v147, 1.0, v147
	v_rcp_f32_e32 v168, v147
	v_mul_f32_e32 v147, 0x3d372713, v166
	v_mul_f32_e32 v147, v166, v147
	v_fma_f32 v147, v166, v147, v166
	v_mul_f32_e32 v147, 0x3fcc422a, v147
	v_mul_f32_e32 v147, 0xbfb8aa3b, v147
	v_exp_f32_e32 v147, v147
	s_nop 0
	v_add_f32_e32 v147, 1.0, v147
	v_rcp_f32_e32 v170, v147
	v_mul_f32_e32 v147, 0x3d372713, v163
	v_mul_f32_e32 v147, v163, v147
	v_fma_f32 v147, v163, v147, v163
	v_mul_f32_e32 v147, 0x3fcc422a, v147
	v_mul_f32_e32 v147, 0xbfb8aa3b, v147
	v_exp_f32_e32 v147, v147
	s_nop 0
	v_add_f32_e32 v147, 1.0, v147
	v_rcp_f32_e32 v169, v147
	v_mul_f32_e32 v147, 0x3d372713, v167
	v_mul_f32_e32 v147, v167, v147
	v_fma_f32 v147, v167, v147, v167
	v_mul_f32_e32 v147, 0x3fcc422a, v147
	v_mul_f32_e32 v147, 0xbfb8aa3b, v147
	v_exp_f32_e32 v147, v147
	v_pk_mul_f32 v[162:163], v[162:163], v[168:169]
	v_add_f32_e32 v147, 1.0, v147
	v_rcp_f32_e32 v171, v147
	v_mul_f32_e32 v147, 0x3d372713, v160
	v_mul_f32_e32 v147, v160, v147
	v_fma_f32 v147, v160, v147, v160
	v_mul_f32_e32 v147, 0x3fcc422a, v147
	v_mul_f32_e32 v147, 0xbfb8aa3b, v147
	v_exp_f32_e32 v147, v147
	v_pk_mul_f32 v[166:167], v[166:167], v[170:171]
	v_add_f32_e32 v147, 1.0, v147
	v_rcp_f32_e32 v168, v147
	v_mul_f32_e32 v147, 0x3d372713, v164
	v_mul_f32_e32 v147, v164, v147
	v_fma_f32 v147, v164, v147, v164
	v_mul_f32_e32 v147, 0x3fcc422a, v147
	v_mul_f32_e32 v147, 0xbfb8aa3b, v147
	v_exp_f32_e32 v147, v147
	s_nop 0
	v_add_f32_e32 v147, 1.0, v147
	v_rcp_f32_e32 v170, v147
	v_mul_f32_e32 v147, 0x3d372713, v161
	v_mul_f32_e32 v147, v161, v147
	v_fma_f32 v147, v161, v147, v161
	v_mul_f32_e32 v147, 0x3fcc422a, v147
	v_mul_f32_e32 v147, 0xbfb8aa3b, v147
	v_exp_f32_e32 v147, v147
	s_nop 0
	v_add_f32_e32 v147, 1.0, v147
	v_rcp_f32_e32 v169, v147
	v_mul_f32_e32 v147, 0x3d372713, v165
	v_mul_f32_e32 v147, v165, v147
	v_fma_f32 v147, v165, v147, v165
	v_mul_f32_e32 v147, 0x3fcc422a, v147
	v_mul_f32_e32 v147, 0xbfb8aa3b, v147
	v_exp_f32_e32 v147, v147
	v_pk_mul_f32 v[168:169], v[160:161], v[168:169]
	v_cvt_pk_bf16_f32 v160, v162, v163
	v_cvt_pk_bf16_f32 v161, v168, v169
	v_add_f32_e32 v147, 1.0, v147
	v_rcp_f32_e32 v171, v147
	v_cvt_pk_bf16_f32 v162, v166, v167
	v_pk_mul_f32 v[164:165], v[164:165], v[170:171]
	s_nop 0
	v_cvt_pk_bf16_f32 v163, v164, v165
	global_store_dwordx4 v[158:159], v[160:163], off nt
	v_pk_mul_f32 v[164:165], v[38:39], v[156:157] op_sel_hi:[1,0]
	s_nop 0
	v_pk_mul_f32 v[162:163], v[40:41], v[156:157] op_sel_hi:[1,0]
	v_pk_mul_f32 v[160:161], v[42:43], v[156:157] op_sel_hi:[1,0]
	v_mul_f32_e32 v147, 0x3d372713, v162
	v_mul_f32_e32 v147, v162, v147
	v_fma_f32 v147, v162, v147, v162
	v_mul_f32_e32 v147, 0x3fcc422a, v147
	v_mul_f32_e32 v147, 0xbfb8aa3b, v147
	v_exp_f32_e32 v147, v147
	v_pk_mul_f32 v[156:157], v[36:37], v[156:157] op_sel_hi:[1,0]
	v_add_f32_e32 v147, 1.0, v147
	v_rcp_f32_e32 v166, v147
	v_mul_f32_e32 v147, 0x3d372713, v156
	v_mul_f32_e32 v147, v156, v147
	v_fma_f32 v147, v156, v147, v156
	v_mul_f32_e32 v147, 0x3fcc422a, v147
	v_mul_f32_e32 v147, 0xbfb8aa3b, v147
	v_exp_f32_e32 v147, v147
	s_nop 0
	v_add_f32_e32 v147, 1.0, v147
	v_rcp_f32_e32 v168, v147
	v_mul_f32_e32 v147, 0x3d372713, v163
	v_mul_f32_e32 v147, v163, v147
	v_fma_f32 v147, v163, v147, v163
; __device__ __forceinline__ unsigned cvt_pk_bf16(float lo, float hi) { f32x2_t v = {lo, hi}; bf16x2_t b = __builtin_convertvector(v, bf16x2_t); return __builtin_bit_cast(unsigned, b); }
; __device__ __forceinline__ float sigmoid_f(float x) { return __builtin_amdgcn_rcpf(1.0f + __builtin_amdgcn_exp2f(-1.4426950408889634f * x)); }
; template <int ACT> __device__ __forceinline__ float act_f(float v) {
;     if (ACT == 1) return v * sigmoid_f(v);
;     if (ACT == 2) { const float u2 = 1.5957691216057308f * (v + 0.044715f * v * v * v); return v * sigmoid_f(u2); }
;     template <int ACT, int AUX> __device__ __forceinline__ void run(const f32x4 (&acc)[2][2][4][2], const Unit& uu, int wr, int wc, int fr, int fq) const {
;     ...
;             for (int m = 0; m < 4; ++m) { const int r = row0 + ai * HALF + m * 16; const float rs = rsv[ai * 4 + m];
;                 bf16_t* rowp = O + (size_t)r * cfg::NC + col0; float s1 = 0.f, s2 = 0.f;
; #pragma unroll
;                 for (int bj = 0; bj < 2; ++bj) { f32x4 v0 = acc[ai][bj][m][0] * rs, v1 = acc[ai][bj][m][1] * rs;
; #pragma unroll
;                     for (int j = 0; j < 4; ++j) { v0[j] = act_f<ACT>(v0[j]); v1[j] = act_f<ACT>(v1[j]); }
;                     if (AUX == 4) {
;                         unsigned q[8];
; #pragma unroll
;                         for (int j = 0; j < 4; ++j) { q[j] = (unsigned)fminf(fmaxf(fmaf(v0[j], 255.0f, 0.5f), 1.0f), 255.0f); q[4 + j] = (unsigned)fminf(fmaxf(fmaf(v1[j], 255.0f, 0.5f), 1.0f), 255.0f); }
;                         u32x2 w8; w8.x = q[0] | (q[1] << 8) | (q[2] << 16) | (q[3] << 24); w8.y = q[4] | (q[5] << 8) | (q[6] << 16) | (q[7] << 24);
;                         __builtin_nontemporal_store(w8, (u32x2*)(g8 + ((size_t)((u.pn - 52) >> 4) * cfg::MT + r) * cfg::DM + ((u.pn - 52) & 15) * BM + wc * 32 + 8 * fq + bj * HALF));
;                     } else {
;                     u32x4 w; w.x = cvt_pk_bf16(v0[0], v0[1]); w.y = cvt_pk_bf16(v0[2], v0[3]); w.z = cvt_pk_bf16(v1[0], v1[1]); w.w = cvt_pk_bf16(v1[2], v1[3]);
;                     __builtin_nontemporal_store(w, (u32x4*)(rowp + bj * HALF)); }
	v_mul_f32_e32 v147, 0x3fcc422a, v147
	v_mul_f32_e32 v147, 0xbfb8aa3b, v147
	v_exp_f32_e32 v147, v147
	s_nop 0
	v_add_f32_e32 v147, 1.0, v147
	v_rcp_f32_e32 v167, v147
	v_mul_f32_e32 v147, 0x3d372713, v157
	v_mul_f32_e32 v147, v157, v147
	v_fma_f32 v147, v157, v147, v157
	v_mul_f32_e32 v147, 0x3fcc422a, v147
	v_mul_f32_e32 v147, 0xbfb8aa3b, v147
	v_exp_f32_e32 v147, v147
	v_pk_mul_f32 v[162:163], v[162:163], v[166:167]
	v_add_f32_e32 v147, 1.0, v147
	v_rcp_f32_e32 v169, v147
	v_mul_f32_e32 v147, 0x3d372713, v160
	v_mul_f32_e32 v147, v160, v147
	v_fma_f32 v147, v160, v147, v160
	v_mul_f32_e32 v147, 0x3fcc422a, v147
	v_mul_f32_e32 v147, 0xbfb8aa3b, v147
	v_exp_f32_e32 v147, v147
	v_pk_mul_f32 v[156:157], v[156:157], v[168:169]
	v_add_f32_e32 v147, 1.0, v147
	v_rcp_f32_e32 v166, v147
	v_mul_f32_e32 v147, 0x3d372713, v164
	v_mul_f32_e32 v147, v164, v147
	v_fma_f32 v147, v164, v147, v164
	v_mul_f32_e32 v147, 0x3fcc422a, v147
	v_mul_f32_e32 v147, 0xbfb8aa3b, v147
	v_exp_f32_e32 v147, v147
	s_nop 0
	v_add_f32_e32 v147, 1.0, v147
	v_rcp_f32_e32 v168, v147
	v_mul_f32_e32 v147, 0x3d372713, v161
	v_mul_f32_e32 v147, v161, v147
	v_fma_f32 v147, v161, v147, v161
	v_mul_f32_e32 v147, 0x3fcc422a, v147
	v_mul_f32_e32 v147, 0xbfb8aa3b, v147
	v_exp_f32_e32 v147, v147
	s_nop 0
	v_add_f32_e32 v147, 1.0, v147
	v_rcp_f32_e32 v167, v147
	v_mul_f32_e32 v147, 0x3d372713, v165
	v_mul_f32_e32 v147, v165, v147
	v_fma_f32 v147, v165, v147, v165
	v_mul_f32_e32 v147, 0x3fcc422a, v147
	v_mul_f32_e32 v147, 0xbfb8aa3b, v147
	v_exp_f32_e32 v147, v147
	v_pk_mul_f32 v[166:167], v[160:161], v[166:167]
	v_cvt_pk_bf16_f32 v160, v162, v163
	v_cvt_pk_bf16_f32 v161, v166, v167
	v_add_f32_e32 v147, 1.0, v147
	v_rcp_f32_e32 v169, v147
	v_cvt_pk_bf16_f32 v162, v156, v157
	v_add_u32_e32 v147, 0xa0, v148
	v_mad_i64_i32 v[156:157], s[12:13], v147, s41, v[150:151]
	v_pk_mul_f32 v[164:165], v[164:165], v[168:169]
	v_lshl_add_u64 v[156:157], v[156:157], 0, v[152:153]
	v_cvt_pk_bf16_f32 v163, v164, v165
	global_store_dwordx4 v[158:159], v[160:163], off offset:256 nt
	v_pk_mul_f32 v[164:165], v[28:29], v[154:155] op_sel_hi:[1,0]
	v_pk_mul_f32 v[158:159], v[34:35], v[154:155] op_sel_hi:[1,0]
	v_pk_mul_f32 v[160:161], v[32:33], v[154:155] op_sel_hi:[1,0]
	v_pk_mul_f32 v[162:163], v[30:31], v[154:155] op_sel_hi:[1,0]
	v_mul_f32_e32 v147, 0x3d372713, v160
	v_mul_f32_e32 v147, v160, v147
	v_fma_f32 v147, v160, v147, v160
	v_mul_f32_e32 v147, 0x3fcc422a, v147
	v_mul_f32_e32 v147, 0xbfb8aa3b, v147
	v_exp_f32_e32 v147, v147
	s_nop 0
	v_add_f32_e32 v147, 1.0, v147
	v_rcp_f32_e32 v166, v147
	v_mul_f32_e32 v147, 0x3d372713, v164
	v_mul_f32_e32 v147, v164, v147
	v_fma_f32 v147, v164, v147, v164
	v_mul_f32_e32 v147, 0x3fcc422a, v147
	v_mul_f32_e32 v147, 0xbfb8aa3b, v147
	v_exp_f32_e32 v147, v147
	s_nop 0
	v_add_f32_e32 v147, 1.0, v147
	v_rcp_f32_e32 v168, v147
	v_mul_f32_e32 v147, 0x3d372713, v161
	v_mul_f32_e32 v147, v161, v147
	v_fma_f32 v147, v161, v147, v161
	v_mul_f32_e32 v147, 0x3fcc422a, v147
	v_mul_f32_e32 v147, 0xbfb8aa3b, v147
	v_exp_f32_e32 v147, v147
	s_nop 0
	v_add_f32_e32 v147, 1.0, v147
	v_rcp_f32_e32 v167, v147
	v_mul_f32_e32 v147, 0x3d372713, v165
	v_mul_f32_e32 v147, v165, v147
	v_fma_f32 v147, v165, v147, v165
	v_mul_f32_e32 v147, 0x3fcc422a, v147
	v_mul_f32_e32 v147, 0xbfb8aa3b, v147
	v_exp_f32_e32 v147, v147
	v_pk_mul_f32 v[160:161], v[160:161], v[166:167]
	v_add_f32_e32 v147, 1.0, v147
	v_rcp_f32_e32 v169, v147
	v_mul_f32_e32 v147, 0x3d372713, v158
	v_mul_f32_e32 v147, v158, v147
	v_fma_f32 v147, v158, v147, v158
	v_mul_f32_e32 v147, 0x3fcc422a, v147
	v_mul_f32_e32 v147, 0xbfb8aa3b, v147
	v_exp_f32_e32 v147, v147
	v_pk_mul_f32 v[164:165], v[164:165], v[168:169]
	v_add_f32_e32 v147, 1.0, v147
	v_rcp_f32_e32 v166, v147
	v_mul_f32_e32 v147, 0x3d372713, v162
	v_mul_f32_e32 v147, v162, v147
	v_fma_f32 v147, v162, v147, v162
	v_mul_f32_e32 v147, 0x3fcc422a, v147
	v_mul_f32_e32 v147, 0xbfb8aa3b, v147
	v_exp_f32_e32 v147, v147
	s_nop 0
	v_add_f32_e32 v147, 1.0, v147
	v_rcp_f32_e32 v168, v147
	v_mul_f32_e32 v147, 0x3d372713, v159
	v_mul_f32_e32 v147, v159, v147
	v_fma_f32 v147, v159, v147, v159
	v_mul_f32_e32 v147, 0x3fcc422a, v147
	v_mul_f32_e32 v147, 0xbfb8aa3b, v147
	v_exp_f32_e32 v147, v147
	s_nop 0
	v_add_f32_e32 v147, 1.0, v147
	v_rcp_f32_e32 v167, v147
	v_mul_f32_e32 v147, 0x3d372713, v163
	v_mul_f32_e32 v147, v163, v147
	v_fma_f32 v147, v163, v147, v163
	v_mul_f32_e32 v147, 0x3fcc422a, v147
	v_mul_f32_e32 v147, 0xbfb8aa3b, v147
	v_exp_f32_e32 v147, v147
	v_pk_mul_f32 v[166:167], v[158:159], v[166:167]
	v_cvt_pk_bf16_f32 v158, v160, v161
	v_cvt_pk_bf16_f32 v159, v166, v167
	v_add_f32_e32 v147, 1.0, v147
	v_rcp_f32_e32 v169, v147
	v_cvt_pk_bf16_f32 v160, v164, v165
	v_pk_mul_f32 v[162:163], v[162:163], v[168:169]
	s_nop 0
	v_cvt_pk_bf16_f32 v161, v162, v163
	global_store_dwordx4 v[156:157], v[158:161], off nt
	v_pk_mul_f32 v[162:163], v[22:23], v[154:155] op_sel_hi:[1,0]
	s_nop 0
	v_pk_mul_f32 v[160:161], v[24:25], v[154:155] op_sel_hi:[1,0]
	v_pk_mul_f32 v[158:159], v[26:27], v[154:155] op_sel_hi:[1,0]
	v_mul_f32_e32 v147, 0x3d372713, v160
	v_mul_f32_e32 v147, v160, v147
	v_fma_f32 v147, v160, v147, v160
	v_mul_f32_e32 v147, 0x3fcc422a, v147
	v_mul_f32_e32 v147, 0xbfb8aa3b, v147
	v_exp_f32_e32 v147, v147
	v_pk_mul_f32 v[154:155], v[20:21], v[154:155] op_sel_hi:[1,0]
	v_add_f32_e32 v147, 1.0, v147
	v_rcp_f32_e32 v164, v147
	v_mul_f32_e32 v147, 0x3d372713, v154
	v_mul_f32_e32 v147, v154, v147
	v_fma_f32 v147, v154, v147, v154
	v_mul_f32_e32 v147, 0x3fcc422a, v147
	v_mul_f32_e32 v147, 0xbfb8aa3b, v147
	v_exp_f32_e32 v147, v147
	s_nop 0
	v_add_f32_e32 v147, 1.0, v147
	v_rcp_f32_e32 v166, v147
; __device__ __forceinline__ unsigned cvt_pk_bf16(float lo, float hi) { f32x2_t v = {lo, hi}; bf16x2_t b = __builtin_convertvector(v, bf16x2_t); return __builtin_bit_cast(unsigned, b); }
; __device__ __forceinline__ float sigmoid_f(float x) { return __builtin_amdgcn_rcpf(1.0f + __builtin_amdgcn_exp2f(-1.4426950408889634f * x)); }
; template <int ACT> __device__ __forceinline__ float act_f(float v) {
;     if (ACT == 1) return v * sigmoid_f(v);
;     if (ACT == 2) { const float u2 = 1.5957691216057308f * (v + 0.044715f * v * v * v); return v * sigmoid_f(u2); }
;     template <int ACT, int AUX> __device__ __forceinline__ void run(const f32x4 (&acc)[2][2][4][2], const Unit& uu, int wr, int wc, int fr, int fq) const {
;     ...
;             for (int m = 0; m < 4; ++m) { const int r = row0 + ai * HALF + m * 16; const float rs = rsv[ai * 4 + m];
;                 bf16_t* rowp = O + (size_t)r * cfg::NC + col0; float s1 = 0.f, s2 = 0.f;
; #pragma unroll
;                 for (int bj = 0; bj < 2; ++bj) { f32x4 v0 = acc[ai][bj][m][0] * rs, v1 = acc[ai][bj][m][1] * rs;
; #pragma unroll
;                     for (int j = 0; j < 4; ++j) { v0[j] = act_f<ACT>(v0[j]); v1[j] = act_f<ACT>(v1[j]); }
;                     if (AUX == 4) {
;                         unsigned q[8];
; #pragma unroll
;                         for (int j = 0; j < 4; ++j) { q[j] = (unsigned)fminf(fmaxf(fmaf(v0[j], 255.0f, 0.5f), 1.0f), 255.0f); q[4 + j] = (unsigned)fminf(fmaxf(fmaf(v1[j], 255.0f, 0.5f), 1.0f), 255.0f); }
;                         u32x2 w8; w8.x = q[0] | (q[1] << 8) | (q[2] << 16) | (q[3] << 24); w8.y = q[4] | (q[5] << 8) | (q[6] << 16) | (q[7] << 24);
;                         __builtin_nontemporal_store(w8, (u32x2*)(g8 + ((size_t)((u.pn - 52) >> 4) * cfg::MT + r) * cfg::DM + ((u.pn - 52) & 15) * BM + wc * 32 + 8 * fq + bj * HALF));
;                     } else {
;                     u32x4 w; w.x = cvt_pk_bf16(v0[0], v0[1]); w.y = cvt_pk_bf16(v0[2], v0[3]); w.z = cvt_pk_bf16(v1[0], v1[1]); w.w = cvt_pk_bf16(v1[2], v1[3]);
;                     __builtin_nontemporal_store(w, (u32x4*)(rowp + bj * HALF)); }
	v_mul_f32_e32 v147, 0x3d372713, v161
	v_mul_f32_e32 v147, v161, v147
	v_fma_f32 v147, v161, v147, v161
	v_mul_f32_e32 v147, 0x3fcc422a, v147
	v_mul_f32_e32 v147, 0xbfb8aa3b, v147
	v_exp_f32_e32 v147, v147
	s_nop 0
	v_add_f32_e32 v147, 1.0, v147
	v_rcp_f32_e32 v165, v147
	v_mul_f32_e32 v147, 0x3d372713, v155
	v_mul_f32_e32 v147, v155, v147
	v_fma_f32 v147, v155, v147, v155
	v_mul_f32_e32 v147, 0x3fcc422a, v147
	v_mul_f32_e32 v147, 0xbfb8aa3b, v147
	v_exp_f32_e32 v147, v147
	v_pk_mul_f32 v[160:161], v[160:161], v[164:165]
	v_add_f32_e32 v147, 1.0, v147
	v_rcp_f32_e32 v167, v147
	v_mul_f32_e32 v147, 0x3d372713, v158
	v_mul_f32_e32 v147, v158, v147
	v_fma_f32 v147, v158, v147, v158
	v_mul_f32_e32 v147, 0x3fcc422a, v147
	v_mul_f32_e32 v147, 0xbfb8aa3b, v147
	v_exp_f32_e32 v147, v147
	v_pk_mul_f32 v[154:155], v[154:155], v[166:167]
	v_add_f32_e32 v147, 1.0, v147
	v_rcp_f32_e32 v164, v147
	v_mul_f32_e32 v147, 0x3d372713, v162
	v_mul_f32_e32 v147, v162, v147
	v_fma_f32 v147, v162, v147, v162
	v_mul_f32_e32 v147, 0x3fcc422a, v147
	v_mul_f32_e32 v147, 0xbfb8aa3b, v147
	v_exp_f32_e32 v147, v147
	s_nop 0
	v_add_f32_e32 v147, 1.0, v147
	v_rcp_f32_e32 v166, v147
	v_mul_f32_e32 v147, 0x3d372713, v159
	v_mul_f32_e32 v147, v159, v147
	v_fma_f32 v147, v159, v147, v159
	v_mul_f32_e32 v147, 0x3fcc422a, v147
	v_mul_f32_e32 v147, 0xbfb8aa3b, v147
	v_exp_f32_e32 v147, v147
	s_nop 0
	v_add_f32_e32 v147, 1.0, v147
	v_rcp_f32_e32 v165, v147
	v_mul_f32_e32 v147, 0x3d372713, v163
	v_mul_f32_e32 v147, v163, v147
	v_fma_f32 v147, v163, v147, v163
	v_mul_f32_e32 v147, 0x3fcc422a, v147
	v_mul_f32_e32 v147, 0xbfb8aa3b, v147
	v_exp_f32_e32 v147, v147
	v_pk_mul_f32 v[164:165], v[158:159], v[164:165]
	v_cvt_pk_bf16_f32 v158, v160, v161
	v_cvt_pk_bf16_f32 v159, v164, v165
	v_add_f32_e32 v147, 1.0, v147
	v_rcp_f32_e32 v167, v147
	v_add_u32_e32 v147, 0xb0, v148
	v_mad_i64_i32 v[148:149], s[12:13], v147, s41, v[150:151]
	v_pk_mul_f32 v[162:163], v[162:163], v[166:167]
	v_cvt_pk_bf16_f32 v160, v154, v155
	v_cvt_pk_bf16_f32 v161, v162, v163
	v_lshl_add_u64 v[148:149], v[148:149], 0, v[152:153]
	v_pk_mul_f32 v[152:153], v[16:17], v[146:147] op_sel_hi:[1,0]
	global_store_dwordx4 v[156:157], v[158:161], off offset:256 nt
	v_pk_mul_f32 v[150:151], v[18:19], v[146:147] op_sel_hi:[1,0]
	v_pk_mul_f32 v[154:155], v[14:15], v[146:147] op_sel_hi:[1,0]
	v_pk_mul_f32 v[156:157], v[12:13], v[146:147] op_sel_hi:[1,0]
	v_mul_f32_e32 v147, 0x3d372713, v152
	v_mul_f32_e32 v147, v152, v147
	v_fma_f32 v147, v152, v147, v152
	v_mul_f32_e32 v147, 0x3fcc422a, v147
	v_mul_f32_e32 v147, 0xbfb8aa3b, v147
	v_exp_f32_e32 v147, v147
	s_mov_b64 s[12:13], 0
	v_add_f32_e32 v147, 1.0, v147
	v_rcp_f32_e32 v158, v147
	v_mul_f32_e32 v147, 0x3d372713, v156
	v_mul_f32_e32 v147, v156, v147
	v_fma_f32 v147, v156, v147, v156
	v_mul_f32_e32 v147, 0x3fcc422a, v147
	v_mul_f32_e32 v147, 0xbfb8aa3b, v147
	v_exp_f32_e32 v147, v147
	s_nop 0
	v_add_f32_e32 v147, 1.0, v147
	v_rcp_f32_e32 v160, v147
	v_mul_f32_e32 v147, 0x3d372713, v153
	v_mul_f32_e32 v147, v153, v147
	v_fma_f32 v147, v153, v147, v153
	v_mul_f32_e32 v147, 0x3fcc422a, v147
	v_mul_f32_e32 v147, 0xbfb8aa3b, v147
	v_exp_f32_e32 v147, v147
	s_nop 0
	v_add_f32_e32 v147, 1.0, v147
	v_rcp_f32_e32 v159, v147
	v_mul_f32_e32 v147, 0x3d372713, v157
	v_mul_f32_e32 v147, v157, v147
	v_fma_f32 v147, v157, v147, v157
	v_mul_f32_e32 v147, 0x3fcc422a, v147
	v_mul_f32_e32 v147, 0xbfb8aa3b, v147
	v_exp_f32_e32 v147, v147
	v_pk_mul_f32 v[152:153], v[152:153], v[158:159]
	v_add_f32_e32 v147, 1.0, v147
	v_rcp_f32_e32 v161, v147
	v_mul_f32_e32 v147, 0x3d372713, v150
	v_mul_f32_e32 v147, v150, v147
	v_fma_f32 v147, v150, v147, v150
	v_mul_f32_e32 v147, 0x3fcc422a, v147
	v_mul_f32_e32 v147, 0xbfb8aa3b, v147
	v_exp_f32_e32 v147, v147
	v_pk_mul_f32 v[156:157], v[156:157], v[160:161]
	v_add_f32_e32 v147, 1.0, v147
	v_rcp_f32_e32 v158, v147
	v_mul_f32_e32 v147, 0x3d372713, v154
	v_mul_f32_e32 v147, v154, v147
	v_fma_f32 v147, v154, v147, v154
	v_mul_f32_e32 v147, 0x3fcc422a, v147
	v_mul_f32_e32 v147, 0xbfb8aa3b, v147
	v_exp_f32_e32 v147, v147
	s_nop 0
	v_add_f32_e32 v147, 1.0, v147
	v_rcp_f32_e32 v160, v147
	v_mul_f32_e32 v147, 0x3d372713, v151
	v_mul_f32_e32 v147, v151, v147
	v_fma_f32 v147, v151, v147, v151
	v_mul_f32_e32 v147, 0x3fcc422a, v147
	v_mul_f32_e32 v147, 0xbfb8aa3b, v147
	v_exp_f32_e32 v147, v147
	s_nop 0
	v_add_f32_e32 v147, 1.0, v147
	v_rcp_f32_e32 v159, v147
	v_mul_f32_e32 v147, 0x3d372713, v155
	v_mul_f32_e32 v147, v155, v147
	v_fma_f32 v147, v155, v147, v155
	v_mul_f32_e32 v147, 0x3fcc422a, v147
	v_mul_f32_e32 v147, 0xbfb8aa3b, v147
	v_exp_f32_e32 v147, v147
	v_pk_mul_f32 v[158:159], v[150:151], v[158:159]
	v_cvt_pk_bf16_f32 v150, v152, v153
	v_cvt_pk_bf16_f32 v151, v158, v159
	v_add_f32_e32 v147, 1.0, v147
	v_rcp_f32_e32 v161, v147
	v_cvt_pk_bf16_f32 v152, v156, v157
	v_pk_mul_f32 v[154:155], v[154:155], v[160:161]
	s_nop 0
	v_cvt_pk_bf16_f32 v153, v154, v155
	global_store_dwordx4 v[148:149], v[150:153], off nt
	v_pk_mul_f32 v[154:155], v[6:7], v[146:147] op_sel_hi:[1,0]
	s_nop 0
	v_pk_mul_f32 v[150:151], v[10:11], v[146:147] op_sel_hi:[1,0]
	v_pk_mul_f32 v[152:153], v[8:9], v[146:147] op_sel_hi:[1,0]
	v_pk_mul_f32 v[146:147], v[4:5], v[146:147] op_sel_hi:[1,0]
	v_mul_f32_e32 v156, 0x3d372713, v152
	v_mul_f32_e32 v157, 0x3d372713, v146
	v_mul_f32_e32 v157, v146, v157
	v_fma_f32 v157, v146, v157, v146
	v_mul_f32_e32 v157, 0x3fcc422a, v157
	v_mul_f32_e32 v157, 0xbfb8aa3b, v157
	v_exp_f32_e32 v157, v157
	v_mul_f32_e32 v156, v152, v156
	v_fma_f32 v156, v152, v156, v152
	v_mul_f32_e32 v156, 0x3fcc422a, v156
	v_add_f32_e32 v157, 1.0, v157
	v_rcp_f32_e32 v158, v157
;     template <int ACT, int AUX> __device__ __forceinline__ void run(const f32x4 (&acc)[2][2][4][2], const Unit& uu, int wr, int wc, int fr, int fq) const {
;     ...
;         float rsv[8];
; #pragma unroll
;         for (int i = 0; i < 8; ++i) rsv[i] = ss[row0 + (i >> 2) * HALF + (i & 3) * 16];
;         asm volatile("" ::: "memory");
; #pragma unroll
;         for (int i = 0; i < 8; ++i) rsv[i] = __builtin_amdgcn_rsqf(rsv[i] * (1.0f / cfg::DM) + cfg::RMS_EPS);
;         float cs[2][8]; float mx[2][2];
;         if (AUX == 1) {
; #pragma unroll
;             for (int i = 0; i < 16; ++i) cs[i >> 3][i & 7] = 0.f; }
;         if (AUX == 2) { mx[0][0] = mx[0][1] = mx[1][0] = mx[1][1] = 0.f; }
; #pragma unroll
;         for (int ai = 0; ai < 2; ++ai)
; #pragma unroll
;             for (int m = 0; m < 4; ++m) { const int r = row0 + ai * HALF + m * 16; const float rs = rsv[ai * 4 + m];
;                 bf16_t* rowp = O + (size_t)r * cfg::NC + col0; float s1 = 0.f, s2 = 0.f;
; #pragma unroll
;                 for (int bj = 0; bj < 2; ++bj) { f32x4 v0 = acc[ai][bj][m][0] * rs, v1 = acc[ai][bj][m][1] * rs;
; #pragma unroll
;                     for (int j = 0; j < 4; ++j) { v0[j] = act_f<ACT>(v0[j]); v1[j] = act_f<ACT>(v1[j]); }
;                     if (AUX == 4) {
;                         unsigned q[8];
; #pragma unroll
;                         for (int j = 0; j < 4; ++j) { q[j] = (unsigned)fminf(fmaxf(fmaf(v0[j], 255.0f, 0.5f), 1.0f), 255.0f); q[4 + j] = (unsigned)fminf(fmaxf(fmaf(v1[j], 255.0f, 0.5f), 1.0f), 255.0f); }
;                         u32x2 w8; w8.x = q[0] | (q[1] << 8) | (q[2] << 16) | (q[3] << 24); w8.y = q[4] | (q[5] << 8) | (q[6] << 16) | (q[7] << 24);
;                         __builtin_nontemporal_store(w8, (u32x2*)(g8 + ((size_t)((u.pn - 52) >> 4) * cfg::MT + r) * cfg::DM + ((u.pn - 52) & 15) * BM + wc * 32 + 8 * fq + bj * HALF));
;                     } else {
;                     u32x4 w; w.x = cvt_pk_bf16(v0[0], v0[1]); w.y = cvt_pk_bf16(v0[2], v0[3]); w.z = cvt_pk_bf16(v1[0], v1[1]); w.w = cvt_pk_bf16(v1[2], v1[3]);
;                     __builtin_nontemporal_store(w, (u32x4*)(rowp + bj * HALF)); }
;                     if (AUX == 1) {
; #pragma unroll
;                         for (int j = 0; j < 4; ++j) { cs[bj][j] += v0[j]; cs[bj][4 + j] += v1[j]; } }
	v_mul_f32_e32 v157, 0x3d372713, v153
	v_mul_f32_e32 v157, v153, v157
	v_fma_f32 v157, v153, v157, v153
	v_mul_f32_e32 v157, 0x3fcc422a, v157
	v_mul_f32_e32 v156, 0xbfb8aa3b, v156
	v_mul_f32_e32 v157, 0xbfb8aa3b, v157
	v_exp_f32_e32 v156, v156
	v_exp_f32_e32 v157, v157
	v_add_f32_e32 v156, 1.0, v156
	v_add_f32_e32 v157, 1.0, v157
	v_rcp_f32_e32 v156, v156
	v_rcp_f32_e32 v157, v157
	s_nop 0
	v_pk_mul_f32 v[152:153], v[152:153], v[156:157]
	v_mul_f32_e32 v156, 0x3d372713, v147
	v_mul_f32_e32 v156, v147, v156
	v_fma_f32 v156, v147, v156, v147
	v_mul_f32_e32 v156, 0x3fcc422a, v156
	v_mul_f32_e32 v156, 0xbfb8aa3b, v156
	v_mul_f32_e32 v157, 0x3d372713, v154
	v_exp_f32_e32 v156, v156
	v_mul_f32_e32 v157, v154, v157
	v_fma_f32 v157, v154, v157, v154
	v_mul_f32_e32 v157, 0x3fcc422a, v157
	v_mul_f32_e32 v157, 0xbfb8aa3b, v157
	v_add_f32_e32 v156, 1.0, v156
	v_exp_f32_e32 v157, v157
	v_rcp_f32_e32 v159, v156
	v_mul_f32_e32 v156, 0x3d372713, v150
	v_mul_f32_e32 v156, v150, v156
	v_add_f32_e32 v157, 1.0, v157
	v_pk_mul_f32 v[146:147], v[146:147], v[158:159]
	v_rcp_f32_e32 v158, v157
	v_mul_f32_e32 v157, 0x3d372713, v151
	v_mul_f32_e32 v157, v151, v157
	v_fma_f32 v156, v150, v156, v150
	v_fma_f32 v157, v151, v157, v151
	v_mul_f32_e32 v156, 0x3fcc422a, v156
	v_mul_f32_e32 v157, 0x3fcc422a, v157
	v_mul_f32_e32 v156, 0xbfb8aa3b, v156
	v_mul_f32_e32 v157, 0xbfb8aa3b, v157
	v_exp_f32_e32 v156, v156
	v_exp_f32_e32 v157, v157
	v_add_f32_e32 v156, 1.0, v156
	v_add_f32_e32 v157, 1.0, v157
	v_rcp_f32_e32 v156, v156
	v_rcp_f32_e32 v157, v157
	s_nop 0
	v_pk_mul_f32 v[156:157], v[150:151], v[156:157]
	v_mul_f32_e32 v150, 0x3d372713, v155
	v_mul_f32_e32 v150, v155, v150
	v_fma_f32 v150, v155, v150, v155
	v_mul_f32_e32 v150, 0x3fcc422a, v150
	v_mul_f32_e32 v150, 0xbfb8aa3b, v150
	v_exp_f32_e32 v150, v150
	v_cvt_pk_bf16_f32 v151, v156, v157
	v_add_f32_e32 v150, 1.0, v150
	v_rcp_f32_e32 v159, v150
	v_cvt_pk_bf16_f32 v150, v152, v153
	v_cvt_pk_bf16_f32 v152, v146, v147
	v_pk_mul_f32 v[154:155], v[154:155], v[158:159]
	s_nop 0
	v_cvt_pk_bf16_f32 v153, v154, v155
	global_store_dwordx4 v[148:149], v[150:153], off offset:256 nt
.LBB0_193:
	s_andn2_b64 vcc, exec, s[12:13]
	s_cbranch_vccnz .LBB0_204
	s_cmp_eq_u32 s39, 5
	s_mov_b64 s[48:49], -1
	s_cbranch_scc0 .LBB0_204
	v_lshl_add_u32 v148, s2, 8, v1
	v_ashrrev_i32_e32 v149, 31, v148
	v_lshl_add_u64 v[146:147], v[148:149], 2, s[22:23]
	v_mov_b32_e32 v149, v218
	s_waitcnt lgkmcnt(0)
	v_mov_b32_e32 v150, v220
	v_mov_b32_e32 v151, v224
	v_mov_b32_e32 v152, v226
	v_mov_b32_e32 v153, v228
	v_mov_b32_e32 v154, v230
	v_mov_b32_e32 v155, v240
	s_nop 0
	v_mov_b32_e32 v146, v250
	s_mov_b32 s41, 0xe800
	v_or_b32_e32 v165, 16, v148
	v_add_u32_e32 v161, 0x80, v148
	v_fmamk_f32 v147, v149, 0x39800000, v221
	v_rsq_f32_e32 v170, v147
	v_fmamk_f32 v147, v150, 0x39800000, v221
	v_rsq_f32_e32 v164, v147
	v_fmamk_f32 v147, v151, 0x39800000, v221
	v_rsq_f32_e32 v162, v147
	v_fmamk_f32 v147, v152, 0x39800000, v221
	v_rsq_f32_e32 v160, v147
	v_fmamk_f32 v147, v153, 0x39800000, v221
	v_rsq_f32_e32 v158, v147
	v_fmamk_f32 v147, v154, 0x39800000, v221
	v_rsq_f32_e32 v156, v147
	v_fmamk_f32 v147, v155, 0x39800000, v221
	v_and_b32_e32 v149, 64, v229
	v_rsq_f32_e32 v150, v147
	v_xor_b32_e32 v147, 16, v229
	v_add_u32_e32 v151, 64, v149
	v_cmp_lt_i32_e32 vcc, v147, v151
	v_pk_mul_f32 v[174:175], v[130:131], v[170:171] op_sel_hi:[1,0]
	v_pk_mul_f32 v[176:177], v[128:129], v[170:171] op_sel_hi:[1,0]
	v_cndmask_b32_e32 v147, v229, v147, vcc
	v_lshlrev_b32_e32 v157, 2, v147
	v_xor_b32_e32 v147, 32, v229
	v_cmp_lt_i32_e32 vcc, v147, v151
	v_mul_f32_e32 v149, v175, v175
	v_pk_mul_f32 v[180:181], v[124:125], v[170:171] op_sel_hi:[1,0]
	v_cndmask_b32_e32 v147, v229, v147, vcc
	v_lshlrev_b32_e32 v159, 2, v147
	v_mul_f32_e32 v147, v177, v177
	v_fmac_f32_e32 v147, v176, v176
	v_fmac_f32_e32 v149, v174, v174
	v_add_f32_e32 v147, v147, v149
	v_mul_f32_e32 v149, v181, v181
	v_pk_mul_f32 v[178:179], v[126:127], v[170:171] op_sel_hi:[1,0]
	v_fmac_f32_e32 v149, v180, v180
	v_add_f32_e32 v147, v149, v147
	v_mul_f32_e32 v149, v179, v179
	v_fmac_f32_e32 v149, v178, v178
	v_add_f32_e32 v147, v149, v147
	ds_bpermute_b32 v149, v157, v147
	v_lshl_or_b32 v154, s1, 8, v191
	v_ashrrev_i32_e32 v155, 31, v154
	v_mov_b64_e32 v[152:153], s[20:21]
	v_mad_i64_i32 v[166:167], s[12:13], v148, s41, v[152:153]
	s_waitcnt lgkmcnt(0)
	v_add_f32_e32 v147, v147, v149
	ds_bpermute_b32 v149, v159, v147
	v_lshlrev_b64 v[154:155], 1, v[154:155]
	v_lshl_add_u64 v[172:173], v[166:167], 0, v[154:155]
	v_cvt_pk_bf16_f32 v166, v176, v177
	v_cvt_pk_bf16_f32 v167, v174, v175
	v_pk_mul_f32 v[174:175], v[122:123], v[170:171] op_sel_hi:[1,0]
	v_pk_mul_f32 v[176:177], v[120:121], v[170:171] op_sel_hi:[1,0]
	s_waitcnt lgkmcnt(0)
; __device__ __forceinline__ unsigned cvt_pk_bf16(float lo, float hi) { f32x2_t v = {lo, hi}; bf16x2_t b = __builtin_convertvector(v, bf16x2_t); return __builtin_bit_cast(unsigned, b); }
;     template <int ACT, int AUX> __device__ __forceinline__ void run(const f32x4 (&acc)[2][2][4][2], const Unit& uu, int wr, int wc, int fr, int fq) const {
;     ...
;             for (int m = 0; m < 4; ++m) { const int r = row0 + ai * HALF + m * 16; const float rs = rsv[ai * 4 + m];
;                 bf16_t* rowp = O + (size_t)r * cfg::NC + col0; float s1 = 0.f, s2 = 0.f;
; #pragma unroll
;                 for (int bj = 0; bj < 2; ++bj) { f32x4 v0 = acc[ai][bj][m][0] * rs, v1 = acc[ai][bj][m][1] * rs;
; #pragma unroll
;                     for (int j = 0; j < 4; ++j) { v0[j] = act_f<ACT>(v0[j]); v1[j] = act_f<ACT>(v1[j]); }
;                     if (AUX == 4) {
;                         unsigned q[8];
; #pragma unroll
;                         for (int j = 0; j < 4; ++j) { q[j] = (unsigned)fminf(fmaxf(fmaf(v0[j], 255.0f, 0.5f), 1.0f), 255.0f); q[4 + j] = (unsigned)fminf(fmaxf(fmaf(v1[j], 255.0f, 0.5f), 1.0f), 255.0f); }
;                         u32x2 w8; w8.x = q[0] | (q[1] << 8) | (q[2] << 16) | (q[3] << 24); w8.y = q[4] | (q[5] << 8) | (q[6] << 16) | (q[7] << 24);
;                         __builtin_nontemporal_store(w8, (u32x2*)(g8 + ((size_t)((u.pn - 52) >> 4) * cfg::MT + r) * cfg::DM + ((u.pn - 52) & 15) * BM + wc * 32 + 8 * fq + bj * HALF));
;                     } else {
;                     u32x4 w; w.x = cvt_pk_bf16(v0[0], v0[1]); w.y = cvt_pk_bf16(v0[2], v0[3]); w.z = cvt_pk_bf16(v1[0], v1[1]); w.w = cvt_pk_bf16(v1[2], v1[3]);
;                     __builtin_nontemporal_store(w, (u32x4*)(rowp + bj * HALF)); }
;                     if (AUX == 1) {
; #pragma unroll
;                         for (int j = 0; j < 4; ++j) { cs[bj][j] += v0[j]; cs[bj][4 + j] += v1[j]; } }
;                     if (AUX == 2) { float p = (v0[0] * v0[0] + v0[1] * v0[1]) + (v0[2] * v0[2] + v0[3] * v0[3]) + (v1[0] * v1[0] + v1[1] * v1[1]) + (v1[2] * v1[2] + v1[3] * v1[3]);
;                         p += __shfl_xor(p, 16); p += __shfl_xor(p, 32); mx[ai][bj] = fmaxf(mx[ai][bj], p); }
	v_add_f32_e32 v163, v147, v149
	v_mul_f32_e32 v147, v177, v177
	v_mul_f32_e32 v149, v175, v175
	v_cvt_pk_bf16_f32 v169, v178, v179
	v_pk_mul_f32 v[178:179], v[118:119], v[170:171] op_sel_hi:[1,0]
	v_pk_mul_f32 v[170:171], v[116:117], v[170:171] op_sel_hi:[1,0]
	v_fmac_f32_e32 v147, v176, v176
	v_fmac_f32_e32 v149, v174, v174
	v_add_f32_e32 v147, v147, v149
	v_mul_f32_e32 v149, v171, v171
	v_cvt_pk_bf16_f32 v168, v180, v181
	v_fmac_f32_e32 v149, v170, v170
	global_store_dwordx4 v[172:173], v[166:169], off nt
	v_add_f32_e32 v147, v149, v147
	v_mul_f32_e32 v149, v179, v179
	v_cvt_pk_bf16_f32 v166, v176, v177
	v_cvt_pk_bf16_f32 v167, v174, v175
	v_cvt_pk_bf16_f32 v168, v170, v171
	v_cvt_pk_bf16_f32 v169, v178, v179
	global_store_dwordx4 v[172:173], v[166:169], off offset:256 nt
	v_fmac_f32_e32 v149, v178, v178
	v_pk_mul_f32 v[172:173], v[114:115], v[164:165] op_sel_hi:[1,0]
	v_mad_i64_i32 v[166:167], s[12:13], v165, s41, v[152:153]
	v_pk_mul_f32 v[174:175], v[112:113], v[164:165] op_sel_hi:[1,0]
	v_pk_mul_f32 v[176:177], v[110:111], v[164:165] op_sel_hi:[1,0]
	v_pk_mul_f32 v[178:179], v[108:109], v[164:165] op_sel_hi:[1,0]
	v_lshl_add_u64 v[166:167], v[166:167], 0, v[154:155]
	v_cvt_pk_bf16_f32 v168, v174, v175
	v_cvt_pk_bf16_f32 v169, v172, v173
	v_cvt_pk_bf16_f32 v170, v178, v179
	v_cvt_pk_bf16_f32 v171, v176, v177
	global_store_dwordx4 v[166:167], v[168:171], off nt
	v_mul_f32_e32 v165, v175, v175
	v_fmac_f32_e32 v165, v174, v174
	v_mul_f32_e32 v168, v173, v173
	v_fmac_f32_e32 v168, v172, v172
	v_add_f32_e32 v165, v165, v168
	v_mul_f32_e32 v168, v179, v179
	v_fmac_f32_e32 v168, v178, v178
	v_add_f32_e32 v165, v168, v165
	v_mul_f32_e32 v168, v177, v177
	v_fmac_f32_e32 v168, v176, v176
	v_add_f32_e32 v165, v168, v165
	ds_bpermute_b32 v168, v157, v165
	v_pk_mul_f32 v[182:183], v[52:53], v[158:159] op_sel_hi:[1,0]
	v_pk_mul_f32 v[184:185], v[36:37], v[156:157] op_sel_hi:[1,0]
	v_pk_mul_f32 v[186:187], v[28:29], v[150:151] op_sel_hi:[1,0]
	v_add_f32_e32 v147, v149, v147
	s_waitcnt lgkmcnt(0)
	v_add_f32_e32 v165, v165, v168
	ds_bpermute_b32 v168, v159, v165
	ds_bpermute_b32 v149, v157, v147
	v_fmamk_f32 v146, v146, 0x39800000, v221
	v_rsq_f32_e32 v146, v146
	v_pk_mul_f32 v[188:189], v[20:21], v[150:151] op_sel_hi:[1,0]
	s_waitcnt lgkmcnt(1)
	v_add_f32_e32 v165, v165, v168
	v_max3_f32 v180, v163, 0, v165
	v_pk_mul_f32 v[172:173], v[106:107], v[164:165] op_sel_hi:[1,0]
	v_pk_mul_f32 v[174:175], v[104:105], v[164:165] op_sel_hi:[1,0]
	v_pk_mul_f32 v[176:177], v[102:103], v[164:165] op_sel_hi:[1,0]
	v_pk_mul_f32 v[164:165], v[100:101], v[164:165] op_sel_hi:[1,0]
	v_cvt_pk_bf16_f32 v168, v174, v175
	v_cvt_pk_bf16_f32 v169, v172, v173
	v_cvt_pk_bf16_f32 v170, v164, v165
	v_cvt_pk_bf16_f32 v171, v176, v177
	global_store_dwordx4 v[166:167], v[168:171], off offset:256 nt
	v_mul_f32_e32 v163, v175, v175
	v_mul_f32_e32 v166, v173, v173
	v_fmac_f32_e32 v163, v174, v174
	v_fmac_f32_e32 v166, v172, v172
	v_mul_f32_e32 v165, v165, v165
	v_add_f32_e32 v163, v163, v166
	v_fmac_f32_e32 v165, v164, v164
	v_mul_f32_e32 v164, v177, v177
	v_add_f32_e32 v163, v165, v163
	v_fmac_f32_e32 v164, v176, v176
	v_add_f32_e32 v163, v164, v163
	ds_bpermute_b32 v164, v157, v163
	v_or_b32_e32 v165, 32, v148
	v_mad_i64_i32 v[166:167], s[12:13], v165, s41, v[152:153]
	v_lshl_add_u64 v[170:171], v[166:167], 0, v[154:155]
	s_waitcnt lgkmcnt(0)
	v_add_f32_e32 v163, v163, v164
	v_pk_mul_f32 v[172:173], v[98:99], v[162:163] op_sel_hi:[1,0]
	v_pk_mul_f32 v[174:175], v[96:97], v[162:163] op_sel_hi:[1,0]
	v_pk_mul_f32 v[176:177], v[94:95], v[162:163] op_sel_hi:[1,0]
	v_pk_mul_f32 v[178:179], v[92:93], v[162:163] op_sel_hi:[1,0]
	v_cvt_pk_bf16_f32 v166, v174, v175
	v_cvt_pk_bf16_f32 v167, v172, v173
	v_cvt_pk_bf16_f32 v168, v178, v179
	v_cvt_pk_bf16_f32 v169, v176, v177
	global_store_dwordx4 v[170:171], v[166:169], off nt
	v_mul_f32_e32 v165, v175, v175
	v_fmac_f32_e32 v165, v174, v174
	v_mul_f32_e32 v166, v173, v173
	v_fmac_f32_e32 v166, v172, v172
	v_add_f32_e32 v165, v165, v166
	v_mul_f32_e32 v166, v179, v179
	v_fmac_f32_e32 v166, v178, v178
	v_add_f32_e32 v165, v166, v165
	v_mul_f32_e32 v166, v177, v177
	v_fmac_f32_e32 v166, v176, v176
	v_add_f32_e32 v165, v166, v165
	ds_bpermute_b32 v166, v157, v165
	v_pk_mul_f32 v[172:173], v[90:91], v[162:163] op_sel_hi:[1,0]
	v_pk_mul_f32 v[174:175], v[88:89], v[162:163] op_sel_hi:[1,0]
	v_pk_mul_f32 v[176:177], v[86:87], v[162:163] op_sel_hi:[1,0]
	v_pk_mul_f32 v[178:179], v[84:85], v[162:163] op_sel_hi:[1,0]
	s_waitcnt lgkmcnt(0)
	v_add_f32_e32 v165, v165, v166
	ds_bpermute_b32 v166, v159, v165
	v_mul_f32_e32 v162, v175, v175
	v_fmac_f32_e32 v162, v174, v174
	v_cvt_pk_bf16_f32 v167, v172, v173
	v_cvt_pk_bf16_f32 v168, v178, v179
	s_waitcnt lgkmcnt(0)
	v_add_f32_e32 v181, v165, v166
	v_mul_f32_e32 v165, v173, v173
	v_fmac_f32_e32 v165, v172, v172
	v_add_f32_e32 v162, v162, v165
	v_mul_f32_e32 v165, v179, v179
	v_cvt_pk_bf16_f32 v166, v174, v175
	v_cvt_pk_bf16_f32 v169, v176, v177
	v_fmac_f32_e32 v165, v178, v178
	global_store_dwordx4 v[170:171], v[166:169], off offset:256 nt
	v_add_f32_e32 v162, v165, v162
	v_mul_f32_e32 v165, v177, v177
	v_or_b32_e32 v166, 48, v148
	v_fmac_f32_e32 v165, v176, v176
	v_mad_i64_i32 v[166:167], s[12:13], v166, s41, v[152:153]
	v_pk_mul_f32 v[170:171], v[82:83], v[160:161] op_sel_hi:[1,0]
	v_pk_mul_f32 v[174:175], v[80:81], v[160:161] op_sel_hi:[1,0]
	v_pk_mul_f32 v[176:177], v[78:79], v[160:161] op_sel_hi:[1,0]
	v_pk_mul_f32 v[178:179], v[76:77], v[160:161] op_sel_hi:[1,0]
	v_lshl_add_u64 v[172:173], v[166:167], 0, v[154:155]
	v_cvt_pk_bf16_f32 v166, v174, v175
	v_cvt_pk_bf16_f32 v167, v170, v171
	v_cvt_pk_bf16_f32 v168, v178, v179
	v_cvt_pk_bf16_f32 v169, v176, v177
	global_store_dwordx4 v[172:173], v[166:169], off nt
	v_add_f32_e32 v147, v147, v149
	v_add_f32_e32 v162, v165, v162
	v_mul_f32_e32 v166, v175, v175
	v_mul_f32_e32 v167, v171, v171
	v_fmac_f32_e32 v166, v174, v174
	v_fmac_f32_e32 v167, v170, v170
	v_add_f32_e32 v166, v166, v167
	v_mul_f32_e32 v167, v179, v179
	v_fmac_f32_e32 v167, v178, v178
	v_add_f32_e32 v166, v167, v166
	v_mul_f32_e32 v167, v177, v177
	v_fmac_f32_e32 v167, v176, v176
	v_add_f32_e32 v166, v167, v166
	ds_bpermute_b32 v167, v157, v166
	v_pk_mul_f32 v[174:175], v[74:75], v[160:161] op_sel_hi:[1,0]
	v_pk_mul_f32 v[176:177], v[72:73], v[160:161] op_sel_hi:[1,0]
	v_pk_mul_f32 v[178:179], v[70:71], v[160:161] op_sel_hi:[1,0]
	v_cvt_pk_bf16_f32 v168, v176, v177
	s_waitcnt lgkmcnt(0)
; __device__ __forceinline__ unsigned cvt_pk_bf16(float lo, float hi) { f32x2_t v = {lo, hi}; bf16x2_t b = __builtin_convertvector(v, bf16x2_t); return __builtin_bit_cast(unsigned, b); }
;     template <int ACT, int AUX> __device__ __forceinline__ void run(const f32x4 (&acc)[2][2][4][2], const Unit& uu, int wr, int wc, int fr, int fq) const {
;     ...
;             for (int m = 0; m < 4; ++m) { const int r = row0 + ai * HALF + m * 16; const float rs = rsv[ai * 4 + m];
;                 bf16_t* rowp = O + (size_t)r * cfg::NC + col0; float s1 = 0.f, s2 = 0.f;
; #pragma unroll
;                 for (int bj = 0; bj < 2; ++bj) { f32x4 v0 = acc[ai][bj][m][0] * rs, v1 = acc[ai][bj][m][1] * rs;
; #pragma unroll
;                     for (int j = 0; j < 4; ++j) { v0[j] = act_f<ACT>(v0[j]); v1[j] = act_f<ACT>(v1[j]); }
;                     if (AUX == 4) {
;                         unsigned q[8];
; #pragma unroll
;                         for (int j = 0; j < 4; ++j) { q[j] = (unsigned)fminf(fmaxf(fmaf(v0[j], 255.0f, 0.5f), 1.0f), 255.0f); q[4 + j] = (unsigned)fminf(fmaxf(fmaf(v1[j], 255.0f, 0.5f), 1.0f), 255.0f); }
;                         u32x2 w8; w8.x = q[0] | (q[1] << 8) | (q[2] << 16) | (q[3] << 24); w8.y = q[4] | (q[5] << 8) | (q[6] << 16) | (q[7] << 24);
;                         __builtin_nontemporal_store(w8, (u32x2*)(g8 + ((size_t)((u.pn - 52) >> 4) * cfg::MT + r) * cfg::DM + ((u.pn - 52) & 15) * BM + wc * 32 + 8 * fq + bj * HALF));
;                     } else {
;                     u32x4 w; w.x = cvt_pk_bf16(v0[0], v0[1]); w.y = cvt_pk_bf16(v0[2], v0[3]); w.z = cvt_pk_bf16(v1[0], v1[1]); w.w = cvt_pk_bf16(v1[2], v1[3]);
;                     __builtin_nontemporal_store(w, (u32x4*)(rowp + bj * HALF)); }
;                     if (AUX == 1) {
; #pragma unroll
;                         for (int j = 0; j < 4; ++j) { cs[bj][j] += v0[j]; cs[bj][4 + j] += v1[j]; } }
;                     if (AUX == 2) { float p = (v0[0] * v0[0] + v0[1] * v0[1]) + (v0[2] * v0[2] + v0[3] * v0[3]) + (v1[0] * v1[0] + v1[1] * v1[1]) + (v1[2] * v1[2] + v1[3] * v1[3]);
;                         p += __shfl_xor(p, 16); p += __shfl_xor(p, 32); mx[ai][bj] = fmaxf(mx[ai][bj], p); }
	v_add_f32_e32 v166, v166, v167
	ds_bpermute_b32 v167, v159, v166
	v_cvt_pk_bf16_f32 v169, v174, v175
	v_cvt_pk_bf16_f32 v171, v178, v179
	ds_bpermute_b32 v165, v157, v162
	ds_bpermute_b32 v149, v159, v147
	s_waitcnt lgkmcnt(2)
	v_add_f32_e32 v166, v166, v167
	v_max3_f32 v167, v180, v181, v166
	v_pk_mul_f32 v[180:181], v[68:69], v[160:161] op_sel_hi:[1,0]
	v_mul_f32_e32 v160, v177, v177
	v_mul_f32_e32 v166, v175, v175
	v_fmac_f32_e32 v160, v176, v176
	v_fmac_f32_e32 v166, v174, v174
	v_add_f32_e32 v160, v160, v166
	v_mul_f32_e32 v166, v181, v181
	v_fmac_f32_e32 v166, v180, v180
	v_cvt_pk_bf16_f32 v170, v180, v181
	v_add_f32_e32 v160, v166, v160
	v_mul_f32_e32 v166, v179, v179
	global_store_dwordx4 v[172:173], v[168:171], off offset:256 nt
	v_fmac_f32_e32 v166, v178, v178
	v_pk_mul_f32 v[172:173], v[66:67], v[158:159] op_sel_hi:[1,0]
	v_mad_i64_i32 v[168:169], s[12:13], v161, s41, v[152:153]
	v_pk_mul_f32 v[176:177], v[64:65], v[158:159] op_sel_hi:[1,0]
	v_pk_mul_f32 v[178:179], v[62:63], v[158:159] op_sel_hi:[1,0]
	v_pk_mul_f32 v[180:181], v[60:61], v[158:159] op_sel_hi:[1,0]
	v_lshl_add_u64 v[174:175], v[168:169], 0, v[154:155]
	v_cvt_pk_bf16_f32 v168, v176, v177
	v_cvt_pk_bf16_f32 v169, v172, v173
	v_cvt_pk_bf16_f32 v170, v180, v181
	v_cvt_pk_bf16_f32 v171, v178, v179
	global_store_dwordx4 v[174:175], v[168:171], off nt
	v_mul_f32_e32 v161, v177, v177
	v_fmac_f32_e32 v161, v176, v176
	v_mul_f32_e32 v168, v173, v173
	v_fmac_f32_e32 v168, v172, v172
	v_add_f32_e32 v161, v161, v168
	v_mul_f32_e32 v168, v181, v181
	v_fmac_f32_e32 v168, v180, v180
	v_add_f32_e32 v161, v168, v161
	v_mul_f32_e32 v168, v179, v179
	v_fmac_f32_e32 v168, v178, v178
	v_pk_mul_f32 v[176:177], v[58:59], v[158:159] op_sel_hi:[1,0]
	v_pk_mul_f32 v[178:179], v[56:57], v[158:159] op_sel_hi:[1,0]
	v_pk_mul_f32 v[180:181], v[54:55], v[158:159] op_sel_hi:[1,0]
	v_mul_f32_e32 v158, v179, v179
	v_mul_f32_e32 v169, v177, v177
	v_fmac_f32_e32 v158, v178, v178
	v_fmac_f32_e32 v169, v176, v176
	v_add_f32_e32 v158, v158, v169
	v_mul_f32_e32 v169, v183, v183
	v_cvt_pk_bf16_f32 v170, v178, v179
	v_cvt_pk_bf16_f32 v171, v176, v177
	v_cvt_pk_bf16_f32 v172, v182, v183
	v_cvt_pk_bf16_f32 v173, v180, v181
	v_fmac_f32_e32 v169, v182, v182
	global_store_dwordx4 v[174:175], v[170:173], off offset:256 nt
	v_add_f32_e32 v158, v169, v158
	v_mul_f32_e32 v169, v181, v181
	v_add_u32_e32 v170, 0x90, v148
	v_fmac_f32_e32 v169, v180, v180
	v_mad_i64_i32 v[170:171], s[12:13], v170, s41, v[152:153]
	v_pk_mul_f32 v[174:175], v[50:51], v[156:157] op_sel_hi:[1,0]
	v_pk_mul_f32 v[178:179], v[48:49], v[156:157] op_sel_hi:[1,0]
	v_pk_mul_f32 v[180:181], v[46:47], v[156:157] op_sel_hi:[1,0]
	v_pk_mul_f32 v[182:183], v[44:45], v[156:157] op_sel_hi:[1,0]
	v_lshl_add_u64 v[176:177], v[170:171], 0, v[154:155]
	v_cvt_pk_bf16_f32 v170, v178, v179
	v_cvt_pk_bf16_f32 v171, v174, v175
	v_cvt_pk_bf16_f32 v172, v182, v183
	v_cvt_pk_bf16_f32 v173, v180, v181
	global_store_dwordx4 v[176:177], v[170:173], off nt
	v_add_f32_e32 v160, v166, v160
	v_add_f32_e32 v161, v168, v161
	v_mul_f32_e32 v170, v179, v179
	v_mul_f32_e32 v171, v175, v175
	v_fmac_f32_e32 v170, v178, v178
	v_fmac_f32_e32 v171, v174, v174
	v_add_f32_e32 v170, v170, v171
	v_mul_f32_e32 v171, v183, v183
	v_fmac_f32_e32 v171, v182, v182
	v_add_f32_e32 v170, v171, v170
	v_mul_f32_e32 v171, v181, v181
	v_fmac_f32_e32 v171, v180, v180
	v_pk_mul_f32 v[178:179], v[42:43], v[156:157] op_sel_hi:[1,0]
	v_pk_mul_f32 v[180:181], v[40:41], v[156:157] op_sel_hi:[1,0]
	v_pk_mul_f32 v[182:183], v[38:39], v[156:157] op_sel_hi:[1,0]
	v_cvt_pk_bf16_f32 v172, v180, v181
	v_cvt_pk_bf16_f32 v173, v178, v179
	v_cvt_pk_bf16_f32 v174, v184, v185
	v_cvt_pk_bf16_f32 v175, v182, v183
	global_store_dwordx4 v[176:177], v[172:175], off offset:256 nt
	v_mul_f32_e32 v156, v181, v181
	v_fmac_f32_e32 v156, v180, v180
	v_mul_f32_e32 v172, v179, v179
	v_fmac_f32_e32 v172, v178, v178
	v_add_f32_e32 v156, v156, v172
	v_mul_f32_e32 v172, v185, v185
	v_fmac_f32_e32 v172, v184, v184
	v_add_f32_e32 v156, v172, v156
	v_mul_f32_e32 v172, v183, v183
	v_add_u32_e32 v173, 0xa0, v148
	v_fmac_f32_e32 v172, v182, v182
	v_mad_i64_i32 v[174:175], s[12:13], v173, s41, v[152:153]
	v_pk_mul_f32 v[178:179], v[34:35], v[150:151] op_sel_hi:[1,0]
	v_pk_mul_f32 v[182:183], v[32:33], v[150:151] op_sel_hi:[1,0]
	v_pk_mul_f32 v[184:185], v[30:31], v[150:151] op_sel_hi:[1,0]
	v_lshl_add_u64 v[180:181], v[174:175], 0, v[154:155]
	v_cvt_pk_bf16_f32 v174, v182, v183
	v_cvt_pk_bf16_f32 v175, v178, v179
	v_cvt_pk_bf16_f32 v176, v186, v187
	v_cvt_pk_bf16_f32 v177, v184, v185
	global_store_dwordx4 v[180:181], v[174:177], off nt
	v_mul_f32_e32 v173, v183, v183
	v_fmac_f32_e32 v173, v182, v182
	v_mul_f32_e32 v174, v179, v179
	v_fmac_f32_e32 v174, v178, v178
	v_add_f32_e32 v173, v173, v174
	v_mul_f32_e32 v174, v187, v187
	v_fmac_f32_e32 v174, v186, v186
	v_add_f32_e32 v173, v174, v173
	v_mul_f32_e32 v174, v185, v185
	v_fmac_f32_e32 v174, v184, v184
	v_pk_mul_f32 v[182:183], v[26:27], v[150:151] op_sel_hi:[1,0]
	v_pk_mul_f32 v[184:185], v[24:25], v[150:151] op_sel_hi:[1,0]
	v_pk_mul_f32 v[186:187], v[22:23], v[150:151] op_sel_hi:[1,0]
	v_cvt_pk_bf16_f32 v176, v184, v185
;     template <int ACT, int AUX> __device__ __forceinline__ void run(const f32x4 (&acc)[2][2][4][2], const Unit& uu, int wr, int wc, int fr, int fq) const {
;     ...
;                     if (AUX == 2) { float p = (v0[0] * v0[0] + v0[1] * v0[1]) + (v0[2] * v0[2] + v0[3] * v0[3]) + (v1[0] * v1[0] + v1[1] * v1[1]) + (v1[2] * v1[2] + v1[3] * v1[3]);
;                         p += __shfl_xor(p, 16); p += __shfl_xor(p, 32); mx[ai][bj] = fmaxf(mx[ai][bj], p); }
;                     if (AUX == 3) { s1 += (v0[0] + v0[1]) + (v0[2] + v0[3]) + (v1[0] + v1[1]) + (v1[2] + v1[3]);
;                         s2 += (v0[0] * v0[0] + v0[1] * v0[1]) + (v0[2] * v0[2] + v0[3] * v0[3]) + (v1[0] * v1[0] + v1[1] * v1[1]) + (v1[2] * v1[2] + v1[3] * v1[3]); } }
;                 if (AUX == 3) { s1 += __shfl_xor(s1, 16); s1 += __shfl_xor(s1, 32); s2 += __shfl_xor(s2, 16); s2 += __shfl_xor(s2, 32);
;                     if (fq == 0) *(float2*)(st2 + ((size_t)r * 16 + (u.pn - 36) * 4 + wc) * 2) = make_float2(s1, s2); } }
;         if (AUX == 1) {
; #pragma unroll
;             for (int i = 0; i < 16; ++i) { float x = cs[i >> 3][i & 7]; x += __shfl_xor(x, 1); x += __shfl_xor(x, 2); x += __shfl_xor(x, 4); x += __shfl_xor(x, 8); cs[i >> 3][i & 7] = x; }
;             if (fr == 0) {
; #pragma unroll
;                 for (int bj = 0; bj < 2; ++bj) { float* o = kms + ((size_t)(((u.pm >> 3) * 8 + (u.pn - 4) * 2 + bj) * 8 + (u.pm & 7)) * 2 + wr) * 128 + wc * 32 + 8 * fq;
;                     *(f32x4*)o = (f32x4){cs[bj][0], cs[bj][1], cs[bj][2], cs[bj][3]}; *(f32x4*)(o + 4) = (f32x4){cs[bj][4], cs[bj][5], cs[bj][6], cs[bj][7]}; } }
;         }
;         if (AUX == 2) {
; #pragma unroll
;             for (int i = 0; i < 4; ++i) { float x = mx[i >> 1][i & 1]; x = fmaxf(x, __shfl_xor(x, 1)); x = fmaxf(x, __shfl_xor(x, 2)); x = fmaxf(x, __shfl_xor(x, 4)); x = fmaxf(x, __shfl_xor(x, 8));
;                 if (fr == 0 && fq == 0) kn2[((size_t)((((u.pm >> 3) * 4 + (u.pn - 20)) * 2 + (i & 1)) * 32 + (u.pm & 7) * 4 + (i >> 1) * 2 + wr)) * 4 + wc] = x; }
	v_cvt_pk_bf16_f32 v177, v182, v183
	v_cvt_pk_bf16_f32 v178, v188, v189
	v_cvt_pk_bf16_f32 v179, v186, v187
	v_mul_f32_e32 v150, v185, v185
	v_mul_f32_e32 v175, v183, v183
	v_add_u32_e32 v148, 0xb0, v148
	global_store_dwordx4 v[180:181], v[176:179], off offset:256 nt
	v_fmac_f32_e32 v150, v184, v184
	v_fmac_f32_e32 v175, v182, v182
	v_mad_i64_i32 v[152:153], s[12:13], v148, s41, v[152:153]
	v_pk_mul_f32 v[176:177], v[18:19], v[146:147] op_sel_hi:[1,0]
	v_pk_mul_f32 v[178:179], v[16:17], v[146:147] op_sel_hi:[1,0]
	v_pk_mul_f32 v[182:183], v[14:15], v[146:147] op_sel_hi:[1,0]
	v_pk_mul_f32 v[184:185], v[12:13], v[146:147] op_sel_hi:[1,0]
	v_lshl_add_u64 v[180:181], v[152:153], 0, v[154:155]
	v_cvt_pk_bf16_f32 v152, v178, v179
	v_cvt_pk_bf16_f32 v153, v176, v177
	v_cvt_pk_bf16_f32 v154, v184, v185
	v_cvt_pk_bf16_f32 v155, v182, v183
	global_store_dwordx4 v[180:181], v[152:155], off nt
	v_mul_f32_e32 v148, v179, v179
	v_fmac_f32_e32 v148, v178, v178
	v_mul_f32_e32 v152, v177, v177
	v_fmac_f32_e32 v152, v176, v176
	v_add_f32_e32 v148, v148, v152
	v_mul_f32_e32 v152, v185, v185
	v_add_f32_e32 v150, v150, v175
	v_mul_f32_e32 v175, v189, v189
	v_fmac_f32_e32 v152, v184, v184
	v_fmac_f32_e32 v175, v188, v188
	v_add_f32_e32 v148, v152, v148
	v_mul_f32_e32 v152, v183, v183
	v_add_f32_e32 v150, v175, v150
	v_mul_f32_e32 v175, v187, v187
	v_fmac_f32_e32 v152, v182, v182
	v_pk_mul_f32 v[154:155], v[10:11], v[146:147] op_sel_hi:[1,0]
	v_pk_mul_f32 v[182:183], v[8:9], v[146:147] op_sel_hi:[1,0]
	v_fmac_f32_e32 v175, v186, v186
	v_pk_mul_f32 v[184:185], v[6:7], v[146:147] op_sel_hi:[1,0]
	v_pk_mul_f32 v[186:187], v[4:5], v[146:147] op_sel_hi:[1,0]
	v_mul_f32_e32 v146, v183, v183
	v_mul_f32_e32 v153, v155, v155
	v_fmac_f32_e32 v146, v182, v182
	v_fmac_f32_e32 v153, v154, v154
	v_add_f32_e32 v146, v146, v153
	v_mul_f32_e32 v153, v187, v187
	v_fmac_f32_e32 v153, v186, v186
	v_add_f32_e32 v146, v153, v146
	v_mul_f32_e32 v153, v185, v185
	v_fmac_f32_e32 v153, v184, v184
	v_add_f32_e32 v158, v169, v158
	v_add_f32_e32 v170, v171, v170
	v_add_f32_e32 v156, v172, v156
	v_add_f32_e32 v173, v174, v173
	v_add_f32_e32 v150, v175, v150
	v_add_f32_e32 v148, v152, v148
	v_add_f32_e32 v146, v153, v146
	ds_bpermute_b32 v166, v157, v160
	ds_bpermute_b32 v168, v157, v161
	ds_bpermute_b32 v169, v157, v158
	ds_bpermute_b32 v171, v157, v170
	ds_bpermute_b32 v172, v157, v156
	ds_bpermute_b32 v174, v157, v173
	ds_bpermute_b32 v175, v157, v150
	ds_bpermute_b32 v152, v157, v148
	ds_bpermute_b32 v153, v157, v146
	v_cvt_pk_bf16_f32 v177, v154, v155
	v_xor_b32_e32 v154, 1, v229
	v_cmp_lt_i32_e32 vcc, v154, v151
	v_xor_b32_e32 v155, 2, v229
	s_waitcnt lgkmcnt(10)
	v_add_f32_e32 v162, v162, v165
	s_waitcnt lgkmcnt(8)
	v_add_f32_e32 v160, v160, v166
	s_waitcnt lgkmcnt(7)
	v_add_f32_e32 v161, v161, v168
	s_waitcnt lgkmcnt(6)
	v_add_f32_e32 v158, v158, v169
	s_waitcnt lgkmcnt(5)
	v_add_f32_e32 v170, v170, v171
	s_waitcnt lgkmcnt(4)
	v_add_f32_e32 v156, v156, v172
	s_waitcnt lgkmcnt(3)
	v_add_f32_e32 v173, v173, v174
	s_waitcnt lgkmcnt(2)
	v_add_f32_e32 v150, v150, v175
	s_waitcnt lgkmcnt(1)
	v_add_f32_e32 v148, v148, v152
	s_waitcnt lgkmcnt(0)
	v_add_f32_e32 v146, v146, v153
	v_cndmask_b32_e32 v154, v229, v154, vcc
	v_cmp_lt_i32_e32 vcc, v155, v151
	v_xor_b32_e32 v157, 4, v229
	ds_bpermute_b32 v164, v159, v163
	ds_bpermute_b32 v165, v159, v162
	ds_bpermute_b32 v166, v159, v160
	ds_bpermute_b32 v168, v159, v161
	ds_bpermute_b32 v169, v159, v158
	ds_bpermute_b32 v171, v159, v170
	ds_bpermute_b32 v172, v159, v156
	ds_bpermute_b32 v174, v159, v173
	ds_bpermute_b32 v175, v159, v150
	ds_bpermute_b32 v152, v159, v148
	ds_bpermute_b32 v153, v159, v146
	v_cndmask_b32_e32 v155, v229, v155, vcc
	v_cmp_lt_i32_e32 vcc, v157, v151
	v_xor_b32_e32 v159, 8, v229
	v_lshlrev_b32_e32 v154, 2, v154
	v_cndmask_b32_e32 v157, v229, v157, vcc
	v_cmp_lt_i32_e32 vcc, v159, v151
	v_lshlrev_b32_e32 v155, 2, v155
	v_lshlrev_b32_e32 v157, 2, v157
	v_cndmask_b32_e32 v151, v229, v159, vcc
	ds_bpermute_b32 v159, v154, v167
	v_lshlrev_b32_e32 v151, 2, v151
	s_lshl_b32 s12, s1, 1
	s_and_b32 s13, s2, -8
	s_add_i32 s13, s13, s12
	s_waitcnt lgkmcnt(0)
	v_max_f32_e32 v159, v159, v159
	v_max_f32_e32 v159, v167, v159
	ds_bpermute_b32 v167, v155, v159
	s_lshl_b32 s12, s2, 2
	s_and_b32 s48, s12, 28
	v_cvt_pk_bf16_f32 v176, v182, v183
	v_cvt_pk_bf16_f32 v178, v186, v187
	s_waitcnt lgkmcnt(0)
	v_max_f32_e32 v167, v167, v167
	v_max_f32_e32 v159, v159, v167
	ds_bpermute_b32 v167, v157, v159
	v_cvt_pk_bf16_f32 v179, v184, v185
	s_sub_i32 s41, s13, 40
	s_add_i32 s48, s48, s0
	global_store_dwordx4 v[180:181], v[176:179], off offset:256 nt
	s_waitcnt lgkmcnt(0)
	v_max_f32_e32 v167, v167, v167
	v_max_f32_e32 v159, v159, v167
	ds_bpermute_b32 v167, v151, v159
	s_and_saveexec_b64 s[12:13], s[4:5]
	s_cbranch_execz .LBB0_197
	s_lshl_b32 s49, s41, 5
	s_add_i32 s50, s49, s48
	s_ashr_i32 s51, s50, 31
	s_lshl_b64 s[50:51], s[50:51], 4
	v_readlane_b32 s49, v253, 50
	s_waitcnt lgkmcnt(0)
	v_max_f32_e32 v167, v167, v167
	v_max_f32_e32 v159, v159, v159
	s_add_u32 s50, s49, s50
	v_max_f32_e32 v159, v159, v167
	s_addc_u32 s51, s27, s51
	global_store_dword v3, v159, s[50:51]

; __device__ __forceinline__ unsigned cvt_pk_bf16(float lo, float hi) { f32x2_t v = {lo, hi}; bf16x2_t b = __builtin_convertvector(v, bf16x2_t); return __builtin_bit_cast(unsigned, b); }
;     template <int ACT, int AUX> __device__ __forceinline__ void run(const f32x4 (&acc)[2][2][4][2], const Unit& uu, int wr, int wc, int fr, int fq) const {
;     ...
;         float rsv[8];
; #pragma unroll
;         for (int i = 0; i < 8; ++i) rsv[i] = ss[row0 + (i >> 2) * HALF + (i & 3) * 16];
;         asm volatile("" ::: "memory");
; #pragma unroll
;         for (int i = 0; i < 8; ++i) rsv[i] = __builtin_amdgcn_rsqf(rsv[i] * (1.0f / cfg::DM) + cfg::RMS_EPS);
;         float cs[2][8]; float mx[2][2];
;         if (AUX == 1) {
; #pragma unroll
;             for (int i = 0; i < 16; ++i) cs[i >> 3][i & 7] = 0.f; }
;         if (AUX == 2) { mx[0][0] = mx[0][1] = mx[1][0] = mx[1][1] = 0.f; }
; #pragma unroll
;         for (int ai = 0; ai < 2; ++ai)
; #pragma unroll
;             for (int m = 0; m < 4; ++m) { const int r = row0 + ai * HALF + m * 16; const float rs = rsv[ai * 4 + m];
;                 bf16_t* rowp = O + (size_t)r * cfg::NC + col0; float s1 = 0.f, s2 = 0.f;
; #pragma unroll
;                 for (int bj = 0; bj < 2; ++bj) { f32x4 v0 = acc[ai][bj][m][0] * rs, v1 = acc[ai][bj][m][1] * rs;
; #pragma unroll
;                     for (int j = 0; j < 4; ++j) { v0[j] = act_f<ACT>(v0[j]); v1[j] = act_f<ACT>(v1[j]); }
;                     if (AUX == 4) {
;                         unsigned q[8];
; #pragma unroll
;                         for (int j = 0; j < 4; ++j) { q[j] = (unsigned)fminf(fmaxf(fmaf(v0[j], 255.0f, 0.5f), 1.0f), 255.0f); q[4 + j] = (unsigned)fminf(fmaxf(fmaf(v1[j], 255.0f, 0.5f), 1.0f), 255.0f); }
;                         u32x2 w8; w8.x = q[0] | (q[1] << 8) | (q[2] << 16) | (q[3] << 24); w8.y = q[4] | (q[5] << 8) | (q[6] << 16) | (q[7] << 24);
;                         __builtin_nontemporal_store(w8, (u32x2*)(g8 + ((size_t)((u.pn - 52) >> 4) * cfg::MT + r) * cfg::DM + ((u.pn - 52) & 15) * BM + wc * 32 + 8 * fq + bj * HALF));
;                     } else {
;                     u32x4 w; w.x = cvt_pk_bf16(v0[0], v0[1]); w.y = cvt_pk_bf16(v0[2], v0[3]); w.z = cvt_pk_bf16(v1[0], v1[1]); w.w = cvt_pk_bf16(v1[2], v1[3]);
;                     __builtin_nontemporal_store(w, (u32x4*)(rowp + bj * HALF)); }
.LBB0_207:
	s_and_b64 vcc, exec, s[48:49]
	s_cbranch_vccz .LBB0_209
	v_lshl_add_u32 v146, s2, 8, v1
	s_waitcnt lgkmcnt(0)
	v_ashrrev_i32_e32 v147, 31, v146
	v_lshl_add_u64 v[148:149], v[146:147], 2, s[22:23]
	v_mov_b32_e32 v150, v218
	v_mov_b32_e32 v151, v220
	v_mov_b32_e32 v152, v224
	v_mov_b32_e32 v153, v226
	v_mov_b32_e32 v154, v228
	v_mov_b32_e32 v155, v230
	v_mov_b32_e32 v157, v240
	s_nop 0
	v_mov_b32_e32 v148, v250
	v_lshl_or_b32 v158, s1, 8, v191
	v_ashrrev_i32_e32 v159, 31, v158
	s_mov_b32 s39, 0xe800
	v_lshlrev_b64 v[158:159], 1, v[158:159]
	v_add_u32_e32 v147, 0x80, v146
	s_mov_b64 s[50:51], 0
	v_fmamk_f32 v149, v150, 0x39800000, v221
	v_rsq_f32_e32 v168, v149
	v_fmamk_f32 v149, v151, 0x39800000, v221
	v_rsq_f32_e32 v170, v149
	v_fmamk_f32 v149, v152, 0x39800000, v221
	v_rsq_f32_e32 v162, v149
	v_fmamk_f32 v149, v153, 0x39800000, v221
	v_rsq_f32_e32 v160, v149
	v_fmamk_f32 v149, v154, 0x39800000, v221
	v_rsq_f32_e32 v156, v149
	v_fmamk_f32 v149, v155, 0x39800000, v221
	v_mov_b64_e32 v[154:155], s[20:21]
	v_mad_i64_i32 v[164:165], s[12:13], v146, s39, v[154:155]
	v_lshl_add_u64 v[172:173], v[164:165], 0, v[158:159]
	v_pk_mul_f32 v[166:167], v[130:131], v[168:169] op_sel_hi:[1,0]
	v_pk_mul_f32 v[164:165], v[128:129], v[168:169] op_sel_hi:[1,0]
	v_pk_mul_f32 v[174:175], v[126:127], v[168:169] op_sel_hi:[1,0]
	v_pk_mul_f32 v[176:177], v[124:125], v[168:169] op_sel_hi:[1,0]
	v_cvt_pk_bf16_f32 v164, v164, v165
	v_cvt_pk_bf16_f32 v165, v166, v167
	v_cvt_pk_bf16_f32 v166, v176, v177
	v_cvt_pk_bf16_f32 v167, v174, v175
	v_rsq_f32_e32 v152, v149
	v_fmamk_f32 v149, v157, 0x39800000, v221
	global_store_dwordx4 v[172:173], v[164:167], off nt
	v_pk_mul_f32 v[174:175], v[118:119], v[168:169] op_sel_hi:[1,0]
	v_rsq_f32_e32 v150, v149
	v_pk_mul_f32 v[166:167], v[122:123], v[168:169] op_sel_hi:[1,0]
	v_pk_mul_f32 v[164:165], v[120:121], v[168:169] op_sel_hi:[1,0]
	v_pk_mul_f32 v[168:169], v[116:117], v[168:169] op_sel_hi:[1,0]
	v_cvt_pk_bf16_f32 v164, v164, v165
	v_cvt_pk_bf16_f32 v165, v166, v167
	v_cvt_pk_bf16_f32 v166, v168, v169
	v_cvt_pk_bf16_f32 v167, v174, v175
	v_or_b32_e32 v149, 16, v146
	global_store_dwordx4 v[172:173], v[164:167], off offset:256 nt
	v_pk_mul_f32 v[172:173], v[110:111], v[170:171] op_sel_hi:[1,0]
	v_pk_mul_f32 v[174:175], v[108:109], v[170:171] op_sel_hi:[1,0]
	v_mad_i64_i32 v[164:165], s[12:13], v149, s39, v[154:155]
	v_lshl_add_u64 v[168:169], v[164:165], 0, v[158:159]
	v_pk_mul_f32 v[166:167], v[114:115], v[170:171] op_sel_hi:[1,0]
	v_pk_mul_f32 v[164:165], v[112:113], v[170:171] op_sel_hi:[1,0]
	v_or_b32_e32 v149, 32, v146
	v_cvt_pk_bf16_f32 v164, v164, v165
	v_cvt_pk_bf16_f32 v165, v166, v167
	v_cvt_pk_bf16_f32 v166, v174, v175
	v_cvt_pk_bf16_f32 v167, v172, v173
	global_store_dwordx4 v[168:169], v[164:167], off nt
	v_pk_mul_f32 v[172:173], v[102:103], v[170:171] op_sel_hi:[1,0]
	v_fmamk_f32 v148, v148, 0x39800000, v221
	v_pk_mul_f32 v[166:167], v[106:107], v[170:171] op_sel_hi:[1,0]
	v_pk_mul_f32 v[164:165], v[104:105], v[170:171] op_sel_hi:[1,0]
	v_pk_mul_f32 v[170:171], v[100:101], v[170:171] op_sel_hi:[1,0]
	v_cvt_pk_bf16_f32 v164, v164, v165
	v_cvt_pk_bf16_f32 v165, v166, v167
	v_cvt_pk_bf16_f32 v166, v170, v171
	v_cvt_pk_bf16_f32 v167, v172, v173
	global_store_dwordx4 v[168:169], v[164:167], off offset:256 nt
	v_pk_mul_f32 v[168:169], v[98:99], v[162:163] op_sel_hi:[1,0]
	v_pk_mul_f32 v[170:171], v[94:95], v[162:163] op_sel_hi:[1,0]
	v_mad_i64_i32 v[164:165], s[12:13], v149, s39, v[154:155]
	v_pk_mul_f32 v[166:167], v[96:97], v[162:163] op_sel_hi:[1,0]
	v_pk_mul_f32 v[172:173], v[92:93], v[162:163] op_sel_hi:[1,0]
	v_lshl_add_u64 v[164:165], v[164:165], 0, v[158:159]
	v_cvt_pk_bf16_f32 v166, v166, v167
	v_cvt_pk_bf16_f32 v167, v168, v169
	v_cvt_pk_bf16_f32 v168, v172, v173
	v_cvt_pk_bf16_f32 v169, v170, v171
	global_store_dwordx4 v[164:165], v[166:169], off nt
	v_pk_mul_f32 v[170:171], v[86:87], v[162:163] op_sel_hi:[1,0]
	v_or_b32_e32 v149, 48, v146
	v_pk_mul_f32 v[168:169], v[90:91], v[162:163] op_sel_hi:[1,0]
	v_pk_mul_f32 v[166:167], v[88:89], v[162:163] op_sel_hi:[1,0]
	v_pk_mul_f32 v[162:163], v[84:85], v[162:163] op_sel_hi:[1,0]
	v_cvt_pk_bf16_f32 v166, v166, v167
	v_cvt_pk_bf16_f32 v167, v168, v169
	v_cvt_pk_bf16_f32 v168, v162, v163
	v_cvt_pk_bf16_f32 v169, v170, v171
	v_mad_i64_i32 v[162:163], s[12:13], v149, s39, v[154:155]
	global_store_dwordx4 v[164:165], v[166:169], off offset:256 nt
	v_pk_mul_f32 v[164:165], v[82:83], v[160:161] op_sel_hi:[1,0]
	v_pk_mul_f32 v[170:171], v[76:77], v[160:161] op_sel_hi:[1,0]
	v_lshl_add_u64 v[166:167], v[162:163], 0, v[158:159]
	v_pk_mul_f32 v[162:163], v[80:81], v[160:161] op_sel_hi:[1,0]
	v_pk_mul_f32 v[168:169], v[78:79], v[160:161] op_sel_hi:[1,0]
	v_cvt_pk_bf16_f32 v162, v162, v163
	v_cvt_pk_bf16_f32 v163, v164, v165
	v_cvt_pk_bf16_f32 v164, v170, v171
	v_cvt_pk_bf16_f32 v165, v168, v169
	global_store_dwordx4 v[166:167], v[162:165], off nt
	v_pk_mul_f32 v[168:169], v[70:71], v[160:161] op_sel_hi:[1,0]
	v_pk_mul_f32 v[170:171], v[68:69], v[160:161] op_sel_hi:[1,0]
	v_pk_mul_f32 v[162:163], v[74:75], v[160:161] op_sel_hi:[1,0]
	v_pk_mul_f32 v[164:165], v[72:73], v[160:161] op_sel_hi:[1,0]
	v_cvt_pk_bf16_f32 v161, v162, v163
	v_cvt_pk_bf16_f32 v160, v164, v165
	v_cvt_pk_bf16_f32 v162, v170, v171
	v_cvt_pk_bf16_f32 v163, v168, v169
	global_store_dwordx4 v[166:167], v[160:163], off offset:256 nt
	v_pk_mul_f32 v[166:167], v[62:63], v[156:157] op_sel_hi:[1,0]
	v_pk_mul_f32 v[168:169], v[60:61], v[156:157] op_sel_hi:[1,0]
	v_mad_i64_i32 v[160:161], s[12:13], v147, s39, v[154:155]
	v_lshl_add_u64 v[164:165], v[160:161], 0, v[158:159]
;     template <int ACT, int AUX> __device__ __forceinline__ void run(const f32x4 (&acc)[2][2][4][2], const Unit& uu, int wr, int wc, int fr, int fq) const {
;     ...
;         float rsv[8];
; #pragma unroll
;         for (int i = 0; i < 8; ++i) rsv[i] = ss[row0 + (i >> 2) * HALF + (i & 3) * 16];
;         asm volatile("" ::: "memory");
; #pragma unroll
;         for (int i = 0; i < 8; ++i) rsv[i] = __builtin_amdgcn_rsqf(rsv[i] * (1.0f / cfg::DM) + cfg::RMS_EPS);
;         float cs[2][8]; float mx[2][2];
;         if (AUX == 1) {
; #pragma unroll
;             for (int i = 0; i < 16; ++i) cs[i >> 3][i & 7] = 0.f; }
;         if (AUX == 2) { mx[0][0] = mx[0][1] = mx[1][0] = mx[1][1] = 0.f; }
; #pragma unroll
;         for (int ai = 0; ai < 2; ++ai)
; #pragma unroll
;             for (int m = 0; m < 4; ++m) { const int r = row0 + ai * HALF + m * 16; const float rs = rsv[ai * 4 + m];
;                 bf16_t* rowp = O + (size_t)r * cfg::NC + col0; float s1 = 0.f, s2 = 0.f;
; #pragma unroll
;                 for (int bj = 0; bj < 2; ++bj) { f32x4 v0 = acc[ai][bj][m][0] * rs, v1 = acc[ai][bj][m][1] * rs;
; #pragma unroll
;                     for (int j = 0; j < 4; ++j) { v0[j] = act_f<ACT>(v0[j]); v1[j] = act_f<ACT>(v1[j]); }
;                     if (AUX == 4) {
;                         unsigned q[8];
; #pragma unroll
;                         for (int j = 0; j < 4; ++j) { q[j] = (unsigned)fminf(fmaxf(fmaf(v0[j], 255.0f, 0.5f), 1.0f), 255.0f); q[4 + j] = (unsigned)fminf(fmaxf(fmaf(v1[j], 255.0f, 0.5f), 1.0f), 255.0f); }
;                         u32x2 w8; w8.x = q[0] | (q[1] << 8) | (q[2] << 16) | (q[3] << 24); w8.y = q[4] | (q[5] << 8) | (q[6] << 16) | (q[7] << 24);
;                         __builtin_nontemporal_store(w8, (u32x2*)(g8 + ((size_t)((u.pn - 52) >> 4) * cfg::MT + r) * cfg::DM + ((u.pn - 52) & 15) * BM + wc * 32 + 8 * fq + bj * HALF));
;                     } else {
;                     u32x4 w; w.x = cvt_pk_bf16(v0[0], v0[1]); w.y = cvt_pk_bf16(v0[2], v0[3]); w.z = cvt_pk_bf16(v1[0], v1[1]); w.w = cvt_pk_bf16(v1[2], v1[3]);
;                     __builtin_nontemporal_store(w, (u32x4*)(rowp + bj * HALF)); }
;                     if (AUX == 1) {
; #pragma unroll
;                         for (int j = 0; j < 4; ++j) { cs[bj][j] += v0[j]; cs[bj][4 + j] += v1[j]; } }
	v_pk_mul_f32 v[162:163], v[66:67], v[156:157] op_sel_hi:[1,0]
	v_pk_mul_f32 v[160:161], v[64:65], v[156:157] op_sel_hi:[1,0]
	v_add_u32_e32 v147, 0x90, v146
	v_cvt_pk_bf16_f32 v160, v160, v161
	v_cvt_pk_bf16_f32 v161, v162, v163
	v_cvt_pk_bf16_f32 v162, v168, v169
	v_cvt_pk_bf16_f32 v163, v166, v167
	global_store_dwordx4 v[164:165], v[160:163], off nt
	v_pk_mul_f32 v[166:167], v[54:55], v[156:157] op_sel_hi:[1,0]
	v_rsq_f32_e32 v148, v148
	v_pk_mul_f32 v[162:163], v[58:59], v[156:157] op_sel_hi:[1,0]
	v_pk_mul_f32 v[160:161], v[56:57], v[156:157] op_sel_hi:[1,0]
	v_pk_mul_f32 v[156:157], v[52:53], v[156:157] op_sel_hi:[1,0]
	v_cvt_pk_bf16_f32 v160, v160, v161
	v_cvt_pk_bf16_f32 v161, v162, v163
	v_cvt_pk_bf16_f32 v162, v156, v157
	v_cvt_pk_bf16_f32 v163, v166, v167
	global_store_dwordx4 v[164:165], v[160:163], off offset:256 nt
	v_mad_i64_i32 v[156:157], s[12:13], v147, s39, v[154:155]
	s_nop 0
	v_pk_mul_f32 v[162:163], v[50:51], v[152:153] op_sel_hi:[1,0]
	v_pk_mul_f32 v[160:161], v[48:49], v[152:153] op_sel_hi:[1,0]
	v_pk_mul_f32 v[164:165], v[46:47], v[152:153] op_sel_hi:[1,0]
	v_pk_mul_f32 v[166:167], v[44:45], v[152:153] op_sel_hi:[1,0]
	v_lshl_add_u64 v[156:157], v[156:157], 0, v[158:159]
	v_cvt_pk_bf16_f32 v160, v160, v161
	v_cvt_pk_bf16_f32 v161, v162, v163
	v_cvt_pk_bf16_f32 v162, v166, v167
	v_cvt_pk_bf16_f32 v163, v164, v165
	global_store_dwordx4 v[156:157], v[160:163], off nt
	v_pk_mul_f32 v[164:165], v[38:39], v[152:153] op_sel_hi:[1,0]
	v_add_u32_e32 v147, 0xa0, v146
	v_pk_mul_f32 v[162:163], v[42:43], v[152:153] op_sel_hi:[1,0]
	v_pk_mul_f32 v[160:161], v[40:41], v[152:153] op_sel_hi:[1,0]
	v_pk_mul_f32 v[152:153], v[36:37], v[152:153] op_sel_hi:[1,0]
	v_cvt_pk_bf16_f32 v160, v160, v161
	v_cvt_pk_bf16_f32 v161, v162, v163
	v_cvt_pk_bf16_f32 v162, v152, v153
	v_cvt_pk_bf16_f32 v163, v164, v165
	v_mad_i64_i32 v[152:153], s[12:13], v147, s39, v[154:155]
	global_store_dwordx4 v[156:157], v[160:163], off offset:256 nt
	v_lshl_add_u64 v[156:157], v[152:153], 0, v[158:159]
	v_pk_mul_f32 v[152:153], v[34:35], v[150:151] op_sel_hi:[1,0]
	v_pk_mul_f32 v[160:161], v[32:33], v[150:151] op_sel_hi:[1,0]
	v_pk_mul_f32 v[164:165], v[30:31], v[150:151] op_sel_hi:[1,0]
	v_pk_mul_f32 v[162:163], v[28:29], v[150:151] op_sel_hi:[1,0]
	v_cvt_pk_bf16_f32 v160, v160, v161
	v_cvt_pk_bf16_f32 v161, v152, v153
	v_cvt_pk_bf16_f32 v162, v162, v163
	v_cvt_pk_bf16_f32 v163, v164, v165
	global_store_dwordx4 v[156:157], v[160:163], off nt
	v_pk_mul_f32 v[152:153], v[26:27], v[150:151] op_sel_hi:[1,0]
	v_pk_mul_f32 v[164:165], v[20:21], v[150:151] op_sel_hi:[1,0]
	v_pk_mul_f32 v[160:161], v[24:25], v[150:151] op_sel_hi:[1,0]
	v_pk_mul_f32 v[162:163], v[22:23], v[150:151] op_sel_hi:[1,0]
	v_add_u32_e32 v146, 0xb0, v146
	v_cvt_pk_bf16_f32 v150, v160, v161
	v_cvt_pk_bf16_f32 v151, v152, v153
	v_cvt_pk_bf16_f32 v152, v164, v165
	v_cvt_pk_bf16_f32 v153, v162, v163
	v_mad_i64_i32 v[146:147], s[12:13], v146, s39, v[154:155]
	global_store_dwordx4 v[156:157], v[150:153], off offset:256 nt
	v_lshl_add_u64 v[154:155], v[146:147], 0, v[158:159]
	v_pk_mul_f32 v[146:147], v[18:19], v[148:149] op_sel_hi:[1,0]
	v_pk_mul_f32 v[150:151], v[16:17], v[148:149] op_sel_hi:[1,0]
	v_pk_mul_f32 v[156:157], v[14:15], v[148:149] op_sel_hi:[1,0]
	v_pk_mul_f32 v[152:153], v[12:13], v[148:149] op_sel_hi:[1,0]
	v_cvt_pk_bf16_f32 v150, v150, v151
	v_cvt_pk_bf16_f32 v151, v146, v147
	v_cvt_pk_bf16_f32 v152, v152, v153
	v_cvt_pk_bf16_f32 v153, v156, v157
	global_store_dwordx4 v[154:155], v[150:153], off nt
	v_pk_mul_f32 v[146:147], v[8:9], v[148:149] op_sel_hi:[1,0]
	s_nop 0
	v_pk_mul_f32 v[150:151], v[10:11], v[148:149] op_sel_hi:[1,0]
	v_pk_mul_f32 v[152:153], v[6:7], v[148:149] op_sel_hi:[1,0]
	v_pk_mul_f32 v[148:149], v[4:5], v[148:149] op_sel_hi:[1,0]
	v_cvt_pk_bf16_f32 v146, v146, v147
	v_cvt_pk_bf16_f32 v147, v150, v151
	v_cvt_pk_bf16_f32 v148, v148, v149
	v_cvt_pk_bf16_f32 v149, v152, v153
	global_store_dwordx4 v[154:155], v[146:149], off offset:256 nt
.LBB0_209:
	s_andn2_b64 vcc, exec, s[50:51]
	s_cbranch_vccnz .LBB0_213
	v_lshl_add_u32 v174, s2, 8, v1
	v_ashrrev_i32_e32 v175, 31, v174
	v_lshl_add_u64 v[148:149], v[174:175], 2, s[22:23]
	v_mov_b32_e32 v146, v218
	s_waitcnt lgkmcnt(0)
	v_mov_b32_e32 v150, v220
	v_mov_b32_e32 v151, v224
	v_mov_b32_e32 v152, v226
	v_mov_b32_e32 v153, v228
	v_mov_b32_e32 v154, v230
	v_mov_b32_e32 v155, v240
	s_nop 0
	v_mov_b32_e32 v149, v250
	v_lshl_or_b32 v160, s1, 8, v191
	v_ashrrev_i32_e32 v161, 31, v160
	v_mov_b64_e32 v[178:179], s[20:21]
	s_mov_b32 s39, 0xe800
	v_mad_i64_i32 v[162:163], s[12:13], v174, s39, v[178:179]
	v_lshlrev_b64 v[180:181], 1, v[160:161]
	v_lshl_add_u64 v[164:165], v[162:163], 0, v[180:181]
	v_add_u32_e32 v147, 0x80, v174
	v_fmamk_f32 v146, v146, 0x39800000, v221
	v_rsq_f32_e32 v182, v146
	v_fmamk_f32 v146, v150, 0x39800000, v221
	v_rsq_f32_e32 v146, v146
	v_fmamk_f32 v149, v149, 0x39800000, v221
	v_pk_mul_f32 v[162:163], v[130:131], v[182:183] op_sel_hi:[1,0]
	v_pk_mul_f32 v[160:161], v[128:129], v[182:183] op_sel_hi:[1,0]
	v_pk_mul_f32 v[166:167], v[126:127], v[182:183] op_sel_hi:[1,0]
	v_pk_mul_f32 v[168:169], v[124:125], v[182:183] op_sel_hi:[1,0]
	v_cvt_pk_bf16_f32 v160, v160, v161
	v_cvt_pk_bf16_f32 v161, v162, v163
	v_cvt_pk_bf16_f32 v162, v168, v169
	v_cvt_pk_bf16_f32 v163, v166, v167
	global_store_dwordx4 v[164:165], v[160:163], off nt
	v_pk_mul_f32 v[166:167], v[118:119], v[182:183] op_sel_hi:[1,0]
	v_pk_mul_f32 v[184:185], v[116:117], v[182:183] op_sel_hi:[1,0]
	v_pk_mul_f32 v[162:163], v[122:123], v[182:183] op_sel_hi:[1,0]
	v_pk_mul_f32 v[160:161], v[120:121], v[182:183] op_sel_hi:[1,0]
	v_rsq_f32_e32 v158, v149
; __device__ __forceinline__ unsigned cvt_pk_bf16(float lo, float hi) { f32x2_t v = {lo, hi}; bf16x2_t b = __builtin_convertvector(v, bf16x2_t); return __builtin_bit_cast(unsigned, b); }
;     template <int ACT, int AUX> __device__ __forceinline__ void run(const f32x4 (&acc)[2][2][4][2], const Unit& uu, int wr, int wc, int fr, int fq) const {
;     ...
;             for (int m = 0; m < 4; ++m) { const int r = row0 + ai * HALF + m * 16; const float rs = rsv[ai * 4 + m];
;                 bf16_t* rowp = O + (size_t)r * cfg::NC + col0; float s1 = 0.f, s2 = 0.f;
; #pragma unroll
;                 for (int bj = 0; bj < 2; ++bj) { f32x4 v0 = acc[ai][bj][m][0] * rs, v1 = acc[ai][bj][m][1] * rs;
; #pragma unroll
;                     for (int j = 0; j < 4; ++j) { v0[j] = act_f<ACT>(v0[j]); v1[j] = act_f<ACT>(v1[j]); }
;                     if (AUX == 4) {
;                         unsigned q[8];
; #pragma unroll
;                         for (int j = 0; j < 4; ++j) { q[j] = (unsigned)fminf(fmaxf(fmaf(v0[j], 255.0f, 0.5f), 1.0f), 255.0f); q[4 + j] = (unsigned)fminf(fmaxf(fmaf(v1[j], 255.0f, 0.5f), 1.0f), 255.0f); }
;                         u32x2 w8; w8.x = q[0] | (q[1] << 8) | (q[2] << 16) | (q[3] << 24); w8.y = q[4] | (q[5] << 8) | (q[6] << 16) | (q[7] << 24);
;                         __builtin_nontemporal_store(w8, (u32x2*)(g8 + ((size_t)((u.pn - 52) >> 4) * cfg::MT + r) * cfg::DM + ((u.pn - 52) & 15) * BM + wc * 32 + 8 * fq + bj * HALF));
;                     } else {
;                     u32x4 w; w.x = cvt_pk_bf16(v0[0], v0[1]); w.y = cvt_pk_bf16(v0[2], v0[3]); w.z = cvt_pk_bf16(v1[0], v1[1]); w.w = cvt_pk_bf16(v1[2], v1[3]);
;                     __builtin_nontemporal_store(w, (u32x4*)(rowp + bj * HALF)); }
;                     if (AUX == 1) {
; #pragma unroll
;                         for (int j = 0; j < 4; ++j) { cs[bj][j] += v0[j]; cs[bj][4 + j] += v1[j]; } }
	v_cvt_pk_bf16_f32 v160, v160, v161
	v_cvt_pk_bf16_f32 v161, v162, v163
	v_cvt_pk_bf16_f32 v162, v184, v185
	v_cvt_pk_bf16_f32 v163, v166, v167
	v_or_b32_e32 v149, 16, v174
	v_fmamk_f32 v148, v151, 0x39800000, v221
	v_pk_fma_f32 v[176:177], v[128:129], v[182:183], 0 op_sel_hi:[1,0,0]
	v_pk_fma_f32 v[170:171], v[124:125], v[182:183], 0 op_sel_hi:[1,0,0]
	v_pk_fma_f32 v[172:173], v[130:131], v[182:183], 0 op_sel_hi:[1,0,0]
	v_pk_fma_f32 v[168:169], v[126:127], v[182:183], 0 op_sel_hi:[1,0,0]
	global_store_dwordx4 v[164:165], v[160:163], off offset:256 nt
	v_pk_fma_f32 v[166:167], v[120:121], v[182:183], 0 op_sel_hi:[1,0,0]
	v_pk_fma_f32 v[164:165], v[122:123], v[182:183], 0 op_sel_hi:[1,0,0]
	v_pk_fma_f32 v[162:163], v[116:117], v[182:183], 0 op_sel_hi:[1,0,0]
	v_pk_fma_f32 v[160:161], v[118:119], v[182:183], 0 op_sel_hi:[1,0,0]
	v_mad_i64_i32 v[182:183], s[12:13], v149, s39, v[178:179]
	v_rsq_f32_e32 v148, v148
	v_lshl_add_u64 v[186:187], v[182:183], 0, v[180:181]
	v_pk_mul_f32 v[184:185], v[114:115], v[146:147] op_sel_hi:[1,0]
	v_pk_mul_f32 v[182:183], v[112:113], v[146:147] op_sel_hi:[1,0]
	v_pk_mul_f32 v[188:189], v[110:111], v[146:147] op_sel_hi:[1,0]
	v_pk_mul_f32 v[194:195], v[108:109], v[146:147] op_sel_hi:[1,0]
	v_cvt_pk_bf16_f32 v182, v182, v183
	v_cvt_pk_bf16_f32 v183, v184, v185
	v_cvt_pk_bf16_f32 v184, v194, v195
	v_cvt_pk_bf16_f32 v185, v188, v189
	global_store_dwordx4 v[186:187], v[182:185], off nt
	v_pk_mul_f32 v[188:189], v[102:103], v[146:147] op_sel_hi:[1,0]
	v_pk_mul_f32 v[194:195], v[100:101], v[146:147] op_sel_hi:[1,0]
	v_pk_mul_f32 v[184:185], v[106:107], v[146:147] op_sel_hi:[1,0]
	v_pk_mul_f32 v[182:183], v[104:105], v[146:147] op_sel_hi:[1,0]
	v_or_b32_e32 v149, 32, v174
	v_cvt_pk_bf16_f32 v182, v182, v183
	v_cvt_pk_bf16_f32 v183, v184, v185
	v_cvt_pk_bf16_f32 v184, v194, v195
	v_cvt_pk_bf16_f32 v185, v188, v189
	v_fmamk_f32 v150, v152, 0x39800000, v221
	global_store_dwordx4 v[186:187], v[182:185], off offset:256 nt
	v_pk_mul_f32 v[186:187], v[98:99], v[148:149] op_sel_hi:[1,0]
	v_pk_mul_f32 v[188:189], v[94:95], v[148:149] op_sel_hi:[1,0]
	v_mad_i64_i32 v[182:183], s[12:13], v149, s39, v[178:179]
	v_pk_mul_f32 v[184:185], v[96:97], v[148:149] op_sel_hi:[1,0]
	v_pk_mul_f32 v[194:195], v[92:93], v[148:149] op_sel_hi:[1,0]
	v_rsq_f32_e32 v150, v150
	v_lshl_add_u64 v[182:183], v[182:183], 0, v[180:181]
	v_cvt_pk_bf16_f32 v184, v184, v185
	v_cvt_pk_bf16_f32 v185, v186, v187
	v_cvt_pk_bf16_f32 v186, v194, v195
	v_cvt_pk_bf16_f32 v187, v188, v189
	v_fmamk_f32 v151, v153, 0x39800000, v221
	global_store_dwordx4 v[182:183], v[184:187], off nt
	v_pk_mul_f32 v[188:189], v[86:87], v[148:149] op_sel_hi:[1,0]
	v_pk_mul_f32 v[194:195], v[84:85], v[148:149] op_sel_hi:[1,0]
	v_pk_mul_f32 v[186:187], v[90:91], v[148:149] op_sel_hi:[1,0]
	v_pk_mul_f32 v[184:185], v[88:89], v[148:149] op_sel_hi:[1,0]
	v_rsq_f32_e32 v152, v151
	v_fmamk_f32 v151, v154, 0x39800000, v221
	v_cvt_pk_bf16_f32 v184, v184, v185
	v_cvt_pk_bf16_f32 v185, v186, v187
	v_cvt_pk_bf16_f32 v186, v194, v195
	v_cvt_pk_bf16_f32 v187, v188, v189
	v_or_b32_e32 v149, 48, v174
	v_rsq_f32_e32 v154, v151
	v_fmamk_f32 v151, v155, 0x39800000, v221
	global_store_dwordx4 v[182:183], v[184:187], off offset:256 nt
	v_mad_i64_i32 v[182:183], s[12:13], v149, s39, v[178:179]
	s_nop 0
	v_lshl_add_u64 v[186:187], v[182:183], 0, v[180:181]
	v_pk_mul_f32 v[184:185], v[82:83], v[150:151] op_sel_hi:[1,0]
	v_pk_mul_f32 v[182:183], v[80:81], v[150:151] op_sel_hi:[1,0]
	v_pk_mul_f32 v[188:189], v[78:79], v[150:151] op_sel_hi:[1,0]
	v_pk_mul_f32 v[194:195], v[76:77], v[150:151] op_sel_hi:[1,0]
	v_cvt_pk_bf16_f32 v182, v182, v183
	v_cvt_pk_bf16_f32 v183, v184, v185
	v_cvt_pk_bf16_f32 v184, v194, v195
	v_cvt_pk_bf16_f32 v185, v188, v189
	global_store_dwordx4 v[186:187], v[182:185], off nt
	v_pk_mul_f32 v[188:189], v[70:71], v[150:151] op_sel_hi:[1,0]
	v_pk_mul_f32 v[194:195], v[68:69], v[150:151] op_sel_hi:[1,0]
	v_pk_mul_f32 v[184:185], v[74:75], v[150:151] op_sel_hi:[1,0]
	v_pk_mul_f32 v[182:183], v[72:73], v[150:151] op_sel_hi:[1,0]
	v_rsq_f32_e32 v156, v151
	v_cvt_pk_bf16_f32 v182, v182, v183
	v_cvt_pk_bf16_f32 v183, v184, v185
	v_cvt_pk_bf16_f32 v184, v194, v195
	v_cvt_pk_bf16_f32 v185, v188, v189
	global_store_dwordx4 v[186:187], v[182:185], off offset:256 nt
	v_pk_mul_f32 v[188:189], v[62:63], v[152:153] op_sel_hi:[1,0]
	v_pk_mul_f32 v[194:195], v[60:61], v[152:153] op_sel_hi:[1,0]
	v_mad_i64_i32 v[182:183], s[12:13], v147, s39, v[178:179]
	v_lshl_add_u64 v[186:187], v[182:183], 0, v[180:181]
	v_pk_mul_f32 v[184:185], v[66:67], v[152:153] op_sel_hi:[1,0]
	v_pk_mul_f32 v[182:183], v[64:65], v[152:153] op_sel_hi:[1,0]
	v_add_u32_e32 v147, 0x90, v174
	v_cvt_pk_bf16_f32 v182, v182, v183
	v_cvt_pk_bf16_f32 v183, v184, v185
	v_cvt_pk_bf16_f32 v184, v194, v195
	v_cvt_pk_bf16_f32 v185, v188, v189
	global_store_dwordx4 v[186:187], v[182:185], off nt
	v_pk_mul_f32 v[188:189], v[54:55], v[152:153] op_sel_hi:[1,0]
	v_pk_mul_f32 v[194:195], v[52:53], v[152:153] op_sel_hi:[1,0]
	v_pk_mul_f32 v[184:185], v[58:59], v[152:153] op_sel_hi:[1,0]
	v_pk_mul_f32 v[182:183], v[56:57], v[152:153] op_sel_hi:[1,0]
	v_and_b32_e32 v149, 64, v229
	v_cvt_pk_bf16_f32 v182, v182, v183
	v_cvt_pk_bf16_f32 v183, v184, v185
	v_cvt_pk_bf16_f32 v184, v194, v195
	v_cvt_pk_bf16_f32 v185, v188, v189
	global_store_dwordx4 v[186:187], v[182:185], off offset:256 nt
	v_pk_mul_f32 v[188:189], v[46:47], v[154:155] op_sel_hi:[1,0]
	v_pk_mul_f32 v[194:195], v[44:45], v[154:155] op_sel_hi:[1,0]
	v_mad_i64_i32 v[182:183], s[12:13], v147, s39, v[178:179]
	v_lshl_add_u64 v[186:187], v[182:183], 0, v[180:181]
;     template <int ACT, int AUX> __device__ __forceinline__ void run(const f32x4 (&acc)[2][2][4][2], const Unit& uu, int wr, int wc, int fr, int fq) const {
;     ...
;             for (int m = 0; m < 4; ++m) { const int r = row0 + ai * HALF + m * 16; const float rs = rsv[ai * 4 + m];
;                 bf16_t* rowp = O + (size_t)r * cfg::NC + col0; float s1 = 0.f, s2 = 0.f;
; #pragma unroll
;                 for (int bj = 0; bj < 2; ++bj) { f32x4 v0 = acc[ai][bj][m][0] * rs, v1 = acc[ai][bj][m][1] * rs;
; #pragma unroll
;                     for (int j = 0; j < 4; ++j) { v0[j] = act_f<ACT>(v0[j]); v1[j] = act_f<ACT>(v1[j]); }
;                     if (AUX == 4) {
;                         unsigned q[8];
; #pragma unroll
;                         for (int j = 0; j < 4; ++j) { q[j] = (unsigned)fminf(fmaxf(fmaf(v0[j], 255.0f, 0.5f), 1.0f), 255.0f); q[4 + j] = (unsigned)fminf(fmaxf(fmaf(v1[j], 255.0f, 0.5f), 1.0f), 255.0f); }
;                         u32x2 w8; w8.x = q[0] | (q[1] << 8) | (q[2] << 16) | (q[3] << 24); w8.y = q[4] | (q[5] << 8) | (q[6] << 16) | (q[7] << 24);
;                         __builtin_nontemporal_store(w8, (u32x2*)(g8 + ((size_t)((u.pn - 52) >> 4) * cfg::MT + r) * cfg::DM + ((u.pn - 52) & 15) * BM + wc * 32 + 8 * fq + bj * HALF));
;                     } else {
;                     u32x4 w; w.x = cvt_pk_bf16(v0[0], v0[1]); w.y = cvt_pk_bf16(v0[2], v0[3]); w.z = cvt_pk_bf16(v1[0], v1[1]); w.w = cvt_pk_bf16(v1[2], v1[3]);
;                     __builtin_nontemporal_store(w, (u32x4*)(rowp + bj * HALF)); }
;                     if (AUX == 1) {
; #pragma unroll
;                         for (int j = 0; j < 4; ++j) { cs[bj][j] += v0[j]; cs[bj][4 + j] += v1[j]; } }
;                     if (AUX == 2) { float p = (v0[0] * v0[0] + v0[1] * v0[1]) + (v0[2] * v0[2] + v0[3] * v0[3]) + (v1[0] * v1[0] + v1[1] * v1[1]) + (v1[2] * v1[2] + v1[3] * v1[3]);
;                         p += __shfl_xor(p, 16); p += __shfl_xor(p, 32); mx[ai][bj] = fmaxf(mx[ai][bj], p); }
;                     if (AUX == 3) { s1 += (v0[0] + v0[1]) + (v0[2] + v0[3]) + (v1[0] + v1[1]) + (v1[2] + v1[3]);
;                         s2 += (v0[0] * v0[0] + v0[1] * v0[1]) + (v0[2] * v0[2] + v0[3] * v0[3]) + (v1[0] * v1[0] + v1[1] * v1[1]) + (v1[2] * v1[2] + v1[3] * v1[3]); } }
	v_pk_mul_f32 v[184:185], v[50:51], v[154:155] op_sel_hi:[1,0]
	v_pk_mul_f32 v[182:183], v[48:49], v[154:155] op_sel_hi:[1,0]
	v_add_u32_e32 v147, 0xa0, v174
	v_cvt_pk_bf16_f32 v182, v182, v183
	v_cvt_pk_bf16_f32 v183, v184, v185
	v_cvt_pk_bf16_f32 v184, v194, v195
	v_cvt_pk_bf16_f32 v185, v188, v189
	global_store_dwordx4 v[186:187], v[182:185], off nt
	v_pk_mul_f32 v[188:189], v[38:39], v[154:155] op_sel_hi:[1,0]
	v_pk_mul_f32 v[194:195], v[36:37], v[154:155] op_sel_hi:[1,0]
	v_pk_mul_f32 v[184:185], v[42:43], v[154:155] op_sel_hi:[1,0]
	v_pk_mul_f32 v[182:183], v[40:41], v[154:155] op_sel_hi:[1,0]
	v_add_u32_e32 v149, 64, v149
	v_cvt_pk_bf16_f32 v182, v182, v183
	v_cvt_pk_bf16_f32 v183, v184, v185
	v_cvt_pk_bf16_f32 v184, v194, v195
	v_cvt_pk_bf16_f32 v185, v188, v189
	global_store_dwordx4 v[186:187], v[182:185], off offset:256 nt
	v_pk_mul_f32 v[188:189], v[30:31], v[156:157] op_sel_hi:[1,0]
	v_pk_mul_f32 v[194:195], v[28:29], v[156:157] op_sel_hi:[1,0]
	v_mad_i64_i32 v[182:183], s[12:13], v147, s39, v[178:179]
	v_add_u32_e32 v147, 0xb0, v174
	v_mad_i64_i32 v[174:175], s[12:13], v147, s39, v[178:179]
	v_xor_b32_e32 v147, 1, v229
	v_cmp_lt_i32_e32 vcc, v147, v149
	v_lshl_add_u64 v[186:187], v[182:183], 0, v[180:181]
	v_pk_mul_f32 v[184:185], v[34:35], v[156:157] op_sel_hi:[1,0]
	v_pk_mul_f32 v[182:183], v[32:33], v[156:157] op_sel_hi:[1,0]
	v_cndmask_b32_e32 v147, v229, v147, vcc
	v_cvt_pk_bf16_f32 v182, v182, v183
	v_cvt_pk_bf16_f32 v183, v184, v185
	v_cvt_pk_bf16_f32 v184, v194, v195
	v_cvt_pk_bf16_f32 v185, v188, v189
	v_lshlrev_b32_e32 v155, 2, v147
	v_xor_b32_e32 v147, 2, v229
	global_store_dwordx4 v[186:187], v[182:185], off nt
	v_pk_mul_f32 v[188:189], v[22:23], v[156:157] op_sel_hi:[1,0]
	v_pk_mul_f32 v[194:195], v[20:21], v[156:157] op_sel_hi:[1,0]
	v_pk_mul_f32 v[184:185], v[26:27], v[156:157] op_sel_hi:[1,0]
	v_pk_mul_f32 v[182:183], v[24:25], v[156:157] op_sel_hi:[1,0]
	v_cmp_lt_i32_e32 vcc, v147, v149
	v_cvt_pk_bf16_f32 v182, v182, v183
	v_cvt_pk_bf16_f32 v183, v184, v185
	v_cvt_pk_bf16_f32 v184, v194, v195
	v_cvt_pk_bf16_f32 v185, v188, v189
	v_cndmask_b32_e32 v147, v229, v147, vcc
	global_store_dwordx4 v[186:187], v[182:185], off offset:256 nt
	v_lshl_add_u64 v[174:175], v[174:175], 0, v[180:181]
	v_pk_mul_f32 v[180:181], v[18:19], v[158:159] op_sel_hi:[1,0]
	v_pk_mul_f32 v[178:179], v[16:17], v[158:159] op_sel_hi:[1,0]
	v_pk_mul_f32 v[182:183], v[14:15], v[158:159] op_sel_hi:[1,0]
	v_pk_mul_f32 v[184:185], v[12:13], v[158:159] op_sel_hi:[1,0]
	v_lshlrev_b32_e32 v151, 2, v147
	v_xor_b32_e32 v147, 4, v229
	v_cvt_pk_bf16_f32 v178, v178, v179
	v_cvt_pk_bf16_f32 v179, v180, v181
	v_cvt_pk_bf16_f32 v180, v184, v185
	v_cvt_pk_bf16_f32 v181, v182, v183
	v_cmp_lt_i32_e32 vcc, v147, v149
	v_xor_b32_e32 v153, 8, v229
	global_store_dwordx4 v[174:175], v[178:181], off nt
	v_pk_mul_f32 v[182:183], v[6:7], v[158:159] op_sel_hi:[1,0]
	v_pk_mul_f32 v[184:185], v[4:5], v[158:159] op_sel_hi:[1,0]
	v_pk_mul_f32 v[180:181], v[10:11], v[158:159] op_sel_hi:[1,0]
	v_pk_mul_f32 v[178:179], v[8:9], v[158:159] op_sel_hi:[1,0]
	v_cndmask_b32_e32 v147, v229, v147, vcc
	v_cmp_lt_i32_e32 vcc, v153, v149
	v_cvt_pk_bf16_f32 v178, v178, v179
	v_cvt_pk_bf16_f32 v179, v180, v181
	v_cvt_pk_bf16_f32 v180, v184, v185
	v_cvt_pk_bf16_f32 v181, v182, v183
	v_lshlrev_b32_e32 v147, 2, v147
	v_cndmask_b32_e32 v149, v229, v153, vcc
	global_store_dwordx4 v[174:175], v[178:181], off offset:256 nt
	v_lshlrev_b32_e32 v149, 2, v149
	v_pk_fma_f32 v[174:175], v[112:113], v[146:147], v[176:177] op_sel_hi:[1,0,1]
	v_pk_fma_f32 v[172:173], v[114:115], v[146:147], v[172:173] op_sel_hi:[1,0,1]
	v_pk_fma_f32 v[170:171], v[108:109], v[146:147], v[170:171] op_sel_hi:[1,0,1]
	v_pk_fma_f32 v[168:169], v[110:111], v[146:147], v[168:169] op_sel_hi:[1,0,1]
	v_pk_fma_f32 v[166:167], v[104:105], v[146:147], v[166:167] op_sel_hi:[1,0,1]
	v_pk_fma_f32 v[164:165], v[106:107], v[146:147], v[164:165] op_sel_hi:[1,0,1]
	v_pk_fma_f32 v[162:163], v[100:101], v[146:147], v[162:163] op_sel_hi:[1,0,1]
	v_pk_fma_f32 v[160:161], v[102:103], v[146:147], v[160:161] op_sel_hi:[1,0,1]
	v_pk_fma_f32 v[174:175], v[96:97], v[148:149], v[174:175] op_sel_hi:[1,0,1]
	v_pk_fma_f32 v[172:173], v[98:99], v[148:149], v[172:173] op_sel_hi:[1,0,1]
	v_pk_fma_f32 v[170:171], v[92:93], v[148:149], v[170:171] op_sel_hi:[1,0,1]
	v_pk_fma_f32 v[168:169], v[94:95], v[148:149], v[168:169] op_sel_hi:[1,0,1]
	v_pk_fma_f32 v[166:167], v[88:89], v[148:149], v[166:167] op_sel_hi:[1,0,1]
	v_pk_fma_f32 v[164:165], v[90:91], v[148:149], v[164:165] op_sel_hi:[1,0,1]
	v_pk_fma_f32 v[162:163], v[84:85], v[148:149], v[162:163] op_sel_hi:[1,0,1]
	v_pk_fma_f32 v[160:161], v[86:87], v[148:149], v[160:161] op_sel_hi:[1,0,1]
	v_pk_fma_f32 v[174:175], v[80:81], v[150:151], v[174:175] op_sel_hi:[1,0,1]
	v_pk_fma_f32 v[172:173], v[82:83], v[150:151], v[172:173] op_sel_hi:[1,0,1]
	v_pk_fma_f32 v[170:171], v[76:77], v[150:151], v[170:171] op_sel_hi:[1,0,1]
	v_pk_fma_f32 v[168:169], v[78:79], v[150:151], v[168:169] op_sel_hi:[1,0,1]
	v_pk_fma_f32 v[166:167], v[72:73], v[150:151], v[166:167] op_sel_hi:[1,0,1]
	v_pk_fma_f32 v[164:165], v[74:75], v[150:151], v[164:165] op_sel_hi:[1,0,1]
	v_pk_fma_f32 v[162:163], v[68:69], v[150:151], v[162:163] op_sel_hi:[1,0,1]
	v_pk_fma_f32 v[160:161], v[70:71], v[150:151], v[160:161] op_sel_hi:[1,0,1]
	v_pk_fma_f32 v[174:175], v[64:65], v[152:153], v[174:175] op_sel_hi:[1,0,1]
	v_pk_fma_f32 v[172:173], v[66:67], v[152:153], v[172:173] op_sel_hi:[1,0,1]
	v_pk_fma_f32 v[170:171], v[60:61], v[152:153], v[170:171] op_sel_hi:[1,0,1]
	v_pk_fma_f32 v[168:169], v[62:63], v[152:153], v[168:169] op_sel_hi:[1,0,1]
;     template <int ACT, int AUX> __device__ __forceinline__ void run(const f32x4 (&acc)[2][2][4][2], const Unit& uu, int wr, int wc, int fr, int fq) const {
;     ...
;                     if (AUX == 1) {
; #pragma unroll
;                         for (int j = 0; j < 4; ++j) { cs[bj][j] += v0[j]; cs[bj][4 + j] += v1[j]; } }
;                     if (AUX == 2) { float p = (v0[0] * v0[0] + v0[1] * v0[1]) + (v0[2] * v0[2] + v0[3] * v0[3]) + (v1[0] * v1[0] + v1[1] * v1[1]) + (v1[2] * v1[2] + v1[3] * v1[3]);
;                         p += __shfl_xor(p, 16); p += __shfl_xor(p, 32); mx[ai][bj] = fmaxf(mx[ai][bj], p); }
;                     if (AUX == 3) { s1 += (v0[0] + v0[1]) + (v0[2] + v0[3]) + (v1[0] + v1[1]) + (v1[2] + v1[3]);
;                         s2 += (v0[0] * v0[0] + v0[1] * v0[1]) + (v0[2] * v0[2] + v0[3] * v0[3]) + (v1[0] * v1[0] + v1[1] * v1[1]) + (v1[2] * v1[2] + v1[3] * v1[3]); } }
;                 if (AUX == 3) { s1 += __shfl_xor(s1, 16); s1 += __shfl_xor(s1, 32); s2 += __shfl_xor(s2, 16); s2 += __shfl_xor(s2, 32);
;                     if (fq == 0) *(float2*)(st2 + ((size_t)r * 16 + (u.pn - 36) * 4 + wc) * 2) = make_float2(s1, s2); } }
;         if (AUX == 1) {
; #pragma unroll
;             for (int i = 0; i < 16; ++i) { float x = cs[i >> 3][i & 7]; x += __shfl_xor(x, 1); x += __shfl_xor(x, 2); x += __shfl_xor(x, 4); x += __shfl_xor(x, 8); cs[i >> 3][i & 7] = x; }
	v_pk_fma_f32 v[166:167], v[56:57], v[152:153], v[166:167] op_sel_hi:[1,0,1]
	v_pk_fma_f32 v[164:165], v[58:59], v[152:153], v[164:165] op_sel_hi:[1,0,1]
	v_pk_fma_f32 v[162:163], v[52:53], v[152:153], v[162:163] op_sel_hi:[1,0,1]
	v_pk_fma_f32 v[152:153], v[54:55], v[152:153], v[160:161] op_sel_hi:[1,0,1]
	v_pk_fma_f32 v[174:175], v[48:49], v[154:155], v[174:175] op_sel_hi:[1,0,1]
	v_pk_fma_f32 v[172:173], v[50:51], v[154:155], v[172:173] op_sel_hi:[1,0,1]
	v_pk_fma_f32 v[170:171], v[44:45], v[154:155], v[170:171] op_sel_hi:[1,0,1]
	v_pk_fma_f32 v[168:169], v[46:47], v[154:155], v[168:169] op_sel_hi:[1,0,1]
	v_pk_fma_f32 v[166:167], v[40:41], v[154:155], v[166:167] op_sel_hi:[1,0,1]
	v_pk_fma_f32 v[164:165], v[42:43], v[154:155], v[164:165] op_sel_hi:[1,0,1]
	v_pk_fma_f32 v[162:163], v[36:37], v[154:155], v[162:163] op_sel_hi:[1,0,1]
	v_pk_fma_f32 v[152:153], v[38:39], v[154:155], v[152:153] op_sel_hi:[1,0,1]
	v_pk_fma_f32 v[174:175], v[32:33], v[156:157], v[174:175] op_sel_hi:[1,0,1]
	v_pk_fma_f32 v[172:173], v[34:35], v[156:157], v[172:173] op_sel_hi:[1,0,1]
	v_pk_fma_f32 v[170:171], v[28:29], v[156:157], v[170:171] op_sel_hi:[1,0,1]
	v_pk_fma_f32 v[168:169], v[30:31], v[156:157], v[168:169] op_sel_hi:[1,0,1]
	v_pk_fma_f32 v[166:167], v[24:25], v[156:157], v[166:167] op_sel_hi:[1,0,1]
	v_pk_fma_f32 v[164:165], v[26:27], v[156:157], v[164:165] op_sel_hi:[1,0,1]
	v_pk_fma_f32 v[162:163], v[20:21], v[156:157], v[162:163] op_sel_hi:[1,0,1]
	v_pk_fma_f32 v[152:153], v[22:23], v[156:157], v[152:153] op_sel_hi:[1,0,1]
	v_pk_fma_f32 v[174:175], v[16:17], v[158:159], v[174:175] op_sel_hi:[1,0,1]
	v_pk_fma_f32 v[172:173], v[18:19], v[158:159], v[172:173] op_sel_hi:[1,0,1]
	v_pk_fma_f32 v[170:171], v[12:13], v[158:159], v[170:171] op_sel_hi:[1,0,1]
	v_pk_fma_f32 v[168:169], v[14:15], v[158:159], v[168:169] op_sel_hi:[1,0,1]
	v_pk_fma_f32 v[166:167], v[8:9], v[158:159], v[166:167] op_sel_hi:[1,0,1]
	v_pk_fma_f32 v[164:165], v[10:11], v[158:159], v[164:165] op_sel_hi:[1,0,1]
	v_pk_fma_f32 v[162:163], v[4:5], v[158:159], v[162:163] op_sel_hi:[1,0,1]
	v_pk_fma_f32 v[152:153], v[6:7], v[158:159], v[152:153] op_sel_hi:[1,0,1]
	ds_bpermute_b32 v176, v155, v174
	ds_bpermute_b32 v177, v155, v175
	ds_bpermute_b32 v178, v155, v172
	ds_bpermute_b32 v179, v155, v173
	ds_bpermute_b32 v180, v155, v170
	ds_bpermute_b32 v181, v155, v171
	ds_bpermute_b32 v182, v155, v168
	ds_bpermute_b32 v183, v155, v169
	ds_bpermute_b32 v184, v155, v166
	ds_bpermute_b32 v185, v155, v167
	ds_bpermute_b32 v186, v155, v164
	ds_bpermute_b32 v187, v155, v165
	ds_bpermute_b32 v188, v155, v162
	ds_bpermute_b32 v189, v155, v163
	ds_bpermute_b32 v154, v155, v152
	ds_bpermute_b32 v155, v155, v153
	s_waitcnt lgkmcnt(14)
	v_pk_add_f32 v[174:175], v[174:175], v[176:177]
	s_waitcnt lgkmcnt(12)
	v_pk_add_f32 v[172:173], v[172:173], v[178:179]
	s_waitcnt lgkmcnt(10)
	v_pk_add_f32 v[170:171], v[170:171], v[180:181]
	s_waitcnt lgkmcnt(8)
	v_pk_add_f32 v[168:169], v[168:169], v[182:183]
	s_waitcnt lgkmcnt(6)
	v_pk_add_f32 v[166:167], v[166:167], v[184:185]
	s_waitcnt lgkmcnt(4)
	v_pk_add_f32 v[164:165], v[164:165], v[186:187]
	s_waitcnt lgkmcnt(2)
	v_pk_add_f32 v[162:163], v[162:163], v[188:189]
	s_waitcnt lgkmcnt(0)
	v_pk_add_f32 v[152:153], v[152:153], v[154:155]
	ds_bpermute_b32 v176, v151, v174
	ds_bpermute_b32 v177, v151, v175
	ds_bpermute_b32 v178, v151, v172
	ds_bpermute_b32 v179, v151, v173
	ds_bpermute_b32 v180, v151, v170
	ds_bpermute_b32 v181, v151, v171
	ds_bpermute_b32 v182, v151, v168
	ds_bpermute_b32 v183, v151, v169
	ds_bpermute_b32 v184, v151, v166
	ds_bpermute_b32 v185, v151, v167
	ds_bpermute_b32 v186, v151, v164
	ds_bpermute_b32 v187, v151, v165
	ds_bpermute_b32 v188, v151, v162
	ds_bpermute_b32 v189, v151, v163
	ds_bpermute_b32 v150, v151, v152
	ds_bpermute_b32 v151, v151, v153
	s_waitcnt lgkmcnt(14)
	v_pk_add_f32 v[174:175], v[174:175], v[176:177]
	s_waitcnt lgkmcnt(12)
	v_pk_add_f32 v[172:173], v[172:173], v[178:179]
	s_waitcnt lgkmcnt(10)
	v_pk_add_f32 v[170:171], v[170:171], v[180:181]
	s_waitcnt lgkmcnt(8)
	v_pk_add_f32 v[168:169], v[168:169], v[182:183]
	s_waitcnt lgkmcnt(6)
	v_pk_add_f32 v[166:167], v[166:167], v[184:185]
	s_waitcnt lgkmcnt(4)
	v_pk_add_f32 v[164:165], v[164:165], v[186:187]
	s_waitcnt lgkmcnt(2)
	v_pk_add_f32 v[162:163], v[162:163], v[188:189]
	s_waitcnt lgkmcnt(0)
	v_pk_add_f32 v[150:151], v[152:153], v[150:151]
	ds_bpermute_b32 v176, v147, v174
	ds_bpermute_b32 v177, v147, v175
	ds_bpermute_b32 v178, v147, v172
	ds_bpermute_b32 v179, v147, v173
	ds_bpermute_b32 v180, v147, v170
	ds_bpermute_b32 v181, v147, v171
	ds_bpermute_b32 v182, v147, v168
	ds_bpermute_b32 v183, v147, v169
	ds_bpermute_b32 v184, v147, v166
	ds_bpermute_b32 v185, v147, v167
	ds_bpermute_b32 v186, v147, v164
	ds_bpermute_b32 v187, v147, v165
	ds_bpermute_b32 v188, v147, v162
	ds_bpermute_b32 v189, v147, v163
	ds_bpermute_b32 v146, v147, v150
	ds_bpermute_b32 v147, v147, v151
	s_waitcnt lgkmcnt(14)
	v_pk_add_f32 v[174:175], v[174:175], v[176:177]
	s_waitcnt lgkmcnt(12)
	v_pk_add_f32 v[172:173], v[172:173], v[178:179]
	s_waitcnt lgkmcnt(10)
	v_pk_add_f32 v[170:171], v[170:171], v[180:181]
	s_waitcnt lgkmcnt(8)
	v_pk_add_f32 v[168:169], v[168:169], v[182:183]
	s_waitcnt lgkmcnt(6)
	v_pk_add_f32 v[166:167], v[166:167], v[184:185]
	s_waitcnt lgkmcnt(4)
	v_pk_add_f32 v[164:165], v[164:165], v[186:187]
	s_waitcnt lgkmcnt(2)
	v_pk_add_f32 v[162:163], v[162:163], v[188:189]
	s_waitcnt lgkmcnt(0)
	v_pk_add_f32 v[146:147], v[150:151], v[146:147]
	ds_bpermute_b32 v176, v149, v174
	ds_bpermute_b32 v177, v149, v175
	ds_bpermute_b32 v178, v149, v172
	ds_bpermute_b32 v179, v149, v173
	ds_bpermute_b32 v180, v149, v170
	ds_bpermute_b32 v181, v149, v171
	ds_bpermute_b32 v182, v149, v168
	ds_bpermute_b32 v183, v149, v169
	ds_bpermute_b32 v184, v149, v166
	ds_bpermute_b32 v185, v149, v167
	ds_bpermute_b32 v186, v149, v164
	ds_bpermute_b32 v187, v149, v165
	ds_bpermute_b32 v188, v149, v162
	ds_bpermute_b32 v189, v149, v163
	ds_bpermute_b32 v148, v149, v146
	ds_bpermute_b32 v149, v149, v147
	s_and_saveexec_b64 s[12:13], s[6:7]
	s_cbranch_execz .LBB0_212
;     template <int ACT, int AUX> __device__ __forceinline__ void run(const f32x4 (&acc)[2][2][4][2], const Unit& uu, int wr, int wc, int fr, int fq) const {
;     ...
;             if (fr == 0) {
; #pragma unroll
;                 for (int bj = 0; bj < 2; ++bj) { float* o = kms + ((size_t)(((u.pm >> 3) * 8 + (u.pn - 4) * 2 + bj) * 8 + (u.pm & 7)) * 2 + wr) * 128 + wc * 32 + 8 * fq;
;                     *(f32x4*)o = (f32x4){cs[bj][0], cs[bj][1], cs[bj][2], cs[bj][3]}; *(f32x4*)(o + 4) = (f32x4){cs[bj][4], cs[bj][5], cs[bj][6], cs[bj][7]}; } }
	s_and_b32 s39, s2, 7
	s_lshl_b32 s41, s1, 4
	s_lshl_b32 s48, s2, 3
	s_andn2_b32 s48, s48, 63
	s_or_b32 s39, s41, s39
	s_add_i32 s39, s39, s48
	s_sub_i32 s48, s39, 64
	s_ashr_i32 s49, s48, 31
	s_lshl_b64 s[48:49], s[48:49], 10
	v_lshl_add_u64 v[154:155], v[140:141], 0, s[48:49]
	s_sub_i32 s48, s39, 56
	s_waitcnt lgkmcnt(12)
	v_pk_add_f32 v[152:153], v[172:173], v[178:179]
	v_pk_add_f32 v[150:151], v[174:175], v[176:177]
	s_ashr_i32 s49, s48, 31
	global_store_dwordx4 v[154:155], v[150:153], off
	s_lshl_b64 s[48:49], s[48:49], 10
	s_waitcnt lgkmcnt(0)
	v_pk_add_f32 v[148:149], v[146:147], v[148:149]
	v_pk_add_f32 v[152:153], v[168:169], v[182:183]
	v_pk_add_f32 v[150:151], v[170:171], v[180:181]
	global_store_dwordx4 v[154:155], v[150:153], off offset:16
	v_lshl_add_u64 v[154:155], v[140:141], 0, s[48:49]
	v_pk_add_f32 v[146:147], v[162:163], v[188:189]
	v_pk_add_f32 v[152:153], v[164:165], v[186:187]
	v_pk_add_f32 v[150:151], v[166:167], v[184:185]
	global_store_dwordx4 v[154:155], v[150:153], off
	global_store_dwordx4 v[154:155], v[146:149], off offset:16

; __device__ __forceinline__ float sigmoid_f(float x) { return __builtin_amdgcn_rcpf(1.0f + __builtin_amdgcn_exp2f(-1.4426950408889634f * x)); }
; template <int ACT> __device__ __forceinline__ float act_f(float v) {
;     template <int ACT, int AUX> __device__ __forceinline__ void run(const f32x4 (&acc)[2][2][4][2], const Unit& uu, int wr, int wc, int fr, int fq) const {
;     ...
;         float rsv[8];
; #pragma unroll
;         for (int i = 0; i < 8; ++i) rsv[i] = ss[row0 + (i >> 2) * HALF + (i & 3) * 16];
;         asm volatile("" ::: "memory");
; #pragma unroll
;         for (int i = 0; i < 8; ++i) rsv[i] = __builtin_amdgcn_rsqf(rsv[i] * (1.0f / cfg::DM) + cfg::RMS_EPS);
;         float cs[2][8]; float mx[2][2];
;         if (AUX == 1) {
; #pragma unroll
;             for (int i = 0; i < 16; ++i) cs[i >> 3][i & 7] = 0.f; }
;         if (AUX == 2) { mx[0][0] = mx[0][1] = mx[1][0] = mx[1][1] = 0.f; }
; #pragma unroll
;         for (int ai = 0; ai < 2; ++ai)
; #pragma unroll
;             for (int m = 0; m < 4; ++m) { const int r = row0 + ai * HALF + m * 16; const float rs = rsv[ai * 4 + m];
;                 bf16_t* rowp = O + (size_t)r * cfg::NC + col0; float s1 = 0.f, s2 = 0.f;
; #pragma unroll
;                 for (int bj = 0; bj < 2; ++bj) { f32x4 v0 = acc[ai][bj][m][0] * rs, v1 = acc[ai][bj][m][1] * rs;
; #pragma unroll
;                     for (int j = 0; j < 4; ++j) { v0[j] = act_f<ACT>(v0[j]); v1[j] = act_f<ACT>(v1[j]); }
;                     if (AUX == 4) {
;                         unsigned q[8];
; #pragma unroll
;                         for (int j = 0; j < 4; ++j) { q[j] = (unsigned)fminf(fmaxf(fmaf(v0[j], 255.0f, 0.5f), 1.0f), 255.0f); q[4 + j] = (unsigned)fminf(fmaxf(fmaf(v1[j], 255.0f, 0.5f), 1.0f), 255.0f); }
;                         u32x2 w8; w8.x = q[0] | (q[1] << 8) | (q[2] << 16) | (q[3] << 24); w8.y = q[4] | (q[5] << 8) | (q[6] << 16) | (q[7] << 24);
;                         __builtin_nontemporal_store(w8, (u32x2*)(g8 + ((size_t)((u.pn - 52) >> 4) * cfg::MT + r) * cfg::DM + ((u.pn - 52) & 15) * BM + wc * 32 + 8 * fq + bj * HALF));
;                     } else {
;                     u32x4 w; w.x = cvt_pk_bf16(v0[0], v0[1]); w.y = cvt_pk_bf16(v0[2], v0[3]); w.z = cvt_pk_bf16(v1[0], v1[1]); w.w = cvt_pk_bf16(v1[2], v1[3]);
;                     __builtin_nontemporal_store(w, (u32x4*)(rowp + bj * HALF)); }
.LBB0_213:
	s_and_b64 vcc, exec, s[46:47]
	s_cbranch_vccz .LBB0_215
	s_waitcnt lgkmcnt(0)
	v_lshl_add_u32 v148, s2, 8, v1
	v_ashrrev_i32_e32 v149, 31, v148
	v_lshl_add_u64 v[150:151], v[148:149], 2, s[22:23]
	v_mov_b32_e32 v146, v218
	v_mov_b32_e32 v149, v220
	v_mov_b32_e32 v152, v224
	v_mov_b32_e32 v153, v226
	v_mov_b32_e32 v154, v228
	v_mov_b32_e32 v155, v230
	v_mov_b32_e32 v157, v240
	s_nop 0
	v_mov_b32_e32 v150, v250
	s_mov_b32 s39, 0xe800
	v_add_u32_e32 v147, 0x80, v148
	v_fmamk_f32 v146, v146, 0x39800000, v221
	v_rsq_f32_e32 v168, v146
	v_fmamk_f32 v146, v149, 0x39800000, v221
	v_rsq_f32_e32 v164, v146
	v_fmamk_f32 v146, v152, 0x39800000, v221
	v_pk_mul_f32 v[172:173], v[128:129], v[168:169] op_sel_hi:[1,0]
	v_pk_mul_f32 v[176:177], v[124:125], v[168:169] op_sel_hi:[1,0]
	v_mul_f32_e32 v149, 0xbfb8aa3b, v172
	v_exp_f32_e32 v149, v149
	v_pk_mul_f32 v[170:171], v[130:131], v[168:169] op_sel_hi:[1,0]
	v_pk_mul_f32 v[174:175], v[126:127], v[168:169] op_sel_hi:[1,0]
	v_rsq_f32_e32 v162, v146
	v_add_f32_e32 v149, 1.0, v149
	v_rcp_f32_e32 v178, v149
	v_mul_f32_e32 v149, 0xbfb8aa3b, v176
	v_exp_f32_e32 v149, v149
	v_fmamk_f32 v146, v153, 0x39800000, v221
	v_rsq_f32_e32 v160, v146
	v_fmamk_f32 v146, v154, 0x39800000, v221
	v_add_f32_e32 v149, 1.0, v149
	v_rcp_f32_e32 v180, v149
	v_mul_f32_e32 v149, 0xbfb8aa3b, v173
	v_exp_f32_e32 v149, v149
	v_rsq_f32_e32 v158, v146
	v_fmamk_f32 v146, v155, 0x39800000, v221
	v_rsq_f32_e32 v156, v146
	v_add_f32_e32 v149, 1.0, v149
	v_rcp_f32_e32 v179, v149
	v_mul_f32_e32 v149, 0xbfb8aa3b, v177
	v_exp_f32_e32 v149, v149
	v_fmamk_f32 v146, v157, 0x39800000, v221
	v_pk_mul_f32 v[172:173], v[172:173], v[178:179]
	v_lshl_or_b32 v152, s1, 8, v191
	v_add_f32_e32 v149, 1.0, v149
	v_rcp_f32_e32 v181, v149
	v_mul_f32_e32 v149, 0xbfb8aa3b, v170
	v_exp_f32_e32 v149, v149
	v_rsq_f32_e32 v154, v146
	v_pk_mul_f32 v[176:177], v[176:177], v[180:181]
	v_fmamk_f32 v146, v150, 0x39800000, v221
	v_add_f32_e32 v149, 1.0, v149
	v_rcp_f32_e32 v178, v149
	v_mul_f32_e32 v149, 0xbfb8aa3b, v174
	v_exp_f32_e32 v149, v149
	v_ashrrev_i32_e32 v153, 31, v152
	v_mov_b64_e32 v[150:151], s[20:21]
	v_mad_i64_i32 v[166:167], s[12:13], v148, s39, v[150:151]
	v_add_f32_e32 v149, 1.0, v149
	v_rcp_f32_e32 v180, v149
	v_mul_f32_e32 v149, 0xbfb8aa3b, v171
	v_exp_f32_e32 v149, v149
	v_lshlrev_b64 v[152:153], 1, v[152:153]
	v_lshl_add_u64 v[166:167], v[166:167], 0, v[152:153]
	v_rsq_f32_e32 v146, v146
	v_add_f32_e32 v149, 1.0, v149
	v_rcp_f32_e32 v179, v149
	v_mul_f32_e32 v149, 0xbfb8aa3b, v175
	v_exp_f32_e32 v149, v149
	v_pk_mul_f32 v[178:179], v[170:171], v[178:179]
	v_cvt_pk_bf16_f32 v170, v172, v173
	v_add_f32_e32 v149, 1.0, v149
	v_rcp_f32_e32 v181, v149
	v_cvt_pk_bf16_f32 v171, v178, v179
	v_cvt_pk_bf16_f32 v172, v176, v177
	v_pk_mul_f32 v[176:177], v[116:117], v[168:169] op_sel_hi:[1,0]
	v_pk_mul_f32 v[174:175], v[174:175], v[180:181]
	s_nop 0
	v_cvt_pk_bf16_f32 v173, v174, v175
	v_pk_mul_f32 v[174:175], v[120:121], v[168:169] op_sel_hi:[1,0]
	global_store_dwordx4 v[166:167], v[170:173], off nt
	v_mul_f32_e32 v149, 0xbfb8aa3b, v174
	v_exp_f32_e32 v149, v149
	v_pk_mul_f32 v[172:173], v[122:123], v[168:169] op_sel_hi:[1,0]
	v_pk_mul_f32 v[170:171], v[118:119], v[168:169] op_sel_hi:[1,0]
	v_add_f32_e32 v149, 1.0, v149
	v_rcp_f32_e32 v168, v149
	v_mul_f32_e32 v149, 0xbfb8aa3b, v176
	v_exp_f32_e32 v149, v149
	s_nop 0
	v_add_f32_e32 v149, 1.0, v149
	v_rcp_f32_e32 v178, v149
	v_mul_f32_e32 v149, 0xbfb8aa3b, v175
	v_exp_f32_e32 v149, v149
	s_nop 0
	v_add_f32_e32 v149, 1.0, v149
	v_rcp_f32_e32 v169, v149
	v_mul_f32_e32 v149, 0xbfb8aa3b, v177
	v_exp_f32_e32 v149, v149
	v_pk_mul_f32 v[168:169], v[174:175], v[168:169]
	s_nop 0
	v_cvt_pk_bf16_f32 v168, v168, v169
	v_add_f32_e32 v149, 1.0, v149
	v_rcp_f32_e32 v179, v149
	v_mul_f32_e32 v149, 0xbfb8aa3b, v172
	v_exp_f32_e32 v149, v149
	v_pk_mul_f32 v[174:175], v[176:177], v[178:179]
	v_add_f32_e32 v149, 1.0, v149
	v_rcp_f32_e32 v176, v149
	v_mul_f32_e32 v149, 0xbfb8aa3b, v170
	v_exp_f32_e32 v149, v149
	s_nop 0
	v_add_f32_e32 v149, 1.0, v149
	v_rcp_f32_e32 v178, v149
	v_mul_f32_e32 v149, 0xbfb8aa3b, v173
	v_exp_f32_e32 v149, v149
	s_nop 0
	v_add_f32_e32 v149, 1.0, v149
	v_rcp_f32_e32 v177, v149
	v_mul_f32_e32 v149, 0xbfb8aa3b, v171
	v_exp_f32_e32 v149, v149
	v_pk_mul_f32 v[172:173], v[172:173], v[176:177]
	s_nop 0
	v_cvt_pk_bf16_f32 v169, v172, v173
	v_add_f32_e32 v149, 1.0, v149
	v_rcp_f32_e32 v179, v149
	v_or_b32_e32 v149, 16, v148
	v_pk_mul_f32 v[172:173], v[110:111], v[164:165] op_sel_hi:[1,0]
	v_pk_mul_f32 v[176:177], v[170:171], v[178:179]
	v_cvt_pk_bf16_f32 v170, v174, v175
	v_cvt_pk_bf16_f32 v171, v176, v177
	global_store_dwordx4 v[166:167], v[168:171], off offset:256 nt
	v_mad_i64_i32 v[166:167], s[12:13], v149, s39, v[150:151]
	s_nop 0
	v_pk_mul_f32 v[170:171], v[112:113], v[164:165] op_sel_hi:[1,0]
	v_pk_mul_f32 v[174:175], v[108:109], v[164:165] op_sel_hi:[1,0]
	v_mul_f32_e32 v149, 0xbfb8aa3b, v170
	v_exp_f32_e32 v149, v149
	v_pk_mul_f32 v[168:169], v[114:115], v[164:165] op_sel_hi:[1,0]
	v_lshl_add_u64 v[166:167], v[166:167], 0, v[152:153]
	v_add_f32_e32 v149, 1.0, v149
	v_rcp_f32_e32 v176, v149
	v_mul_f32_e32 v149, 0xbfb8aa3b, v174
	v_exp_f32_e32 v149, v149
	s_nop 0
	v_add_f32_e32 v149, 1.0, v149
	v_rcp_f32_e32 v178, v149
	v_mul_f32_e32 v149, 0xbfb8aa3b, v171
	v_exp_f32_e32 v149, v149
	s_nop 0
	v_add_f32_e32 v149, 1.0, v149
	v_rcp_f32_e32 v177, v149
	v_mul_f32_e32 v149, 0xbfb8aa3b, v175
	v_exp_f32_e32 v149, v149
	v_pk_mul_f32 v[170:171], v[170:171], v[176:177]
	v_add_f32_e32 v149, 1.0, v149
	v_rcp_f32_e32 v179, v149
	v_mul_f32_e32 v149, 0xbfb8aa3b, v168
	v_exp_f32_e32 v149, v149
; __device__ __forceinline__ unsigned cvt_pk_bf16(float lo, float hi) { f32x2_t v = {lo, hi}; bf16x2_t b = __builtin_convertvector(v, bf16x2_t); return __builtin_bit_cast(unsigned, b); }
; __device__ __forceinline__ float sigmoid_f(float x) { return __builtin_amdgcn_rcpf(1.0f + __builtin_amdgcn_exp2f(-1.4426950408889634f * x)); }
; template <int ACT> __device__ __forceinline__ float act_f(float v) {
;     if (ACT == 1) return v * sigmoid_f(v);
;     template <int ACT, int AUX> __device__ __forceinline__ void run(const f32x4 (&acc)[2][2][4][2], const Unit& uu, int wr, int wc, int fr, int fq) const {
;     ...
;             for (int m = 0; m < 4; ++m) { const int r = row0 + ai * HALF + m * 16; const float rs = rsv[ai * 4 + m];
;                 bf16_t* rowp = O + (size_t)r * cfg::NC + col0; float s1 = 0.f, s2 = 0.f;
; #pragma unroll
;                 for (int bj = 0; bj < 2; ++bj) { f32x4 v0 = acc[ai][bj][m][0] * rs, v1 = acc[ai][bj][m][1] * rs;
; #pragma unroll
;                     for (int j = 0; j < 4; ++j) { v0[j] = act_f<ACT>(v0[j]); v1[j] = act_f<ACT>(v1[j]); }
;                     if (AUX == 4) {
;                         unsigned q[8];
; #pragma unroll
;                         for (int j = 0; j < 4; ++j) { q[j] = (unsigned)fminf(fmaxf(fmaf(v0[j], 255.0f, 0.5f), 1.0f), 255.0f); q[4 + j] = (unsigned)fminf(fmaxf(fmaf(v1[j], 255.0f, 0.5f), 1.0f), 255.0f); }
;                         u32x2 w8; w8.x = q[0] | (q[1] << 8) | (q[2] << 16) | (q[3] << 24); w8.y = q[4] | (q[5] << 8) | (q[6] << 16) | (q[7] << 24);
;                         __builtin_nontemporal_store(w8, (u32x2*)(g8 + ((size_t)((u.pn - 52) >> 4) * cfg::MT + r) * cfg::DM + ((u.pn - 52) & 15) * BM + wc * 32 + 8 * fq + bj * HALF));
;                     } else {
;                     u32x4 w; w.x = cvt_pk_bf16(v0[0], v0[1]); w.y = cvt_pk_bf16(v0[2], v0[3]); w.z = cvt_pk_bf16(v1[0], v1[1]); w.w = cvt_pk_bf16(v1[2], v1[3]);
;                     __builtin_nontemporal_store(w, (u32x4*)(rowp + bj * HALF)); }
	v_pk_mul_f32 v[174:175], v[174:175], v[178:179]
	v_add_f32_e32 v149, 1.0, v149
	v_rcp_f32_e32 v176, v149
	v_mul_f32_e32 v149, 0xbfb8aa3b, v172
	v_exp_f32_e32 v149, v149
	s_nop 0
	v_add_f32_e32 v149, 1.0, v149
	v_rcp_f32_e32 v178, v149
	v_mul_f32_e32 v149, 0xbfb8aa3b, v169
	v_exp_f32_e32 v149, v149
	s_nop 0
	v_add_f32_e32 v149, 1.0, v149
	v_rcp_f32_e32 v177, v149
	v_mul_f32_e32 v149, 0xbfb8aa3b, v173
	v_exp_f32_e32 v149, v149
	v_pk_mul_f32 v[176:177], v[168:169], v[176:177]
	v_cvt_pk_bf16_f32 v168, v170, v171
	v_add_f32_e32 v149, 1.0, v149
	v_rcp_f32_e32 v179, v149
	v_cvt_pk_bf16_f32 v169, v176, v177
	v_cvt_pk_bf16_f32 v170, v174, v175
	v_pk_mul_f32 v[172:173], v[172:173], v[178:179]
	s_nop 0
	v_cvt_pk_bf16_f32 v171, v172, v173
	global_store_dwordx4 v[166:167], v[168:171], off nt
	v_pk_mul_f32 v[172:173], v[102:103], v[164:165] op_sel_hi:[1,0]
	s_nop 0
	v_pk_mul_f32 v[170:171], v[104:105], v[164:165] op_sel_hi:[1,0]
	v_pk_mul_f32 v[168:169], v[106:107], v[164:165] op_sel_hi:[1,0]
	v_mul_f32_e32 v149, 0xbfb8aa3b, v170
	v_exp_f32_e32 v149, v149
	v_pk_mul_f32 v[164:165], v[100:101], v[164:165] op_sel_hi:[1,0]
	v_add_f32_e32 v149, 1.0, v149
	v_rcp_f32_e32 v174, v149
	v_mul_f32_e32 v149, 0xbfb8aa3b, v164
	v_exp_f32_e32 v149, v149
	s_nop 0
	v_add_f32_e32 v149, 1.0, v149
	v_rcp_f32_e32 v176, v149
	v_mul_f32_e32 v149, 0xbfb8aa3b, v171
	v_exp_f32_e32 v149, v149
	s_nop 0
	v_add_f32_e32 v149, 1.0, v149
	v_rcp_f32_e32 v175, v149
	v_mul_f32_e32 v149, 0xbfb8aa3b, v165
	v_exp_f32_e32 v149, v149
	v_pk_mul_f32 v[170:171], v[170:171], v[174:175]
	v_add_f32_e32 v149, 1.0, v149
	v_rcp_f32_e32 v177, v149
	v_mul_f32_e32 v149, 0xbfb8aa3b, v168
	v_exp_f32_e32 v149, v149
	v_pk_mul_f32 v[164:165], v[164:165], v[176:177]
	v_add_f32_e32 v149, 1.0, v149
	v_rcp_f32_e32 v174, v149
	v_mul_f32_e32 v149, 0xbfb8aa3b, v172
	v_exp_f32_e32 v149, v149
	s_nop 0
	v_add_f32_e32 v149, 1.0, v149
	v_rcp_f32_e32 v176, v149
	v_mul_f32_e32 v149, 0xbfb8aa3b, v169
	v_exp_f32_e32 v149, v149
	s_nop 0
	v_add_f32_e32 v149, 1.0, v149
	v_rcp_f32_e32 v175, v149
	v_mul_f32_e32 v149, 0xbfb8aa3b, v173
	v_exp_f32_e32 v149, v149
	v_pk_mul_f32 v[174:175], v[168:169], v[174:175]
	v_cvt_pk_bf16_f32 v168, v170, v171
	v_add_f32_e32 v149, 1.0, v149
	v_rcp_f32_e32 v177, v149
	v_cvt_pk_bf16_f32 v169, v174, v175
	v_cvt_pk_bf16_f32 v170, v164, v165
	v_or_b32_e32 v149, 32, v148
	v_pk_mul_f32 v[172:173], v[172:173], v[176:177]
	v_mad_i64_i32 v[164:165], s[12:13], v149, s39, v[150:151]
	v_cvt_pk_bf16_f32 v171, v172, v173
	global_store_dwordx4 v[166:167], v[168:171], off offset:256 nt
	v_pk_mul_f32 v[172:173], v[92:93], v[162:163] op_sel_hi:[1,0]
	v_pk_mul_f32 v[166:167], v[98:99], v[162:163] op_sel_hi:[1,0]
	v_pk_mul_f32 v[168:169], v[96:97], v[162:163] op_sel_hi:[1,0]
	v_pk_mul_f32 v[170:171], v[94:95], v[162:163] op_sel_hi:[1,0]
	v_mul_f32_e32 v149, 0xbfb8aa3b, v168
	v_exp_f32_e32 v149, v149
	v_lshl_add_u64 v[164:165], v[164:165], 0, v[152:153]
	v_add_f32_e32 v149, 1.0, v149
	v_rcp_f32_e32 v174, v149
	v_mul_f32_e32 v149, 0xbfb8aa3b, v172
	v_exp_f32_e32 v149, v149
	s_nop 0
	v_add_f32_e32 v149, 1.0, v149
	v_rcp_f32_e32 v176, v149
	v_mul_f32_e32 v149, 0xbfb8aa3b, v169
	v_exp_f32_e32 v149, v149
	s_nop 0
	v_add_f32_e32 v149, 1.0, v149
	v_rcp_f32_e32 v175, v149
	v_mul_f32_e32 v149, 0xbfb8aa3b, v173
	v_exp_f32_e32 v149, v149
	v_pk_mul_f32 v[168:169], v[168:169], v[174:175]
	v_add_f32_e32 v149, 1.0, v149
	v_rcp_f32_e32 v177, v149
	v_mul_f32_e32 v149, 0xbfb8aa3b, v166
	v_exp_f32_e32 v149, v149
	v_pk_mul_f32 v[172:173], v[172:173], v[176:177]
	v_add_f32_e32 v149, 1.0, v149
	v_rcp_f32_e32 v174, v149
	v_mul_f32_e32 v149, 0xbfb8aa3b, v170
	v_exp_f32_e32 v149, v149
	s_nop 0
	v_add_f32_e32 v149, 1.0, v149
	v_rcp_f32_e32 v176, v149
	v_mul_f32_e32 v149, 0xbfb8aa3b, v167
	v_exp_f32_e32 v149, v149
	s_nop 0
	v_add_f32_e32 v149, 1.0, v149
	v_rcp_f32_e32 v175, v149
	v_mul_f32_e32 v149, 0xbfb8aa3b, v171
	v_exp_f32_e32 v149, v149
	v_pk_mul_f32 v[174:175], v[166:167], v[174:175]
	v_cvt_pk_bf16_f32 v166, v168, v169
	v_add_f32_e32 v149, 1.0, v149
	v_rcp_f32_e32 v177, v149
	v_cvt_pk_bf16_f32 v167, v174, v175
	v_cvt_pk_bf16_f32 v168, v172, v173
	v_pk_mul_f32 v[170:171], v[170:171], v[176:177]
	s_nop 0
	v_cvt_pk_bf16_f32 v169, v170, v171
	global_store_dwordx4 v[164:165], v[166:169], off nt
	v_pk_mul_f32 v[170:171], v[86:87], v[162:163] op_sel_hi:[1,0]
	s_nop 0
	v_pk_mul_f32 v[168:169], v[88:89], v[162:163] op_sel_hi:[1,0]
	v_pk_mul_f32 v[166:167], v[90:91], v[162:163] op_sel_hi:[1,0]
	v_mul_f32_e32 v149, 0xbfb8aa3b, v168
	v_exp_f32_e32 v149, v149
	v_pk_mul_f32 v[162:163], v[84:85], v[162:163] op_sel_hi:[1,0]
	v_add_f32_e32 v149, 1.0, v149
	v_rcp_f32_e32 v172, v149
	v_mul_f32_e32 v149, 0xbfb8aa3b, v162
	v_exp_f32_e32 v149, v149
	s_nop 0
	v_add_f32_e32 v149, 1.0, v149
	v_rcp_f32_e32 v174, v149
	v_mul_f32_e32 v149, 0xbfb8aa3b, v169
	v_exp_f32_e32 v149, v149
	s_nop 0
	v_add_f32_e32 v149, 1.0, v149
	v_rcp_f32_e32 v173, v149
	v_mul_f32_e32 v149, 0xbfb8aa3b, v163
	v_exp_f32_e32 v149, v149
	v_pk_mul_f32 v[168:169], v[168:169], v[172:173]
	v_add_f32_e32 v149, 1.0, v149
	v_rcp_f32_e32 v175, v149
	v_mul_f32_e32 v149, 0xbfb8aa3b, v166
	v_exp_f32_e32 v149, v149
	v_pk_mul_f32 v[162:163], v[162:163], v[174:175]
	v_add_f32_e32 v149, 1.0, v149
	v_rcp_f32_e32 v172, v149
	v_mul_f32_e32 v149, 0xbfb8aa3b, v170
	v_exp_f32_e32 v149, v149
	s_nop 0
	v_add_f32_e32 v149, 1.0, v149
	v_rcp_f32_e32 v174, v149
	v_mul_f32_e32 v149, 0xbfb8aa3b, v167
	v_exp_f32_e32 v149, v149
	s_nop 0
	v_add_f32_e32 v149, 1.0, v149
	v_rcp_f32_e32 v173, v149
	v_mul_f32_e32 v149, 0xbfb8aa3b, v171
	v_exp_f32_e32 v149, v149
	v_pk_mul_f32 v[172:173], v[166:167], v[172:173]
; __device__ __forceinline__ unsigned cvt_pk_bf16(float lo, float hi) { f32x2_t v = {lo, hi}; bf16x2_t b = __builtin_convertvector(v, bf16x2_t); return __builtin_bit_cast(unsigned, b); }
; __device__ __forceinline__ float sigmoid_f(float x) { return __builtin_amdgcn_rcpf(1.0f + __builtin_amdgcn_exp2f(-1.4426950408889634f * x)); }
; template <int ACT> __device__ __forceinline__ float act_f(float v) {
;     if (ACT == 1) return v * sigmoid_f(v);
;     template <int ACT, int AUX> __device__ __forceinline__ void run(const f32x4 (&acc)[2][2][4][2], const Unit& uu, int wr, int wc, int fr, int fq) const {
;     ...
;             for (int m = 0; m < 4; ++m) { const int r = row0 + ai * HALF + m * 16; const float rs = rsv[ai * 4 + m];
;                 bf16_t* rowp = O + (size_t)r * cfg::NC + col0; float s1 = 0.f, s2 = 0.f;
; #pragma unroll
;                 for (int bj = 0; bj < 2; ++bj) { f32x4 v0 = acc[ai][bj][m][0] * rs, v1 = acc[ai][bj][m][1] * rs;
; #pragma unroll
;                     for (int j = 0; j < 4; ++j) { v0[j] = act_f<ACT>(v0[j]); v1[j] = act_f<ACT>(v1[j]); }
;                     if (AUX == 4) {
;                         unsigned q[8];
; #pragma unroll
;                         for (int j = 0; j < 4; ++j) { q[j] = (unsigned)fminf(fmaxf(fmaf(v0[j], 255.0f, 0.5f), 1.0f), 255.0f); q[4 + j] = (unsigned)fminf(fmaxf(fmaf(v1[j], 255.0f, 0.5f), 1.0f), 255.0f); }
;                         u32x2 w8; w8.x = q[0] | (q[1] << 8) | (q[2] << 16) | (q[3] << 24); w8.y = q[4] | (q[5] << 8) | (q[6] << 16) | (q[7] << 24);
;                         __builtin_nontemporal_store(w8, (u32x2*)(g8 + ((size_t)((u.pn - 52) >> 4) * cfg::MT + r) * cfg::DM + ((u.pn - 52) & 15) * BM + wc * 32 + 8 * fq + bj * HALF));
;                     } else {
;                     u32x4 w; w.x = cvt_pk_bf16(v0[0], v0[1]); w.y = cvt_pk_bf16(v0[2], v0[3]); w.z = cvt_pk_bf16(v1[0], v1[1]); w.w = cvt_pk_bf16(v1[2], v1[3]);
;                     __builtin_nontemporal_store(w, (u32x4*)(rowp + bj * HALF)); }
	v_cvt_pk_bf16_f32 v166, v168, v169
	v_add_f32_e32 v149, 1.0, v149
	v_rcp_f32_e32 v175, v149
	v_cvt_pk_bf16_f32 v167, v172, v173
	v_cvt_pk_bf16_f32 v168, v162, v163
	v_or_b32_e32 v149, 48, v148
	v_pk_mul_f32 v[170:171], v[170:171], v[174:175]
	v_mad_i64_i32 v[162:163], s[12:13], v149, s39, v[150:151]
	v_cvt_pk_bf16_f32 v169, v170, v171
	global_store_dwordx4 v[164:165], v[166:169], off offset:256 nt
	v_pk_mul_f32 v[170:171], v[76:77], v[160:161] op_sel_hi:[1,0]
	v_pk_mul_f32 v[164:165], v[82:83], v[160:161] op_sel_hi:[1,0]
	v_pk_mul_f32 v[166:167], v[80:81], v[160:161] op_sel_hi:[1,0]
	v_pk_mul_f32 v[168:169], v[78:79], v[160:161] op_sel_hi:[1,0]
	v_mul_f32_e32 v149, 0xbfb8aa3b, v166
	v_exp_f32_e32 v149, v149
	v_lshl_add_u64 v[162:163], v[162:163], 0, v[152:153]
	v_add_f32_e32 v149, 1.0, v149
	v_rcp_f32_e32 v172, v149
	v_mul_f32_e32 v149, 0xbfb8aa3b, v170
	v_exp_f32_e32 v149, v149
	s_nop 0
	v_add_f32_e32 v149, 1.0, v149
	v_rcp_f32_e32 v174, v149
	v_mul_f32_e32 v149, 0xbfb8aa3b, v167
	v_exp_f32_e32 v149, v149
	s_nop 0
	v_add_f32_e32 v149, 1.0, v149
	v_rcp_f32_e32 v173, v149
	v_mul_f32_e32 v149, 0xbfb8aa3b, v171
	v_exp_f32_e32 v149, v149
	v_pk_mul_f32 v[166:167], v[166:167], v[172:173]
	v_add_f32_e32 v149, 1.0, v149
	v_rcp_f32_e32 v175, v149
	v_mul_f32_e32 v149, 0xbfb8aa3b, v164
	v_exp_f32_e32 v149, v149
	v_pk_mul_f32 v[170:171], v[170:171], v[174:175]
	v_add_f32_e32 v149, 1.0, v149
	v_rcp_f32_e32 v172, v149
	v_mul_f32_e32 v149, 0xbfb8aa3b, v168
	v_exp_f32_e32 v149, v149
	s_nop 0
	v_add_f32_e32 v149, 1.0, v149
	v_rcp_f32_e32 v174, v149
	v_mul_f32_e32 v149, 0xbfb8aa3b, v165
	v_exp_f32_e32 v149, v149
	s_nop 0
	v_add_f32_e32 v149, 1.0, v149
	v_rcp_f32_e32 v173, v149
	v_mul_f32_e32 v149, 0xbfb8aa3b, v169
	v_exp_f32_e32 v149, v149
	v_pk_mul_f32 v[172:173], v[164:165], v[172:173]
	v_cvt_pk_bf16_f32 v164, v166, v167
	v_add_f32_e32 v149, 1.0, v149
	v_rcp_f32_e32 v175, v149
	v_cvt_pk_bf16_f32 v165, v172, v173
	v_cvt_pk_bf16_f32 v166, v170, v171
	v_pk_mul_f32 v[168:169], v[168:169], v[174:175]
	s_nop 0
	v_cvt_pk_bf16_f32 v167, v168, v169
	global_store_dwordx4 v[162:163], v[164:167], off nt
	v_pk_mul_f32 v[168:169], v[70:71], v[160:161] op_sel_hi:[1,0]
	s_nop 0
	v_pk_mul_f32 v[166:167], v[72:73], v[160:161] op_sel_hi:[1,0]
	v_pk_mul_f32 v[164:165], v[74:75], v[160:161] op_sel_hi:[1,0]
	v_mul_f32_e32 v149, 0xbfb8aa3b, v166
	v_exp_f32_e32 v149, v149
	v_pk_mul_f32 v[160:161], v[68:69], v[160:161] op_sel_hi:[1,0]
	v_add_f32_e32 v149, 1.0, v149
	v_rcp_f32_e32 v170, v149
	v_mul_f32_e32 v149, 0xbfb8aa3b, v160
	v_exp_f32_e32 v149, v149
	s_nop 0
	v_add_f32_e32 v149, 1.0, v149
	v_rcp_f32_e32 v172, v149
	v_mul_f32_e32 v149, 0xbfb8aa3b, v167
	v_exp_f32_e32 v149, v149
	s_nop 0
	v_add_f32_e32 v149, 1.0, v149
	v_rcp_f32_e32 v171, v149
	v_mul_f32_e32 v149, 0xbfb8aa3b, v161
	v_exp_f32_e32 v149, v149
	v_pk_mul_f32 v[166:167], v[166:167], v[170:171]
	v_add_f32_e32 v149, 1.0, v149
	v_rcp_f32_e32 v173, v149
	v_mul_f32_e32 v149, 0xbfb8aa3b, v164
	v_exp_f32_e32 v149, v149
	v_pk_mul_f32 v[160:161], v[160:161], v[172:173]
	v_add_f32_e32 v149, 1.0, v149
	v_rcp_f32_e32 v170, v149
	v_mul_f32_e32 v149, 0xbfb8aa3b, v168
	v_exp_f32_e32 v149, v149
	s_nop 0
	v_add_f32_e32 v149, 1.0, v149
	v_rcp_f32_e32 v172, v149
	v_mul_f32_e32 v149, 0xbfb8aa3b, v165
	v_exp_f32_e32 v149, v149
	s_nop 0
	v_add_f32_e32 v149, 1.0, v149
	v_rcp_f32_e32 v171, v149
	v_mul_f32_e32 v149, 0xbfb8aa3b, v169
	v_exp_f32_e32 v149, v149
	v_pk_mul_f32 v[170:171], v[164:165], v[170:171]
	v_cvt_pk_bf16_f32 v164, v166, v167
	v_add_f32_e32 v149, 1.0, v149
	v_rcp_f32_e32 v173, v149
	v_cvt_pk_bf16_f32 v165, v170, v171
	v_cvt_pk_bf16_f32 v166, v160, v161
	v_mad_i64_i32 v[160:161], s[12:13], v147, s39, v[150:151]
	v_pk_mul_f32 v[168:169], v[168:169], v[172:173]
	v_lshl_add_u64 v[160:161], v[160:161], 0, v[152:153]
	v_cvt_pk_bf16_f32 v167, v168, v169
	global_store_dwordx4 v[162:163], v[164:167], off offset:256 nt
	v_pk_mul_f32 v[168:169], v[60:61], v[158:159] op_sel_hi:[1,0]
	v_pk_mul_f32 v[162:163], v[66:67], v[158:159] op_sel_hi:[1,0]
	v_pk_mul_f32 v[164:165], v[64:65], v[158:159] op_sel_hi:[1,0]
	v_pk_mul_f32 v[166:167], v[62:63], v[158:159] op_sel_hi:[1,0]
	v_mul_f32_e32 v147, 0xbfb8aa3b, v164
	v_exp_f32_e32 v147, v147
	s_nop 0
	v_add_f32_e32 v147, 1.0, v147
	v_rcp_f32_e32 v170, v147
	v_mul_f32_e32 v147, 0xbfb8aa3b, v168
	v_exp_f32_e32 v147, v147
	s_nop 0
	v_add_f32_e32 v147, 1.0, v147
	v_rcp_f32_e32 v172, v147
	v_mul_f32_e32 v147, 0xbfb8aa3b, v165
	v_exp_f32_e32 v147, v147
	s_nop 0
	v_add_f32_e32 v147, 1.0, v147
	v_rcp_f32_e32 v171, v147
	v_mul_f32_e32 v147, 0xbfb8aa3b, v169
	v_exp_f32_e32 v147, v147
	v_pk_mul_f32 v[164:165], v[164:165], v[170:171]
	v_add_f32_e32 v147, 1.0, v147
	v_rcp_f32_e32 v173, v147
	v_mul_f32_e32 v147, 0xbfb8aa3b, v162
	v_exp_f32_e32 v147, v147
	v_pk_mul_f32 v[168:169], v[168:169], v[172:173]
	v_add_f32_e32 v147, 1.0, v147
	v_rcp_f32_e32 v170, v147
	v_mul_f32_e32 v147, 0xbfb8aa3b, v166
	v_exp_f32_e32 v147, v147
	s_nop 0
	v_add_f32_e32 v147, 1.0, v147
	v_rcp_f32_e32 v172, v147
	v_mul_f32_e32 v147, 0xbfb8aa3b, v163
	v_exp_f32_e32 v147, v147
	s_nop 0
	v_add_f32_e32 v147, 1.0, v147
	v_rcp_f32_e32 v171, v147
	v_mul_f32_e32 v147, 0xbfb8aa3b, v167
	v_exp_f32_e32 v147, v147
	v_pk_mul_f32 v[170:171], v[162:163], v[170:171]
	v_cvt_pk_bf16_f32 v162, v164, v165
	v_add_f32_e32 v147, 1.0, v147
	v_rcp_f32_e32 v173, v147
	v_cvt_pk_bf16_f32 v163, v170, v171
	v_cvt_pk_bf16_f32 v164, v168, v169
	v_pk_mul_f32 v[166:167], v[166:167], v[172:173]
	s_nop 0
	v_cvt_pk_bf16_f32 v165, v166, v167
	global_store_dwordx4 v[160:161], v[162:165], off nt
	v_pk_mul_f32 v[166:167], v[54:55], v[158:159] op_sel_hi:[1,0]
	s_nop 0
; __device__ __forceinline__ unsigned cvt_pk_bf16(float lo, float hi) { f32x2_t v = {lo, hi}; bf16x2_t b = __builtin_convertvector(v, bf16x2_t); return __builtin_bit_cast(unsigned, b); }
; __device__ __forceinline__ float sigmoid_f(float x) { return __builtin_amdgcn_rcpf(1.0f + __builtin_amdgcn_exp2f(-1.4426950408889634f * x)); }
; template <int ACT> __device__ __forceinline__ float act_f(float v) {
;     if (ACT == 1) return v * sigmoid_f(v);
;     template <int ACT, int AUX> __device__ __forceinline__ void run(const f32x4 (&acc)[2][2][4][2], const Unit& uu, int wr, int wc, int fr, int fq) const {
;     ...
;             for (int m = 0; m < 4; ++m) { const int r = row0 + ai * HALF + m * 16; const float rs = rsv[ai * 4 + m];
;                 bf16_t* rowp = O + (size_t)r * cfg::NC + col0; float s1 = 0.f, s2 = 0.f;
; #pragma unroll
;                 for (int bj = 0; bj < 2; ++bj) { f32x4 v0 = acc[ai][bj][m][0] * rs, v1 = acc[ai][bj][m][1] * rs;
; #pragma unroll
;                     for (int j = 0; j < 4; ++j) { v0[j] = act_f<ACT>(v0[j]); v1[j] = act_f<ACT>(v1[j]); }
;                     if (AUX == 4) {
;                         unsigned q[8];
; #pragma unroll
;                         for (int j = 0; j < 4; ++j) { q[j] = (unsigned)fminf(fmaxf(fmaf(v0[j], 255.0f, 0.5f), 1.0f), 255.0f); q[4 + j] = (unsigned)fminf(fmaxf(fmaf(v1[j], 255.0f, 0.5f), 1.0f), 255.0f); }
;                         u32x2 w8; w8.x = q[0] | (q[1] << 8) | (q[2] << 16) | (q[3] << 24); w8.y = q[4] | (q[5] << 8) | (q[6] << 16) | (q[7] << 24);
;                         __builtin_nontemporal_store(w8, (u32x2*)(g8 + ((size_t)((u.pn - 52) >> 4) * cfg::MT + r) * cfg::DM + ((u.pn - 52) & 15) * BM + wc * 32 + 8 * fq + bj * HALF));
;                     } else {
;                     u32x4 w; w.x = cvt_pk_bf16(v0[0], v0[1]); w.y = cvt_pk_bf16(v0[2], v0[3]); w.z = cvt_pk_bf16(v1[0], v1[1]); w.w = cvt_pk_bf16(v1[2], v1[3]);
;                     __builtin_nontemporal_store(w, (u32x4*)(rowp + bj * HALF)); }
	v_pk_mul_f32 v[164:165], v[56:57], v[158:159] op_sel_hi:[1,0]
	v_pk_mul_f32 v[162:163], v[58:59], v[158:159] op_sel_hi:[1,0]
	v_mul_f32_e32 v147, 0xbfb8aa3b, v164
	v_exp_f32_e32 v147, v147
	v_pk_mul_f32 v[158:159], v[52:53], v[158:159] op_sel_hi:[1,0]
	v_add_f32_e32 v147, 1.0, v147
	v_rcp_f32_e32 v168, v147
	v_mul_f32_e32 v147, 0xbfb8aa3b, v158
	v_exp_f32_e32 v147, v147
	s_nop 0
	v_add_f32_e32 v147, 1.0, v147
	v_rcp_f32_e32 v170, v147
	v_mul_f32_e32 v147, 0xbfb8aa3b, v165
	v_exp_f32_e32 v147, v147
	s_nop 0
	v_add_f32_e32 v147, 1.0, v147
	v_rcp_f32_e32 v169, v147
	v_mul_f32_e32 v147, 0xbfb8aa3b, v159
	v_exp_f32_e32 v147, v147
	v_pk_mul_f32 v[164:165], v[164:165], v[168:169]
	v_add_f32_e32 v147, 1.0, v147
	v_rcp_f32_e32 v171, v147
	v_mul_f32_e32 v147, 0xbfb8aa3b, v162
	v_exp_f32_e32 v147, v147
	v_pk_mul_f32 v[158:159], v[158:159], v[170:171]
	v_add_f32_e32 v147, 1.0, v147
	v_rcp_f32_e32 v168, v147
	v_mul_f32_e32 v147, 0xbfb8aa3b, v166
	v_exp_f32_e32 v147, v147
	s_nop 0
	v_add_f32_e32 v147, 1.0, v147
	v_rcp_f32_e32 v170, v147
	v_mul_f32_e32 v147, 0xbfb8aa3b, v163
	v_exp_f32_e32 v147, v147
	s_nop 0
	v_add_f32_e32 v147, 1.0, v147
	v_rcp_f32_e32 v169, v147
	v_mul_f32_e32 v147, 0xbfb8aa3b, v167
	v_exp_f32_e32 v147, v147
	v_pk_mul_f32 v[168:169], v[162:163], v[168:169]
	v_cvt_pk_bf16_f32 v162, v164, v165
	v_add_f32_e32 v147, 1.0, v147
	v_rcp_f32_e32 v171, v147
	v_cvt_pk_bf16_f32 v163, v168, v169
	v_cvt_pk_bf16_f32 v164, v158, v159
	v_add_u32_e32 v147, 0x90, v148
	v_pk_mul_f32 v[166:167], v[166:167], v[170:171]
	v_mad_i64_i32 v[158:159], s[12:13], v147, s39, v[150:151]
	v_cvt_pk_bf16_f32 v165, v166, v167
	global_store_dwordx4 v[160:161], v[162:165], off offset:256 nt
	v_pk_mul_f32 v[166:167], v[44:45], v[156:157] op_sel_hi:[1,0]
	v_pk_mul_f32 v[160:161], v[50:51], v[156:157] op_sel_hi:[1,0]
	v_pk_mul_f32 v[162:163], v[48:49], v[156:157] op_sel_hi:[1,0]
	v_pk_mul_f32 v[164:165], v[46:47], v[156:157] op_sel_hi:[1,0]
	v_mul_f32_e32 v147, 0xbfb8aa3b, v162
	v_exp_f32_e32 v147, v147
	v_lshl_add_u64 v[158:159], v[158:159], 0, v[152:153]
	v_add_f32_e32 v147, 1.0, v147
	v_rcp_f32_e32 v168, v147
	v_mul_f32_e32 v147, 0xbfb8aa3b, v166
	v_exp_f32_e32 v147, v147
	s_nop 0
	v_add_f32_e32 v147, 1.0, v147
	v_rcp_f32_e32 v170, v147
	v_mul_f32_e32 v147, 0xbfb8aa3b, v163
	v_exp_f32_e32 v147, v147
	s_nop 0
	v_add_f32_e32 v147, 1.0, v147
	v_rcp_f32_e32 v169, v147
	v_mul_f32_e32 v147, 0xbfb8aa3b, v167
	v_exp_f32_e32 v147, v147
	v_pk_mul_f32 v[162:163], v[162:163], v[168:169]
	v_add_f32_e32 v147, 1.0, v147
	v_rcp_f32_e32 v171, v147
	v_mul_f32_e32 v147, 0xbfb8aa3b, v160
	v_exp_f32_e32 v147, v147
	v_pk_mul_f32 v[166:167], v[166:167], v[170:171]
	v_add_f32_e32 v147, 1.0, v147
	v_rcp_f32_e32 v168, v147
	v_mul_f32_e32 v147, 0xbfb8aa3b, v164
	v_exp_f32_e32 v147, v147
	s_nop 0
	v_add_f32_e32 v147, 1.0, v147
	v_rcp_f32_e32 v170, v147
	v_mul_f32_e32 v147, 0xbfb8aa3b, v161
	v_exp_f32_e32 v147, v147
	s_nop 0
	v_add_f32_e32 v147, 1.0, v147
	v_rcp_f32_e32 v169, v147
	v_mul_f32_e32 v147, 0xbfb8aa3b, v165
	v_exp_f32_e32 v147, v147
	v_pk_mul_f32 v[168:169], v[160:161], v[168:169]
	v_cvt_pk_bf16_f32 v160, v162, v163
	v_add_f32_e32 v147, 1.0, v147
	v_rcp_f32_e32 v171, v147
	v_cvt_pk_bf16_f32 v161, v168, v169
	v_cvt_pk_bf16_f32 v162, v166, v167
	v_pk_mul_f32 v[164:165], v[164:165], v[170:171]
	s_nop 0
	v_cvt_pk_bf16_f32 v163, v164, v165
	global_store_dwordx4 v[158:159], v[160:163], off nt
	v_pk_mul_f32 v[164:165], v[38:39], v[156:157] op_sel_hi:[1,0]
	s_nop 0
	v_pk_mul_f32 v[162:163], v[40:41], v[156:157] op_sel_hi:[1,0]
	v_pk_mul_f32 v[160:161], v[42:43], v[156:157] op_sel_hi:[1,0]
	v_mul_f32_e32 v147, 0xbfb8aa3b, v162
	v_exp_f32_e32 v147, v147
	v_pk_mul_f32 v[156:157], v[36:37], v[156:157] op_sel_hi:[1,0]
	v_add_f32_e32 v147, 1.0, v147
	v_rcp_f32_e32 v166, v147
	v_mul_f32_e32 v147, 0xbfb8aa3b, v156
	v_exp_f32_e32 v147, v147
	s_nop 0
	v_add_f32_e32 v147, 1.0, v147
	v_rcp_f32_e32 v168, v147
	v_mul_f32_e32 v147, 0xbfb8aa3b, v163
	v_exp_f32_e32 v147, v147
	s_nop 0
	v_add_f32_e32 v147, 1.0, v147
	v_rcp_f32_e32 v167, v147
	v_mul_f32_e32 v147, 0xbfb8aa3b, v157
	v_exp_f32_e32 v147, v147
	v_pk_mul_f32 v[162:163], v[162:163], v[166:167]
	v_add_f32_e32 v147, 1.0, v147
	v_rcp_f32_e32 v169, v147
	v_mul_f32_e32 v147, 0xbfb8aa3b, v160
	v_exp_f32_e32 v147, v147
	v_pk_mul_f32 v[156:157], v[156:157], v[168:169]
	v_add_f32_e32 v147, 1.0, v147
	v_rcp_f32_e32 v166, v147
	v_mul_f32_e32 v147, 0xbfb8aa3b, v164
	v_exp_f32_e32 v147, v147
	s_nop 0
	v_add_f32_e32 v147, 1.0, v147
	v_rcp_f32_e32 v168, v147
	v_mul_f32_e32 v147, 0xbfb8aa3b, v161
	v_exp_f32_e32 v147, v147
	s_nop 0
	v_add_f32_e32 v147, 1.0, v147
	v_rcp_f32_e32 v167, v147
	v_mul_f32_e32 v147, 0xbfb8aa3b, v165
	v_exp_f32_e32 v147, v147
	v_pk_mul_f32 v[166:167], v[160:161], v[166:167]
	v_cvt_pk_bf16_f32 v160, v162, v163
	v_add_f32_e32 v147, 1.0, v147
	v_rcp_f32_e32 v169, v147
	v_cvt_pk_bf16_f32 v161, v166, v167
	v_cvt_pk_bf16_f32 v162, v156, v157
	v_add_u32_e32 v147, 0xa0, v148
	v_pk_mul_f32 v[164:165], v[164:165], v[168:169]
	v_mad_i64_i32 v[156:157], s[12:13], v147, s39, v[150:151]
	v_cvt_pk_bf16_f32 v163, v164, v165
	global_store_dwordx4 v[158:159], v[160:163], off offset:256 nt
	v_pk_mul_f32 v[164:165], v[28:29], v[154:155] op_sel_hi:[1,0]
	v_pk_mul_f32 v[158:159], v[34:35], v[154:155] op_sel_hi:[1,0]
	v_pk_mul_f32 v[160:161], v[32:33], v[154:155] op_sel_hi:[1,0]
	v_pk_mul_f32 v[162:163], v[30:31], v[154:155] op_sel_hi:[1,0]
	v_mul_f32_e32 v147, 0xbfb8aa3b, v160
	v_exp_f32_e32 v147, v147
	v_lshl_add_u64 v[156:157], v[156:157], 0, v[152:153]
	v_add_f32_e32 v147, 1.0, v147
	v_rcp_f32_e32 v166, v147
	v_mul_f32_e32 v147, 0xbfb8aa3b, v164
	v_exp_f32_e32 v147, v147
; __device__ __forceinline__ unsigned cvt_pk_bf16(float lo, float hi) { f32x2_t v = {lo, hi}; bf16x2_t b = __builtin_convertvector(v, bf16x2_t); return __builtin_bit_cast(unsigned, b); }
; __device__ __forceinline__ float sigmoid_f(float x) { return __builtin_amdgcn_rcpf(1.0f + __builtin_amdgcn_exp2f(-1.4426950408889634f * x)); }
; template <int ACT> __device__ __forceinline__ float act_f(float v) {
;     if (ACT == 1) return v * sigmoid_f(v);
;     template <int ACT, int AUX> __device__ __forceinline__ void run(const f32x4 (&acc)[2][2][4][2], const Unit& uu, int wr, int wc, int fr, int fq) const {
;     ...
;             for (int m = 0; m < 4; ++m) { const int r = row0 + ai * HALF + m * 16; const float rs = rsv[ai * 4 + m];
;                 bf16_t* rowp = O + (size_t)r * cfg::NC + col0; float s1 = 0.f, s2 = 0.f;
; #pragma unroll
;                 for (int bj = 0; bj < 2; ++bj) { f32x4 v0 = acc[ai][bj][m][0] * rs, v1 = acc[ai][bj][m][1] * rs;
; #pragma unroll
;                     for (int j = 0; j < 4; ++j) { v0[j] = act_f<ACT>(v0[j]); v1[j] = act_f<ACT>(v1[j]); }
;                     if (AUX == 4) {
;                         unsigned q[8];
; #pragma unroll
;                         for (int j = 0; j < 4; ++j) { q[j] = (unsigned)fminf(fmaxf(fmaf(v0[j], 255.0f, 0.5f), 1.0f), 255.0f); q[4 + j] = (unsigned)fminf(fmaxf(fmaf(v1[j], 255.0f, 0.5f), 1.0f), 255.0f); }
;                         u32x2 w8; w8.x = q[0] | (q[1] << 8) | (q[2] << 16) | (q[3] << 24); w8.y = q[4] | (q[5] << 8) | (q[6] << 16) | (q[7] << 24);
;                         __builtin_nontemporal_store(w8, (u32x2*)(g8 + ((size_t)((u.pn - 52) >> 4) * cfg::MT + r) * cfg::DM + ((u.pn - 52) & 15) * BM + wc * 32 + 8 * fq + bj * HALF));
;                     } else {
;                     u32x4 w; w.x = cvt_pk_bf16(v0[0], v0[1]); w.y = cvt_pk_bf16(v0[2], v0[3]); w.z = cvt_pk_bf16(v1[0], v1[1]); w.w = cvt_pk_bf16(v1[2], v1[3]);
;                     __builtin_nontemporal_store(w, (u32x4*)(rowp + bj * HALF)); }
	s_nop 0
	v_add_f32_e32 v147, 1.0, v147
	v_rcp_f32_e32 v168, v147
	v_mul_f32_e32 v147, 0xbfb8aa3b, v161
	v_exp_f32_e32 v147, v147
	s_nop 0
	v_add_f32_e32 v147, 1.0, v147
	v_rcp_f32_e32 v167, v147
	v_mul_f32_e32 v147, 0xbfb8aa3b, v165
	v_exp_f32_e32 v147, v147
	v_pk_mul_f32 v[160:161], v[160:161], v[166:167]
	v_add_f32_e32 v147, 1.0, v147
	v_rcp_f32_e32 v169, v147
	v_mul_f32_e32 v147, 0xbfb8aa3b, v158
	v_exp_f32_e32 v147, v147
	v_pk_mul_f32 v[164:165], v[164:165], v[168:169]
	v_add_f32_e32 v147, 1.0, v147
	v_rcp_f32_e32 v166, v147
	v_mul_f32_e32 v147, 0xbfb8aa3b, v162
	v_exp_f32_e32 v147, v147
	s_nop 0
	v_add_f32_e32 v147, 1.0, v147
	v_rcp_f32_e32 v168, v147
	v_mul_f32_e32 v147, 0xbfb8aa3b, v159
	v_exp_f32_e32 v147, v147
	s_nop 0
	v_add_f32_e32 v147, 1.0, v147
	v_rcp_f32_e32 v167, v147
	v_mul_f32_e32 v147, 0xbfb8aa3b, v163
	v_exp_f32_e32 v147, v147
	v_pk_mul_f32 v[166:167], v[158:159], v[166:167]
	v_cvt_pk_bf16_f32 v158, v160, v161
	v_add_f32_e32 v147, 1.0, v147
	v_rcp_f32_e32 v169, v147
	v_cvt_pk_bf16_f32 v159, v166, v167
	v_cvt_pk_bf16_f32 v160, v164, v165
	v_pk_mul_f32 v[162:163], v[162:163], v[168:169]
	s_nop 0
	v_cvt_pk_bf16_f32 v161, v162, v163
	global_store_dwordx4 v[156:157], v[158:161], off nt
	v_pk_mul_f32 v[162:163], v[22:23], v[154:155] op_sel_hi:[1,0]
	s_nop 0
	v_pk_mul_f32 v[160:161], v[24:25], v[154:155] op_sel_hi:[1,0]
	v_pk_mul_f32 v[158:159], v[26:27], v[154:155] op_sel_hi:[1,0]
	v_mul_f32_e32 v147, 0xbfb8aa3b, v160
	v_exp_f32_e32 v147, v147
	v_pk_mul_f32 v[154:155], v[20:21], v[154:155] op_sel_hi:[1,0]
	v_add_f32_e32 v147, 1.0, v147
	v_rcp_f32_e32 v164, v147
	v_mul_f32_e32 v147, 0xbfb8aa3b, v154
	v_exp_f32_e32 v147, v147
	s_nop 0
	v_add_f32_e32 v147, 1.0, v147
	v_rcp_f32_e32 v166, v147
	v_mul_f32_e32 v147, 0xbfb8aa3b, v161
	v_exp_f32_e32 v147, v147
	s_nop 0
	v_add_f32_e32 v147, 1.0, v147
	v_rcp_f32_e32 v165, v147
	v_mul_f32_e32 v147, 0xbfb8aa3b, v155
	v_exp_f32_e32 v147, v147
	v_pk_mul_f32 v[160:161], v[160:161], v[164:165]
	v_add_f32_e32 v147, 1.0, v147
	v_rcp_f32_e32 v167, v147
	v_mul_f32_e32 v147, 0xbfb8aa3b, v158
	v_exp_f32_e32 v147, v147
	v_pk_mul_f32 v[154:155], v[154:155], v[166:167]
	v_add_f32_e32 v147, 1.0, v147
	v_rcp_f32_e32 v164, v147
	v_mul_f32_e32 v147, 0xbfb8aa3b, v162
	v_exp_f32_e32 v147, v147
	s_nop 0
	v_add_f32_e32 v147, 1.0, v147
	v_rcp_f32_e32 v166, v147
	v_mul_f32_e32 v147, 0xbfb8aa3b, v159
	v_exp_f32_e32 v147, v147
	s_nop 0
	v_add_f32_e32 v147, 1.0, v147
	v_rcp_f32_e32 v165, v147
	v_mul_f32_e32 v147, 0xbfb8aa3b, v163
	v_exp_f32_e32 v147, v147
	v_pk_mul_f32 v[164:165], v[158:159], v[164:165]
	v_cvt_pk_bf16_f32 v158, v160, v161
	v_add_f32_e32 v147, 1.0, v147
	v_rcp_f32_e32 v167, v147
	v_add_u32_e32 v147, 0xb0, v148
	v_mad_i64_i32 v[148:149], s[12:13], v147, s39, v[150:151]
	v_pk_mul_f32 v[162:163], v[162:163], v[166:167]
	v_cvt_pk_bf16_f32 v159, v164, v165
	v_cvt_pk_bf16_f32 v160, v154, v155
	v_cvt_pk_bf16_f32 v161, v162, v163
	v_lshl_add_u64 v[148:149], v[148:149], 0, v[152:153]
	v_pk_mul_f32 v[152:153], v[16:17], v[146:147] op_sel_hi:[1,0]
	global_store_dwordx4 v[156:157], v[158:161], off offset:256 nt
	v_pk_mul_f32 v[150:151], v[18:19], v[146:147] op_sel_hi:[1,0]
	v_pk_mul_f32 v[154:155], v[14:15], v[146:147] op_sel_hi:[1,0]
	v_pk_mul_f32 v[156:157], v[12:13], v[146:147] op_sel_hi:[1,0]
	v_mul_f32_e32 v147, 0xbfb8aa3b, v152
	v_exp_f32_e32 v147, v147
	s_nop 0
	v_add_f32_e32 v147, 1.0, v147
	v_rcp_f32_e32 v158, v147
	v_mul_f32_e32 v147, 0xbfb8aa3b, v156
	v_exp_f32_e32 v147, v147
	s_nop 0
	v_add_f32_e32 v147, 1.0, v147
	v_rcp_f32_e32 v160, v147
	v_mul_f32_e32 v147, 0xbfb8aa3b, v153
	v_exp_f32_e32 v147, v147
	s_nop 0
	v_add_f32_e32 v147, 1.0, v147
	v_rcp_f32_e32 v159, v147
	v_mul_f32_e32 v147, 0xbfb8aa3b, v157
	v_exp_f32_e32 v147, v147
	v_pk_mul_f32 v[152:153], v[152:153], v[158:159]
	v_add_f32_e32 v147, 1.0, v147
	v_rcp_f32_e32 v161, v147
	v_mul_f32_e32 v147, 0xbfb8aa3b, v150
	v_exp_f32_e32 v147, v147
	v_pk_mul_f32 v[156:157], v[156:157], v[160:161]
	v_add_f32_e32 v147, 1.0, v147
	v_rcp_f32_e32 v158, v147
	v_mul_f32_e32 v147, 0xbfb8aa3b, v154
	v_exp_f32_e32 v147, v147
	s_nop 0
	v_add_f32_e32 v147, 1.0, v147
	v_rcp_f32_e32 v160, v147
	v_mul_f32_e32 v147, 0xbfb8aa3b, v151
	v_exp_f32_e32 v147, v147
	s_nop 0
	v_add_f32_e32 v147, 1.0, v147
	v_rcp_f32_e32 v159, v147
	v_mul_f32_e32 v147, 0xbfb8aa3b, v155
	v_exp_f32_e32 v147, v147
	v_pk_mul_f32 v[158:159], v[150:151], v[158:159]
	v_cvt_pk_bf16_f32 v150, v152, v153
	v_add_f32_e32 v147, 1.0, v147
	v_rcp_f32_e32 v161, v147
	v_cvt_pk_bf16_f32 v151, v158, v159
	v_cvt_pk_bf16_f32 v152, v156, v157
	v_pk_mul_f32 v[154:155], v[154:155], v[160:161]
	s_nop 0
	v_cvt_pk_bf16_f32 v153, v154, v155
	global_store_dwordx4 v[148:149], v[150:153], off nt
	v_pk_mul_f32 v[154:155], v[6:7], v[146:147] op_sel_hi:[1,0]
	s_nop 0
	v_pk_mul_f32 v[150:151], v[10:11], v[146:147] op_sel_hi:[1,0]
	v_pk_mul_f32 v[152:153], v[8:9], v[146:147] op_sel_hi:[1,0]
	v_pk_mul_f32 v[146:147], v[4:5], v[146:147] op_sel_hi:[1,0]
	v_mul_f32_e32 v156, 0xbfb8aa3b, v152
	v_mul_f32_e32 v157, 0xbfb8aa3b, v146
	v_exp_f32_e32 v157, v157
	v_exp_f32_e32 v156, v156
	v_add_f32_e32 v157, 1.0, v157
	v_rcp_f32_e32 v158, v157
	v_mul_f32_e32 v157, 0xbfb8aa3b, v153
	v_exp_f32_e32 v157, v157
	v_add_f32_e32 v156, 1.0, v156
	v_rcp_f32_e32 v156, v156
	v_add_f32_e32 v157, 1.0, v157
	v_rcp_f32_e32 v157, v157
	s_nop 0
	v_pk_mul_f32 v[152:153], v[152:153], v[156:157]
	v_mul_f32_e32 v156, 0xbfb8aa3b, v147
	v_exp_f32_e32 v156, v156
	v_mul_f32_e32 v157, 0xbfb8aa3b, v154
	v_exp_f32_e32 v157, v157
	v_add_f32_e32 v156, 1.0, v156
	v_rcp_f32_e32 v159, v156
	v_add_f32_e32 v157, 1.0, v157
	v_mul_f32_e32 v156, 0xbfb8aa3b, v150
	v_exp_f32_e32 v156, v156
	v_pk_mul_f32 v[146:147], v[146:147], v[158:159]
	v_rcp_f32_e32 v158, v157
	v_mul_f32_e32 v157, 0xbfb8aa3b, v151
	v_exp_f32_e32 v157, v157
	v_add_f32_e32 v156, 1.0, v156
	v_rcp_f32_e32 v156, v156
	v_add_f32_e32 v157, 1.0, v157
	v_rcp_f32_e32 v157, v157
	s_nop 0
	v_pk_mul_f32 v[156:157], v[150:151], v[156:157]
	v_mul_f32_e32 v150, 0xbfb8aa3b, v155
	v_exp_f32_e32 v150, v150
	v_cvt_pk_bf16_f32 v151, v156, v157
	v_add_f32_e32 v150, 1.0, v150
	v_rcp_f32_e32 v159, v150
	v_cvt_pk_bf16_f32 v150, v152, v153
	v_cvt_pk_bf16_f32 v152, v146, v147
	v_pk_mul_f32 v[154:155], v[154:155], v[158:159]
	s_nop 0
	v_cvt_pk_bf16_f32 v153, v154, v155
	global_store_dwordx4 v[148:149], v[150:153], off offset:256 nt
